# all s_setprio flips around the GEMM MFMA blocks removed
# speedup vs baseline: 1.0031x; 1.0016x over previous
; #define PG8_STAGE(bufoff, gbase, voff) do { _Pragma("unroll") for (int _i = 0; _i < 2; ++_i) \
;         __builtin_amdgcn_global_load_lds((const unsigned*)((const char*)(gbase) + (voff)[_i]), (PG8_LAS unsigned*)(lds + (bufoff) + ldsw + _i * 8192), 16, 0, 0); } while (0)
; #define PG8_LDA(dst, b, h) do { _Pragma("unroll") for (int m = 0; m < 4; ++m) _Pragma("unroll") for (int k = 0; k < 2; ++k) dst[m][k] = *(const PG8_LAS bf16x8*)(lds + PG8_SA(b, h) + aoff + m * 2048 + k * 1024); } while (0)
; #define PG8_LDB(dst, b, h) do { _Pragma("unroll") for (int n = 0; n < 2; ++n) _Pragma("unroll") for (int k = 0; k < 2; ++k) dst[n][k] = *(const PG8_LAS bf16x8*)(lds + PG8_SB(b, h) + boff + n * 2048 + k * 1024); } while (0)
; #define PG8_WAIT_V8_UNLESS_FIRST(t) asm volatile("s_cmp_eq_u32 %0, 0\n\ts_cbranch_scc1 .Lpg8skip%=\n\ts_waitcnt vmcnt(8)\n.Lpg8skip%=:" :: "s"(t) : "scc", "memory")
; #define PG8_WAIT_L(n) asm volatile("s_waitcnt lgkmcnt(" #n ")" ::: "memory")
; #define PG8_BAR __builtin_amdgcn_s_barrier()
; #define PG8_SCHED __builtin_amdgcn_sched_barrier(0)
; template <class Epi, class Sched, bool ALIGN_EPI = false, bool SP2 = false, bool FP8 = false, bool ABLK = false>
; __device__ __forceinline__ void gemm_phase(PG8_LAS unsigned char* lds, const Gemm g, const Sched& S, const Epi& E) {
;     ...
;             if constexpr (SP2) {
;             PG8_LDB(B0, 0, 0); PG8_LDB(B1, 0, 1); PG8_SCHED; PG8_LDA(At, 0, 0); PG8_STAGE(PG8_SA(1, 1), a1 + hstepA, voffA);
;             PG8_WAIT_V8_UNLESS_FIRST(t); PG8_WAIT_L(0); PG8_BAR; PG8_MMA(0, 0, At, B0); PG8_MMA(0, 1, At, B1); PG8_BAR; PG8_SCHED;
;             PG8_LDA(At, 0, 1); PG8_STAGE(PG8_SB(0, 0), b2, voffB); PG8_STAGE(PG8_SB(0, 1), b2 + hstep, voffB); PG8_STAGE(PG8_SA(0, 0), a2, voffA);
;             PG8_WAIT_V8_UNLESS_FIRST(t); PG8_WAIT_L(0); PG8_BAR; PG8_MMA(1, 0, At, B0); PG8_MMA(1, 1, At, B1); PG8_BAR; PG8_SCHED;
.Lpg8skip0:
	s_waitcnt lgkmcnt(0)
	s_barrier
	s_waitcnt lgkmcnt(0)
	v_mfma_f32_16x16x32_bf16 v[128:131], v[132:135], v[180:183], v[128:131]
	v_mfma_f32_16x16x32_bf16 v[124:127], v[140:143], v[180:183], v[124:127]
	v_mfma_f32_16x16x32_bf16 v[112:115], v[132:135], v[188:191], v[112:115]
	v_mfma_f32_16x16x32_bf16 v[108:111], v[140:143], v[188:191], v[108:111]
	v_mfma_f32_16x16x32_bf16 v[96:99], v[132:135], v[208:211], v[96:99]
	v_mfma_f32_16x16x32_bf16 v[92:95], v[140:143], v[208:211], v[92:95]
	v_mfma_f32_16x16x32_bf16 v[80:83], v[132:135], v[216:219], v[80:83]
	v_mfma_f32_16x16x32_bf16 v[76:79], v[140:143], v[216:219], v[76:79]
	v_mfma_f32_16x16x32_bf16 v[128:131], v[136:139], v[184:187], v[128:131]
	v_mfma_f32_16x16x32_bf16 v[124:127], v[144:147], v[184:187], v[124:127]
	v_mfma_f32_16x16x32_bf16 v[112:115], v[136:139], v[192:195], v[112:115]
	v_mfma_f32_16x16x32_bf16 v[108:111], v[144:147], v[192:195], v[108:111]
	v_mfma_f32_16x16x32_bf16 v[96:99], v[136:139], v[212:215], v[96:99]
	v_mfma_f32_16x16x32_bf16 v[92:95], v[144:147], v[212:215], v[92:95]
	v_mfma_f32_16x16x32_bf16 v[80:83], v[136:139], v[220:223], v[80:83]
	v_mfma_f32_16x16x32_bf16 v[76:79], v[144:147], v[220:223], v[76:79]
	v_mfma_f32_16x16x32_bf16 v[120:123], v[148:151], v[180:183], v[120:123]
	v_mfma_f32_16x16x32_bf16 v[116:119], v[172:175], v[180:183], v[116:119]
	v_mfma_f32_16x16x32_bf16 v[104:107], v[148:151], v[188:191], v[104:107]
	v_mfma_f32_16x16x32_bf16 v[100:103], v[172:175], v[188:191], v[100:103]
	v_mfma_f32_16x16x32_bf16 v[88:91], v[148:151], v[208:211], v[88:91]
	v_mfma_f32_16x16x32_bf16 v[84:87], v[172:175], v[208:211], v[84:87]
	v_mfma_f32_16x16x32_bf16 v[72:75], v[148:151], v[216:219], v[72:75]
	v_mfma_f32_16x16x32_bf16 v[68:71], v[172:175], v[216:219], v[68:71]
	v_mfma_f32_16x16x32_bf16 v[120:123], v[168:171], v[184:187], v[120:123]
	v_mfma_f32_16x16x32_bf16 v[116:119], v[176:179], v[184:187], v[116:119]
	v_mfma_f32_16x16x32_bf16 v[104:107], v[168:171], v[192:195], v[104:107]
	v_mfma_f32_16x16x32_bf16 v[100:103], v[176:179], v[192:195], v[100:103]
	v_mfma_f32_16x16x32_bf16 v[88:91], v[168:171], v[212:215], v[88:91]
	v_mfma_f32_16x16x32_bf16 v[84:87], v[176:179], v[212:215], v[84:87]
	v_mfma_f32_16x16x32_bf16 v[72:75], v[168:171], v[220:223], v[72:75]
	v_mfma_f32_16x16x32_bf16 v[68:71], v[176:179], v[220:223], v[68:71]
	s_barrier
	s_add_i32 s75, s75, s17
	v_lshl_add_u64 v[162:163], s[62:63], 0, v[2:3]
	s_mov_b32 m0, s75
	ds_read_b128 v[180:183], v166 offset:16384
	ds_read_b128 v[184:187], v166 offset:17408
	ds_read_b128 v[188:191], v166 offset:18432
	ds_read_b128 v[192:195], v166 offset:19456
	ds_read_b128 v[208:211], v166 offset:20480
	ds_read_b128 v[212:215], v166 offset:21504
	ds_read_b128 v[216:219], v166 offset:22528
	ds_read_b128 v[220:223], v166 offset:23552
	global_load_lds_dwordx4 v[162:163], off
	s_add_i32 m0, s75, 0x2000
	s_add_u32 s76, s62, 0x40000
	v_lshl_add_u64 v[224:225], s[62:63], 0, v[152:153]
	s_addc_u32 s77, s63, 0
	s_add_i32 s75, s81, s17
	global_load_lds_dwordx4 v[224:225], off
	v_lshl_add_u64 v[228:229], s[76:77], 0, v[2:3]
	s_mov_b32 m0, s75
	v_lshl_add_u64 v[230:231], s[64:65], 0, v[154:155]
	global_load_lds_dwordx4 v[228:229], off
	v_lshl_add_u64 v[228:229], s[76:77], 0, v[152:153]
	s_add_i32 m0, s75, 0x2000
	s_nop 0
	global_load_lds_dwordx4 v[228:229], off
	v_lshl_add_u64 v[228:229], s[64:65], 0, v[156:157]
	s_mov_b32 m0, s18
	s_nop 0
	global_load_lds_dwordx4 v[228:229], off
	s_mov_b32 m0, s19
	s_nop 0
	global_load_lds_dwordx4 v[230:231], off
	s_cmp_eq_u32 s74, 0
	s_cbranch_scc1 .Lpg8skip1
	s_waitcnt vmcnt(8)
.Lpg8skip1:
	s_waitcnt lgkmcnt(0)
	s_barrier
	s_waitcnt lgkmcnt(0)
	v_mfma_f32_16x16x32_bf16 v[64:67], v[132:135], v[180:183], v[64:67]
	v_mfma_f32_16x16x32_bf16 v[60:63], v[140:143], v[180:183], v[60:63]
	v_mfma_f32_16x16x32_bf16 v[48:51], v[132:135], v[188:191], v[48:51]
	v_mfma_f32_16x16x32_bf16 v[44:47], v[140:143], v[188:191], v[44:47]
	v_mfma_f32_16x16x32_bf16 v[32:35], v[132:135], v[208:211], v[32:35]
	v_mfma_f32_16x16x32_bf16 v[28:31], v[140:143], v[208:211], v[28:31]
	v_mfma_f32_16x16x32_bf16 v[16:19], v[132:135], v[216:219], v[16:19]
	v_mfma_f32_16x16x32_bf16 v[12:15], v[140:143], v[216:219], v[12:15]
	v_mfma_f32_16x16x32_bf16 v[64:67], v[136:139], v[184:187], v[64:67]
	v_mfma_f32_16x16x32_bf16 v[60:63], v[144:147], v[184:187], v[60:63]
	v_mfma_f32_16x16x32_bf16 v[48:51], v[136:139], v[192:195], v[48:51]
	v_mfma_f32_16x16x32_bf16 v[44:47], v[144:147], v[192:195], v[44:47]
	v_mfma_f32_16x16x32_bf16 v[32:35], v[136:139], v[212:215], v[32:35]
	v_mfma_f32_16x16x32_bf16 v[28:31], v[144:147], v[212:215], v[28:31]
	v_mfma_f32_16x16x32_bf16 v[16:19], v[136:139], v[220:223], v[16:19]
	v_mfma_f32_16x16x32_bf16 v[12:15], v[144:147], v[220:223], v[12:15]
	v_mfma_f32_16x16x32_bf16 v[56:59], v[148:151], v[180:183], v[56:59]
	v_mfma_f32_16x16x32_bf16 v[52:55], v[172:175], v[180:183], v[52:55]
	v_mfma_f32_16x16x32_bf16 v[40:43], v[148:151], v[188:191], v[40:43]
	v_mfma_f32_16x16x32_bf16 v[36:39], v[172:175], v[188:191], v[36:39]
	v_mfma_f32_16x16x32_bf16 v[24:27], v[148:151], v[208:211], v[24:27]
	v_mfma_f32_16x16x32_bf16 v[20:23], v[172:175], v[208:211], v[20:23]
	v_mfma_f32_16x16x32_bf16 v[8:11], v[148:151], v[216:219], v[8:11]
	v_mfma_f32_16x16x32_bf16 v[4:7], v[172:175], v[216:219], v[4:7]
	v_mfma_f32_16x16x32_bf16 v[56:59], v[168:171], v[184:187], v[56:59]
	v_mfma_f32_16x16x32_bf16 v[52:55], v[176:179], v[184:187], v[52:55]
	v_mfma_f32_16x16x32_bf16 v[40:43], v[168:171], v[192:195], v[40:43]
	v_mfma_f32_16x16x32_bf16 v[36:39], v[176:179], v[192:195], v[36:39]
	v_mfma_f32_16x16x32_bf16 v[24:27], v[168:171], v[212:215], v[24:27]
	v_mfma_f32_16x16x32_bf16 v[20:23], v[176:179], v[212:215], v[20:23]
	v_mfma_f32_16x16x32_bf16 v[8:11], v[168:171], v[220:223], v[8:11]
	v_mfma_f32_16x16x32_bf16 v[4:7], v[176:179], v[220:223], v[4:7]
	s_barrier
; #define PG8_STAGE(bufoff, gbase, voff) do { _Pragma("unroll") for (int _i = 0; _i < 2; ++_i) \
;         __builtin_amdgcn_global_load_lds((const unsigned*)((const char*)(gbase) + (voff)[_i]), (PG8_LAS unsigned*)(lds + (bufoff) + ldsw + _i * 8192), 16, 0, 0); } while (0)
; #define PG8_LDA(dst, b, h) do { _Pragma("unroll") for (int m = 0; m < 4; ++m) _Pragma("unroll") for (int k = 0; k < 2; ++k) dst[m][k] = *(const PG8_LAS bf16x8*)(lds + PG8_SA(b, h) + aoff + m * 2048 + k * 1024); } while (0)
; #define PG8_LDB(dst, b, h) do { _Pragma("unroll") for (int n = 0; n < 2; ++n) _Pragma("unroll") for (int k = 0; k < 2; ++k) dst[n][k] = *(const PG8_LAS bf16x8*)(lds + PG8_SB(b, h) + boff + n * 2048 + k * 1024); } while (0)
; #define PG8_WAIT_V(n) asm volatile("s_waitcnt vmcnt(" #n ")" ::: "memory")
; #define PG8_WAIT_L(n) asm volatile("s_waitcnt lgkmcnt(" #n ")" ::: "memory")
; #define PG8_BAR __builtin_amdgcn_s_barrier()
; #define PG8_SCHED __builtin_amdgcn_sched_barrier(0)
; template <class Epi, class Sched, bool ALIGN_EPI = false, bool SP2 = false, bool FP8 = false, bool ABLK = false>
; __device__ __forceinline__ void gemm_phase(PG8_LAS unsigned char* lds, const Gemm g, const Sched& S, const Epi& E) {
;     ...
;             PG8_LDB(B0, 1, 0); PG8_LDB(B1, 1, 1); PG8_SCHED; PG8_LDA(At, 1, 0); PG8_STAGE(PG8_SA(0, 1), a2 + hstepA, voffA);
;             PG8_WAIT_V(8); PG8_WAIT_L(0); PG8_BAR; PG8_MMA(0, 0, At, B0); PG8_MMA(0, 1, At, B1); PG8_BAR; PG8_SCHED;
	s_add_i32 s75, 0, 0x18000
	s_add_i32 s76, 0, 0x1c000
	v_add_u32_e32 v144, s75, v165
	v_add_u32_e32 v167, s76, v165
	ds_read_b128 v[132:135], v144
	ds_read_b128 v[136:139], v144 offset:1024
	ds_read_b128 v[140:143], v144 offset:2048
	ds_read_b128 v[144:147], v144 offset:3072
	ds_read_b128 v[148:151], v167
	ds_read_b128 v[168:171], v167 offset:1024
	ds_read_b128 v[172:175], v167 offset:2048
	ds_read_b128 v[176:179], v167 offset:3072
	s_add_u32 s64, s64, 0x40000
	s_addc_u32 s65, s65, 0
	s_mov_b32 m0, s20
	v_lshl_add_u64 v[232:233], s[64:65], 0, v[156:157]
	ds_read_b128 v[180:183], v166 offset:32768
	ds_read_b128 v[184:187], v166 offset:33792
	ds_read_b128 v[188:191], v166 offset:34816
	ds_read_b128 v[192:195], v166 offset:35840
	ds_read_b128 v[208:211], v166 offset:36864
	ds_read_b128 v[212:215], v166 offset:37888
	ds_read_b128 v[216:219], v166 offset:38912
	ds_read_b128 v[220:223], v166 offset:39936
	global_load_lds_dwordx4 v[232:233], off
	v_lshl_add_u64 v[232:233], s[64:65], 0, v[154:155]
	s_mov_b32 m0, s21
	s_nop 0
	global_load_lds_dwordx4 v[232:233], off
	s_waitcnt vmcnt(8)
	s_waitcnt lgkmcnt(0)
	s_barrier
	s_waitcnt lgkmcnt(0)
	v_mfma_f32_16x16x32_bf16 v[128:131], v[132:135], v[180:183], v[128:131]
	v_mfma_f32_16x16x32_bf16 v[124:127], v[140:143], v[180:183], v[124:127]
	v_mfma_f32_16x16x32_bf16 v[112:115], v[132:135], v[188:191], v[112:115]
	v_mfma_f32_16x16x32_bf16 v[108:111], v[140:143], v[188:191], v[108:111]
	v_mfma_f32_16x16x32_bf16 v[96:99], v[132:135], v[208:211], v[96:99]
	v_mfma_f32_16x16x32_bf16 v[92:95], v[140:143], v[208:211], v[92:95]
	v_mfma_f32_16x16x32_bf16 v[80:83], v[132:135], v[216:219], v[80:83]
	v_mfma_f32_16x16x32_bf16 v[76:79], v[140:143], v[216:219], v[76:79]
	v_mfma_f32_16x16x32_bf16 v[128:131], v[136:139], v[184:187], v[128:131]
	v_mfma_f32_16x16x32_bf16 v[124:127], v[144:147], v[184:187], v[124:127]
	v_mfma_f32_16x16x32_bf16 v[112:115], v[136:139], v[192:195], v[112:115]
	v_mfma_f32_16x16x32_bf16 v[108:111], v[144:147], v[192:195], v[108:111]
	v_mfma_f32_16x16x32_bf16 v[96:99], v[136:139], v[212:215], v[96:99]
	v_mfma_f32_16x16x32_bf16 v[92:95], v[144:147], v[212:215], v[92:95]
	v_mfma_f32_16x16x32_bf16 v[80:83], v[136:139], v[220:223], v[80:83]
	v_mfma_f32_16x16x32_bf16 v[76:79], v[144:147], v[220:223], v[76:79]
	v_mfma_f32_16x16x32_bf16 v[120:123], v[148:151], v[180:183], v[120:123]
	v_mfma_f32_16x16x32_bf16 v[116:119], v[172:175], v[180:183], v[116:119]
	v_mfma_f32_16x16x32_bf16 v[104:107], v[148:151], v[188:191], v[104:107]
	v_mfma_f32_16x16x32_bf16 v[100:103], v[172:175], v[188:191], v[100:103]
	v_mfma_f32_16x16x32_bf16 v[88:91], v[148:151], v[208:211], v[88:91]
	v_mfma_f32_16x16x32_bf16 v[84:87], v[172:175], v[208:211], v[84:87]
	v_mfma_f32_16x16x32_bf16 v[72:75], v[148:151], v[216:219], v[72:75]
	v_mfma_f32_16x16x32_bf16 v[68:71], v[172:175], v[216:219], v[68:71]
	v_mfma_f32_16x16x32_bf16 v[120:123], v[168:171], v[184:187], v[120:123]
	v_mfma_f32_16x16x32_bf16 v[116:119], v[176:179], v[184:187], v[116:119]
	v_mfma_f32_16x16x32_bf16 v[104:107], v[168:171], v[192:195], v[104:107]
	v_mfma_f32_16x16x32_bf16 v[100:103], v[176:179], v[192:195], v[100:103]
	v_mfma_f32_16x16x32_bf16 v[88:91], v[168:171], v[212:215], v[88:91]
	v_mfma_f32_16x16x32_bf16 v[84:87], v[176:179], v[212:215], v[84:87]
	v_mfma_f32_16x16x32_bf16 v[72:75], v[168:171], v[220:223], v[72:75]
	v_mfma_f32_16x16x32_bf16 v[68:71], v[176:179], v[220:223], v[68:71]
	s_barrier
; #define PG8_STAGE(bufoff, gbase, voff) do { _Pragma("unroll") for (int _i = 0; _i < 2; ++_i) \
;         __builtin_amdgcn_global_load_lds((const unsigned*)((const char*)(gbase) + (voff)[_i]), (PG8_LAS unsigned*)(lds + (bufoff) + ldsw + _i * 8192), 16, 0, 0); } while (0)
; #define PG8_LDA(dst, b, h) do { _Pragma("unroll") for (int m = 0; m < 4; ++m) _Pragma("unroll") for (int k = 0; k < 2; ++k) dst[m][k] = *(const PG8_LAS bf16x8*)(lds + PG8_SA(b, h) + aoff + m * 2048 + k * 1024); } while (0)
; #define PG8_WAIT_V(n) asm volatile("s_waitcnt vmcnt(" #n ")" ::: "memory")
; #define PG8_WAIT_L(n) asm volatile("s_waitcnt lgkmcnt(" #n ")" ::: "memory")
; #define PG8_BAR __builtin_amdgcn_s_barrier()
; #define PG8_SCHED __builtin_amdgcn_sched_barrier(0)
; template <class Epi, class Sched, bool ALIGN_EPI = false, bool SP2 = false, bool FP8 = false, bool ABLK = false>
; __device__ __forceinline__ void gemm_phase(PG8_LAS unsigned char* lds, const Gemm g, const Sched& S, const Epi& E) {
;     ...
;             PG8_LDA(At, 1, 1); PG8_STAGE(PG8_SB(1, 0), b3, voffB); PG8_STAGE(PG8_SB(1, 1), b3 + hstep, voffB); PG8_STAGE(PG8_SA(1, 0), a3, voffA);
;             PG8_WAIT_V(8); PG8_WAIT_L(0); PG8_BAR; PG8_MMA(1, 0, At, B0); PG8_MMA(1, 1, At, B1); PG8_BAR; PG8_SCHED;
;     ...
;         if constexpr (SP2) PG8_WAIT_V(0);
;         if constexpr (FP8) asm volatile("s_nop 15\n\ts_nop 15" ::: "memory");
;         if constexpr (ALIGN_EPI) { if (wr == 0) PG8_BAR; }
	s_add_i32 s64, s75, s17
	v_lshl_add_u64 v[162:163], v[162:163], 0, s[34:35]
	s_mov_b32 m0, s64
	ds_read_b128 v[180:183], v166 offset:49152
	ds_read_b128 v[184:187], v166 offset:50176
	ds_read_b128 v[188:191], v166 offset:51200
	ds_read_b128 v[192:195], v166 offset:52224
	ds_read_b128 v[208:211], v166 offset:53248
	ds_read_b128 v[212:215], v166 offset:54272
	ds_read_b128 v[216:219], v166 offset:55296
	ds_read_b128 v[220:223], v166 offset:56320
	global_load_lds_dwordx4 v[162:163], off
	s_add_i32 m0, s64, 0x2000
	s_add_u32 s62, s62, 0x40080
	v_lshl_add_u64 v[162:163], v[224:225], 0, s[34:35]
	s_addc_u32 s63, s63, 0
	s_add_i32 s64, s76, s17
	global_load_lds_dwordx4 v[162:163], off
	v_lshl_add_u64 v[162:163], s[62:63], 0, v[2:3]
	s_mov_b32 m0, s64
	s_nop 0
	global_load_lds_dwordx4 v[162:163], off
	v_lshl_add_u64 v[162:163], s[62:63], 0, v[152:153]
	s_add_i32 m0, s64, 0x2000
	s_nop 0
	global_load_lds_dwordx4 v[162:163], off
	v_lshl_add_u64 v[162:163], v[228:229], 0, s[34:35]
	s_mov_b32 m0, s66
	s_nop 0
	global_load_lds_dwordx4 v[162:163], off
	v_lshl_add_u64 v[162:163], v[230:231], 0, s[34:35]
	s_mov_b32 m0, s67
	s_nop 0
	global_load_lds_dwordx4 v[162:163], off
	s_waitcnt vmcnt(8)
	s_waitcnt lgkmcnt(0)
	s_barrier
	s_waitcnt lgkmcnt(0)
	v_mfma_f32_16x16x32_bf16 v[64:67], v[132:135], v[180:183], v[64:67]
	v_mfma_f32_16x16x32_bf16 v[60:63], v[140:143], v[180:183], v[60:63]
	v_mfma_f32_16x16x32_bf16 v[48:51], v[132:135], v[188:191], v[48:51]
	v_mfma_f32_16x16x32_bf16 v[44:47], v[140:143], v[188:191], v[44:47]
	v_mfma_f32_16x16x32_bf16 v[32:35], v[132:135], v[208:211], v[32:35]
	v_mfma_f32_16x16x32_bf16 v[28:31], v[140:143], v[208:211], v[28:31]
	v_mfma_f32_16x16x32_bf16 v[16:19], v[132:135], v[216:219], v[16:19]
	v_mfma_f32_16x16x32_bf16 v[12:15], v[140:143], v[216:219], v[12:15]
	v_mfma_f32_16x16x32_bf16 v[64:67], v[136:139], v[184:187], v[64:67]
	v_mfma_f32_16x16x32_bf16 v[60:63], v[144:147], v[184:187], v[60:63]
	v_mfma_f32_16x16x32_bf16 v[48:51], v[136:139], v[192:195], v[48:51]
	v_mfma_f32_16x16x32_bf16 v[44:47], v[144:147], v[192:195], v[44:47]
	v_mfma_f32_16x16x32_bf16 v[32:35], v[136:139], v[212:215], v[32:35]
	v_mfma_f32_16x16x32_bf16 v[28:31], v[144:147], v[212:215], v[28:31]
	v_mfma_f32_16x16x32_bf16 v[16:19], v[136:139], v[220:223], v[16:19]
	v_mfma_f32_16x16x32_bf16 v[12:15], v[144:147], v[220:223], v[12:15]
	v_mfma_f32_16x16x32_bf16 v[56:59], v[148:151], v[180:183], v[56:59]
	v_mfma_f32_16x16x32_bf16 v[52:55], v[172:175], v[180:183], v[52:55]
	v_mfma_f32_16x16x32_bf16 v[40:43], v[148:151], v[188:191], v[40:43]
	v_mfma_f32_16x16x32_bf16 v[36:39], v[172:175], v[188:191], v[36:39]
	v_mfma_f32_16x16x32_bf16 v[24:27], v[148:151], v[208:211], v[24:27]
	v_mfma_f32_16x16x32_bf16 v[20:23], v[172:175], v[208:211], v[20:23]
	v_mfma_f32_16x16x32_bf16 v[8:11], v[148:151], v[216:219], v[8:11]
	v_mfma_f32_16x16x32_bf16 v[4:7], v[172:175], v[216:219], v[4:7]
	v_mfma_f32_16x16x32_bf16 v[56:59], v[168:171], v[184:187], v[56:59]
	v_mfma_f32_16x16x32_bf16 v[52:55], v[176:179], v[184:187], v[52:55]
	v_mfma_f32_16x16x32_bf16 v[40:43], v[168:171], v[192:195], v[40:43]
	v_mfma_f32_16x16x32_bf16 v[36:39], v[176:179], v[192:195], v[36:39]
	v_mfma_f32_16x16x32_bf16 v[24:27], v[168:171], v[212:215], v[24:27]
	v_mfma_f32_16x16x32_bf16 v[20:23], v[176:179], v[212:215], v[20:23]
	v_mfma_f32_16x16x32_bf16 v[8:11], v[168:171], v[220:223], v[8:11]
	v_mfma_f32_16x16x32_bf16 v[4:7], v[176:179], v[220:223], v[4:7]
	s_barrier
	s_add_u32 s60, s60, 0x100
	s_addc_u32 s61, s61, 0
	s_add_u32 s72, s72, 0x100
	s_addc_u32 s73, s73, 0
	s_cmp_gt_u32 s74, 13
	s_mov_b32 s62, s74
	s_cbranch_scc0 .LBB0_431
	s_waitcnt vmcnt(0)
	s_and_b64 vcc, exec, s[50:51]
	s_cbranch_vccz .LBB0_434
	s_barrier

; #define PG8_STAGE(bufoff, gbase, voff) do { _Pragma("unroll") for (int _i = 0; _i < 2; ++_i) \
;         __builtin_amdgcn_global_load_lds((const unsigned*)((const char*)(gbase) + (voff)[_i]), (PG8_LAS unsigned*)(lds + (bufoff) + ldsw + _i * 8192), 16, 0, 0); } while (0)
; #define PG8_LDA(dst, b, h) do { _Pragma("unroll") for (int m = 0; m < 4; ++m) _Pragma("unroll") for (int k = 0; k < 2; ++k) dst[m][k] = *(const PG8_LAS bf16x8*)(lds + PG8_SA(b, h) + aoff + m * 2048 + k * 1024); } while (0)
; #define PG8_LDB(dst, b, h) do { _Pragma("unroll") for (int n = 0; n < 2; ++n) _Pragma("unroll") for (int k = 0; k < 2; ++k) dst[n][k] = *(const PG8_LAS bf16x8*)(lds + PG8_SB(b, h) + boff + n * 2048 + k * 1024); } while (0)
; #define PG8_WAIT_V(n) asm volatile("s_waitcnt vmcnt(" #n ")" ::: "memory")
; #define PG8_WAIT_V8_UNLESS_FIRST(t) asm volatile("s_cmp_eq_u32 %0, 0\n\ts_cbranch_scc1 .Lpg8skip%=\n\ts_waitcnt vmcnt(8)\n.Lpg8skip%=:" :: "s"(t) : "scc", "memory")
; #define PG8_WAIT_L(n) asm volatile("s_waitcnt lgkmcnt(" #n ")" ::: "memory")
; #define PG8_BAR __builtin_amdgcn_s_barrier()
; #define PG8_SCHED __builtin_amdgcn_sched_barrier(0)
; template <class Epi, class Sched, bool ALIGN_EPI = false, bool SP2 = false, bool FP8 = false, bool ABLK = false>
; __device__ __forceinline__ void gemm_phase(PG8_LAS unsigned char* lds, const Gemm g, const Sched& S, const Epi& E) {
;     ...
;             PG8_WAIT_V8_UNLESS_FIRST(t); PG8_WAIT_L(0); PG8_BAR; PG8_MMA(0, 0, At, B0); PG8_MMA(0, 1, At, B1); PG8_BAR; PG8_SCHED;
;             PG8_LDA(At, 0, 1); PG8_STAGE(PG8_SB(0, 0), b2, voffB); PG8_STAGE(PG8_SB(0, 1), b2 + hstep, voffB); PG8_STAGE(PG8_SA(0, 0), a2, voffA);
;             PG8_WAIT_V8_UNLESS_FIRST(t); PG8_WAIT_L(0); PG8_BAR; PG8_MMA(1, 0, At, B0); PG8_MMA(1, 1, At, B1); PG8_BAR; PG8_SCHED;
;             PG8_LDB(B0, 1, 0); PG8_LDB(B1, 1, 1); PG8_SCHED; PG8_LDA(At, 1, 0); PG8_STAGE(PG8_SA(0, 1), a2 + hstepA, voffA);
;             PG8_WAIT_V(8); PG8_WAIT_L(0); PG8_BAR; PG8_MMA(0, 0, At, B0); PG8_MMA(0, 1, At, B1); PG8_BAR; PG8_SCHED;
.Lpg8skip2:
	s_waitcnt lgkmcnt(0)
	s_barrier
	s_waitcnt lgkmcnt(0)
	v_mfma_scale_f32_16x16x128_f8f6f4 v[160:163], v[28:35], v[186:193], v[160:163], v245, v245 op_sel_hi:[0,0,0]
	v_mfma_scale_f32_16x16x128_f8f6f4 v[156:159], v[20:27], v[186:193], v[156:159], v245, v245 op_sel_hi:[0,0,0]
	v_mfma_scale_f32_16x16x128_f8f6f4 v[144:147], v[28:35], v[208:215], v[144:147], v245, v245 op_sel_hi:[0,0,0]
	v_mfma_scale_f32_16x16x128_f8f6f4 v[140:143], v[20:27], v[208:215], v[140:143], v245, v245 op_sel_hi:[0,0,0]
	v_mfma_scale_f32_16x16x128_f8f6f4 v[128:131], v[28:35], v[216:223], v[128:131], v245, v245 op_sel_hi:[0,0,0]
	v_mfma_scale_f32_16x16x128_f8f6f4 v[124:127], v[20:27], v[216:223], v[124:127], v245, v245 op_sel_hi:[0,0,0]
	v_mfma_scale_f32_16x16x128_f8f6f4 v[112:115], v[28:35], v[228:235], v[112:115], v245, v245 op_sel_hi:[0,0,0]
	v_mfma_scale_f32_16x16x128_f8f6f4 v[108:111], v[20:27], v[228:235], v[108:111], v245, v245 op_sel_hi:[0,0,0]
	v_mfma_scale_f32_16x16x128_f8f6f4 v[152:155], v[12:19], v[186:193], v[152:155], v245, v245 op_sel_hi:[0,0,0]
	v_mfma_scale_f32_16x16x128_f8f6f4 v[148:151], v[4:11], v[186:193], v[148:151], v245, v245 op_sel_hi:[0,0,0]
	v_mfma_scale_f32_16x16x128_f8f6f4 v[136:139], v[12:19], v[208:215], v[136:139], v245, v245 op_sel_hi:[0,0,0]
	v_mfma_scale_f32_16x16x128_f8f6f4 v[132:135], v[4:11], v[208:215], v[132:135], v245, v245 op_sel_hi:[0,0,0]
	v_mfma_scale_f32_16x16x128_f8f6f4 v[120:123], v[12:19], v[216:223], v[120:123], v245, v245 op_sel_hi:[0,0,0]
	v_mfma_scale_f32_16x16x128_f8f6f4 v[116:119], v[4:11], v[216:223], v[116:119], v245, v245 op_sel_hi:[0,0,0]
	v_mfma_scale_f32_16x16x128_f8f6f4 v[104:107], v[12:19], v[228:235], v[104:107], v245, v245 op_sel_hi:[0,0,0]
	v_mfma_scale_f32_16x16x128_f8f6f4 v[100:103], v[4:11], v[228:235], v[100:103], v245, v245 op_sel_hi:[0,0,0]
	s_barrier
	s_add_i32 s73, s73, s17
	v_lshl_add_u64 v[178:179], s[60:61], 0, v[2:3]
	s_mov_b32 m0, s73
	ds_read_b128 v[186:189], v184 offset:16384
	ds_read_b128 v[190:193], v184 offset:17408
	ds_read_b128 v[208:211], v184 offset:18432
	ds_read_b128 v[212:215], v184 offset:19456
	ds_read_b128 v[216:219], v184 offset:20480
	ds_read_b128 v[220:223], v184 offset:21504
	ds_read_b128 v[228:231], v184 offset:22528
	ds_read_b128 v[232:235], v184 offset:23552
	global_load_lds_dwordx4 v[178:179], off
	s_add_i32 m0, s73, 0x2000
	s_add_u32 s74, s60, 0x58000
	v_lshl_add_u64 v[180:181], s[60:61], 0, v[164:165]
	s_addc_u32 s75, s61, 0
	s_add_i32 s72, s72, s17
	global_load_lds_dwordx4 v[180:181], off
	v_lshl_add_u64 v[194:195], s[74:75], 0, v[2:3]
	s_mov_b32 m0, s72
	v_lshl_add_u64 v[224:225], s[62:63], 0, v[166:167]
	global_load_lds_dwordx4 v[194:195], off
	v_lshl_add_u64 v[194:195], s[74:75], 0, v[164:165]
	s_add_i32 m0, s72, 0x2000
	s_nop 0
	global_load_lds_dwordx4 v[194:195], off
	v_lshl_add_u64 v[194:195], s[62:63], 0, v[168:169]
	s_mov_b32 m0, s18
	s_nop 0
	global_load_lds_dwordx4 v[194:195], off
	s_mov_b32 m0, s19
	s_nop 0
	global_load_lds_dwordx4 v[224:225], off
	s_cmp_eq_u32 s71, 0
	s_cbranch_scc1 .Lpg8skip3
	s_waitcnt vmcnt(8)
.Lpg8skip3:
	s_waitcnt lgkmcnt(0)
	s_barrier
	s_waitcnt lgkmcnt(0)
	v_mfma_scale_f32_16x16x128_f8f6f4 v[96:99], v[28:35], v[186:193], v[96:99], v245, v245 op_sel_hi:[0,0,0]
	v_mfma_scale_f32_16x16x128_f8f6f4 v[92:95], v[20:27], v[186:193], v[92:95], v245, v245 op_sel_hi:[0,0,0]
	v_mfma_scale_f32_16x16x128_f8f6f4 v[80:83], v[28:35], v[208:215], v[80:83], v245, v245 op_sel_hi:[0,0,0]
	v_mfma_scale_f32_16x16x128_f8f6f4 v[76:79], v[20:27], v[208:215], v[76:79], v245, v245 op_sel_hi:[0,0,0]
	v_mfma_scale_f32_16x16x128_f8f6f4 v[64:67], v[28:35], v[216:223], v[64:67], v245, v245 op_sel_hi:[0,0,0]
	v_mfma_scale_f32_16x16x128_f8f6f4 v[60:63], v[20:27], v[216:223], v[60:63], v245, v245 op_sel_hi:[0,0,0]
	v_mfma_scale_f32_16x16x128_f8f6f4 v[48:51], v[28:35], v[228:235], v[48:51], v245, v245 op_sel_hi:[0,0,0]
	v_mfma_scale_f32_16x16x128_f8f6f4 v[44:47], v[20:27], v[228:235], v[44:47], v245, v245 op_sel_hi:[0,0,0]
	v_mfma_scale_f32_16x16x128_f8f6f4 v[88:91], v[12:19], v[186:193], v[88:91], v245, v245 op_sel_hi:[0,0,0]
	v_mfma_scale_f32_16x16x128_f8f6f4 v[84:87], v[4:11], v[186:193], v[84:87], v245, v245 op_sel_hi:[0,0,0]
	v_mfma_scale_f32_16x16x128_f8f6f4 v[72:75], v[12:19], v[208:215], v[72:75], v245, v245 op_sel_hi:[0,0,0]
	v_mfma_scale_f32_16x16x128_f8f6f4 v[68:71], v[4:11], v[208:215], v[68:71], v245, v245 op_sel_hi:[0,0,0]
	v_mfma_scale_f32_16x16x128_f8f6f4 v[56:59], v[12:19], v[216:223], v[56:59], v245, v245 op_sel_hi:[0,0,0]
	v_mfma_scale_f32_16x16x128_f8f6f4 v[52:55], v[4:11], v[216:223], v[52:55], v245, v245 op_sel_hi:[0,0,0]
	v_mfma_scale_f32_16x16x128_f8f6f4 v[40:43], v[12:19], v[228:235], v[40:43], v245, v245 op_sel_hi:[0,0,0]
	v_mfma_scale_f32_16x16x128_f8f6f4 v[36:39], v[4:11], v[228:235], v[36:39], v245, v245 op_sel_hi:[0,0,0]
	s_barrier
	s_add_i32 s62, 0, 0x18000
	s_add_i32 s63, 0, 0x1c000
	v_add_u32_e32 v16, s62, v183
	v_add_u32_e32 v32, s63, v183
	ds_read_b128 v[4:7], v16
	ds_read_b128 v[8:11], v16 offset:1024
	ds_read_b128 v[12:15], v16 offset:2048
	ds_read_b128 v[16:19], v16 offset:3072
	ds_read_b128 v[20:23], v32
	ds_read_b128 v[24:27], v32 offset:1024
	ds_read_b128 v[28:31], v32 offset:2048
	ds_read_b128 v[32:35], v32 offset:3072
	s_mov_b32 m0, s20
	v_lshl_add_u64 v[194:195], v[194:195], 0, s[24:25]
	ds_read_b128 v[186:189], v184 offset:32768
	ds_read_b128 v[190:193], v184 offset:33792
	ds_read_b128 v[208:211], v184 offset:34816
	ds_read_b128 v[212:215], v184 offset:35840
	ds_read_b128 v[216:219], v184 offset:36864
	ds_read_b128 v[220:223], v184 offset:37888
	ds_read_b128 v[228:231], v184 offset:38912
	ds_read_b128 v[232:235], v184 offset:39936
	global_load_lds_dwordx4 v[194:195], off
	v_lshl_add_u64 v[194:195], v[224:225], 0, s[24:25]
	s_mov_b32 m0, s21
	s_nop 0
	global_load_lds_dwordx4 v[194:195], off
	s_waitcnt vmcnt(8)
	s_waitcnt lgkmcnt(0)
	s_barrier
; #define PG8_STAGE(bufoff, gbase, voff) do { _Pragma("unroll") for (int _i = 0; _i < 2; ++_i) \
;         __builtin_amdgcn_global_load_lds((const unsigned*)((const char*)(gbase) + (voff)[_i]), (PG8_LAS unsigned*)(lds + (bufoff) + ldsw + _i * 8192), 16, 0, 0); } while (0)
; #define PG8_LDA(dst, b, h) do { _Pragma("unroll") for (int m = 0; m < 4; ++m) _Pragma("unroll") for (int k = 0; k < 2; ++k) dst[m][k] = *(const PG8_LAS bf16x8*)(lds + PG8_SA(b, h) + aoff + m * 2048 + k * 1024); } while (0)
; #define PG8_WAIT_V(n) asm volatile("s_waitcnt vmcnt(" #n ")" ::: "memory")
; #define PG8_WAIT_L(n) asm volatile("s_waitcnt lgkmcnt(" #n ")" ::: "memory")
; #define PG8_BAR __builtin_amdgcn_s_barrier()
; #define PG8_SCHED __builtin_amdgcn_sched_barrier(0)
; template <class Epi, class Sched, bool ALIGN_EPI = false, bool SP2 = false, bool FP8 = false, bool ABLK = false>
; __device__ __forceinline__ void gemm_phase(PG8_LAS unsigned char* lds, const Gemm g, const Sched& S, const Epi& E) {
;     ...
;             PG8_WAIT_V(8); PG8_WAIT_L(0); PG8_BAR; PG8_MMA(0, 0, At, B0); PG8_MMA(0, 1, At, B1); PG8_BAR; PG8_SCHED;
;             PG8_LDA(At, 1, 1); PG8_STAGE(PG8_SB(1, 0), b3, voffB); PG8_STAGE(PG8_SB(1, 1), b3 + hstep, voffB); PG8_STAGE(PG8_SA(1, 0), a3, voffA);
;             PG8_WAIT_V(8); PG8_WAIT_L(0); PG8_BAR; PG8_MMA(1, 0, At, B0); PG8_MMA(1, 1, At, B1); PG8_BAR; PG8_SCHED;
;     ...
;         if constexpr (SP2) PG8_WAIT_V(0);
;         if constexpr (FP8) asm volatile("s_nop 15\n\ts_nop 15" ::: "memory");
;         if constexpr (ALIGN_EPI) { if (wr == 0) PG8_BAR; }
	s_waitcnt lgkmcnt(0)
	v_mfma_scale_f32_16x16x128_f8f6f4 v[160:163], v[4:11], v[186:193], v[160:163], v245, v245 op_sel_hi:[0,0,0]
	v_mfma_scale_f32_16x16x128_f8f6f4 v[156:159], v[12:19], v[186:193], v[156:159], v245, v245 op_sel_hi:[0,0,0]
	v_mfma_scale_f32_16x16x128_f8f6f4 v[144:147], v[4:11], v[208:215], v[144:147], v245, v245 op_sel_hi:[0,0,0]
	v_mfma_scale_f32_16x16x128_f8f6f4 v[140:143], v[12:19], v[208:215], v[140:143], v245, v245 op_sel_hi:[0,0,0]
	v_mfma_scale_f32_16x16x128_f8f6f4 v[128:131], v[4:11], v[216:223], v[128:131], v245, v245 op_sel_hi:[0,0,0]
	v_mfma_scale_f32_16x16x128_f8f6f4 v[124:127], v[12:19], v[216:223], v[124:127], v245, v245 op_sel_hi:[0,0,0]
	v_mfma_scale_f32_16x16x128_f8f6f4 v[112:115], v[4:11], v[228:235], v[112:115], v245, v245 op_sel_hi:[0,0,0]
	v_mfma_scale_f32_16x16x128_f8f6f4 v[108:111], v[12:19], v[228:235], v[108:111], v245, v245 op_sel_hi:[0,0,0]
	v_mfma_scale_f32_16x16x128_f8f6f4 v[152:155], v[20:27], v[186:193], v[152:155], v245, v245 op_sel_hi:[0,0,0]
	v_mfma_scale_f32_16x16x128_f8f6f4 v[148:151], v[28:35], v[186:193], v[148:151], v245, v245 op_sel_hi:[0,0,0]
	v_mfma_scale_f32_16x16x128_f8f6f4 v[136:139], v[20:27], v[208:215], v[136:139], v245, v245 op_sel_hi:[0,0,0]
	v_mfma_scale_f32_16x16x128_f8f6f4 v[132:135], v[28:35], v[208:215], v[132:135], v245, v245 op_sel_hi:[0,0,0]
	v_mfma_scale_f32_16x16x128_f8f6f4 v[120:123], v[20:27], v[216:223], v[120:123], v245, v245 op_sel_hi:[0,0,0]
	v_mfma_scale_f32_16x16x128_f8f6f4 v[116:119], v[28:35], v[216:223], v[116:119], v245, v245 op_sel_hi:[0,0,0]
	v_mfma_scale_f32_16x16x128_f8f6f4 v[104:107], v[20:27], v[228:235], v[104:107], v245, v245 op_sel_hi:[0,0,0]
	v_mfma_scale_f32_16x16x128_f8f6f4 v[100:103], v[28:35], v[228:235], v[100:103], v245, v245 op_sel_hi:[0,0,0]
	s_barrier
	s_add_i32 s62, s62, s17
	v_lshl_add_u64 v[178:179], v[178:179], 0, s[34:35]
	s_mov_b32 m0, s62
	ds_read_b128 v[186:189], v184 offset:49152
	ds_read_b128 v[190:193], v184 offset:50176
	ds_read_b128 v[208:211], v184 offset:51200
	ds_read_b128 v[212:215], v184 offset:52224
	ds_read_b128 v[216:219], v184 offset:53248
	ds_read_b128 v[220:223], v184 offset:54272
	ds_read_b128 v[228:231], v184 offset:55296
	ds_read_b128 v[232:235], v184 offset:56320
	global_load_lds_dwordx4 v[178:179], off
	s_add_i32 m0, s62, 0x2000
	s_add_u32 s60, s60, 0x58080
	v_lshl_add_u64 v[178:179], v[180:181], 0, s[34:35]
	s_addc_u32 s61, s61, 0
	s_add_i32 s62, s63, s17
	global_load_lds_dwordx4 v[178:179], off
	v_lshl_add_u64 v[178:179], s[60:61], 0, v[2:3]
	s_mov_b32 m0, s62
	s_nop 0
	global_load_lds_dwordx4 v[178:179], off
	v_lshl_add_u64 v[178:179], s[60:61], 0, v[164:165]
	s_add_i32 m0, s62, 0x2000
	s_nop 0
	global_load_lds_dwordx4 v[178:179], off
	v_lshl_add_u64 v[178:179], s[58:59], 0, v[168:169]
	s_mov_b32 m0, s64
	s_nop 0
	global_load_lds_dwordx4 v[178:179], off
	v_lshl_add_u64 v[178:179], s[58:59], 0, v[166:167]
	s_mov_b32 m0, s65
	s_nop 0
	global_load_lds_dwordx4 v[178:179], off
	s_waitcnt vmcnt(8)
	s_waitcnt lgkmcnt(0)
	s_barrier
	s_waitcnt lgkmcnt(0)
	v_mfma_scale_f32_16x16x128_f8f6f4 v[96:99], v[4:11], v[186:193], v[96:99], v245, v245 op_sel_hi:[0,0,0]
	v_mfma_scale_f32_16x16x128_f8f6f4 v[92:95], v[12:19], v[186:193], v[92:95], v245, v245 op_sel_hi:[0,0,0]
	v_mfma_scale_f32_16x16x128_f8f6f4 v[80:83], v[4:11], v[208:215], v[80:83], v245, v245 op_sel_hi:[0,0,0]
	v_mfma_scale_f32_16x16x128_f8f6f4 v[76:79], v[12:19], v[208:215], v[76:79], v245, v245 op_sel_hi:[0,0,0]
	v_mfma_scale_f32_16x16x128_f8f6f4 v[64:67], v[4:11], v[216:223], v[64:67], v245, v245 op_sel_hi:[0,0,0]
	v_mfma_scale_f32_16x16x128_f8f6f4 v[60:63], v[12:19], v[216:223], v[60:63], v245, v245 op_sel_hi:[0,0,0]
	v_mfma_scale_f32_16x16x128_f8f6f4 v[48:51], v[4:11], v[228:235], v[48:51], v245, v245 op_sel_hi:[0,0,0]
	v_mfma_scale_f32_16x16x128_f8f6f4 v[44:47], v[12:19], v[228:235], v[44:47], v245, v245 op_sel_hi:[0,0,0]
	v_mfma_scale_f32_16x16x128_f8f6f4 v[88:91], v[20:27], v[186:193], v[88:91], v245, v245 op_sel_hi:[0,0,0]
	v_mfma_scale_f32_16x16x128_f8f6f4 v[84:87], v[28:35], v[186:193], v[84:87], v245, v245 op_sel_hi:[0,0,0]
	v_mfma_scale_f32_16x16x128_f8f6f4 v[72:75], v[20:27], v[208:215], v[72:75], v245, v245 op_sel_hi:[0,0,0]
	v_mfma_scale_f32_16x16x128_f8f6f4 v[68:71], v[28:35], v[208:215], v[68:71], v245, v245 op_sel_hi:[0,0,0]
	v_mfma_scale_f32_16x16x128_f8f6f4 v[56:59], v[20:27], v[216:223], v[56:59], v245, v245 op_sel_hi:[0,0,0]
	v_mfma_scale_f32_16x16x128_f8f6f4 v[52:55], v[28:35], v[216:223], v[52:55], v245, v245 op_sel_hi:[0,0,0]
	v_mfma_scale_f32_16x16x128_f8f6f4 v[40:43], v[20:27], v[228:235], v[40:43], v245, v245 op_sel_hi:[0,0,0]
	v_mfma_scale_f32_16x16x128_f8f6f4 v[36:39], v[28:35], v[228:235], v[36:39], v245, v245 op_sel_hi:[0,0,0]
	s_barrier
	s_add_u32 s4, s4, 0x100
	s_addc_u32 s5, s5, 0
	s_add_u32 s56, s56, 0x10000
	s_addc_u32 s57, s57, 0
	s_cmp_gt_u32 s71, 19
	s_cbranch_scc0 .LBB0_508
	s_waitcnt vmcnt(0)
	s_nop 15
	s_nop 15
	s_and_b64 vcc, exec, s[50:51]
	s_cbranch_vccz .LBB0_511
	s_barrier

; #define PG8_STAGE(bufoff, gbase, voff) do { _Pragma("unroll") for (int _i = 0; _i < 2; ++_i) \
;         __builtin_amdgcn_global_load_lds((const unsigned*)((const char*)(gbase) + (voff)[_i]), (PG8_LAS unsigned*)(lds + (bufoff) + ldsw + _i * 8192), 16, 0, 0); } while (0)
; #define PG8_LDA(dst, b, h) do { _Pragma("unroll") for (int m = 0; m < 4; ++m) _Pragma("unroll") for (int k = 0; k < 2; ++k) dst[m][k] = *(const PG8_LAS bf16x8*)(lds + PG8_SA(b, h) + aoff + m * 2048 + k * 1024); } while (0)
; #define PG8_WAIT_V8_UNLESS_FIRST(t) asm volatile("s_cmp_eq_u32 %0, 0\n\ts_cbranch_scc1 .Lpg8skip%=\n\ts_waitcnt vmcnt(8)\n.Lpg8skip%=:" :: "s"(t) : "scc", "memory")
; #define PG8_WAIT_L(n) asm volatile("s_waitcnt lgkmcnt(" #n ")" ::: "memory")
; #define PG8_BAR __builtin_amdgcn_s_barrier()
; #define PG8_SCHED __builtin_amdgcn_sched_barrier(0)
; template <class Epi, class Sched, bool ALIGN_EPI = false, bool SP2 = false, bool FP8 = false, bool ABLK = false>
; __device__ __forceinline__ void gemm_phase(PG8_LAS unsigned char* lds, const Gemm g, const Sched& S, const Epi& E) {
;     ...
;             PG8_WAIT_V8_UNLESS_FIRST(t); PG8_WAIT_L(0); PG8_BAR; PG8_MMA(0, 0, At, B0); PG8_MMA(0, 1, At, B1); PG8_BAR; PG8_SCHED;
;             PG8_LDA(At, 0, 1); PG8_STAGE(PG8_SB(0, 0), b2, voffB); PG8_STAGE(PG8_SB(0, 1), b2 + hstep, voffB); PG8_STAGE(PG8_SA(0, 0), a2, voffA);
;             PG8_WAIT_V8_UNLESS_FIRST(t); PG8_WAIT_L(0); PG8_BAR; PG8_MMA(1, 0, At, B0); PG8_MMA(1, 1, At, B1); PG8_BAR; PG8_SCHED;
.Lpg8skip4:
	s_waitcnt lgkmcnt(0)
	s_barrier
	s_waitcnt lgkmcnt(0)
	v_mfma_f32_16x16x32_bf16 v[128:131], v[132:135], v[164:167], v[128:131]
	v_mfma_f32_16x16x32_bf16 v[124:127], v[140:143], v[164:167], v[124:127]
	v_mfma_f32_16x16x32_bf16 v[112:115], v[132:135], v[182:185], v[112:115]
	v_mfma_f32_16x16x32_bf16 v[108:111], v[140:143], v[182:185], v[108:111]
	v_mfma_f32_16x16x32_bf16 v[96:99], v[132:135], v[212:215], v[96:99]
	v_mfma_f32_16x16x32_bf16 v[92:95], v[140:143], v[212:215], v[92:95]
	v_mfma_f32_16x16x32_bf16 v[80:83], v[132:135], v[220:223], v[80:83]
	v_mfma_f32_16x16x32_bf16 v[76:79], v[140:143], v[220:223], v[76:79]
	v_mfma_f32_16x16x32_bf16 v[128:131], v[136:139], v[168:171], v[128:131]
	v_mfma_f32_16x16x32_bf16 v[124:127], v[144:147], v[168:171], v[124:127]
	v_mfma_f32_16x16x32_bf16 v[112:115], v[136:139], v[208:211], v[112:115]
	v_mfma_f32_16x16x32_bf16 v[108:111], v[144:147], v[208:211], v[108:111]
	v_mfma_f32_16x16x32_bf16 v[96:99], v[136:139], v[216:219], v[96:99]
	v_mfma_f32_16x16x32_bf16 v[92:95], v[144:147], v[216:219], v[92:95]
	v_mfma_f32_16x16x32_bf16 v[80:83], v[136:139], v[228:231], v[80:83]
	v_mfma_f32_16x16x32_bf16 v[76:79], v[144:147], v[228:231], v[76:79]
	v_mfma_f32_16x16x32_bf16 v[120:123], v[148:151], v[164:167], v[120:123]
	v_mfma_f32_16x16x32_bf16 v[116:119], v[156:159], v[164:167], v[116:119]
	v_mfma_f32_16x16x32_bf16 v[104:107], v[148:151], v[182:185], v[104:107]
	v_mfma_f32_16x16x32_bf16 v[100:103], v[156:159], v[182:185], v[100:103]
	v_mfma_f32_16x16x32_bf16 v[88:91], v[148:151], v[212:215], v[88:91]
	v_mfma_f32_16x16x32_bf16 v[84:87], v[156:159], v[212:215], v[84:87]
	v_mfma_f32_16x16x32_bf16 v[72:75], v[148:151], v[220:223], v[72:75]
	v_mfma_f32_16x16x32_bf16 v[68:71], v[156:159], v[220:223], v[68:71]
	v_mfma_f32_16x16x32_bf16 v[120:123], v[152:155], v[168:171], v[120:123]
	v_mfma_f32_16x16x32_bf16 v[116:119], v[160:163], v[168:171], v[116:119]
	v_mfma_f32_16x16x32_bf16 v[104:107], v[152:155], v[208:211], v[104:107]
	v_mfma_f32_16x16x32_bf16 v[100:103], v[160:163], v[208:211], v[100:103]
	v_mfma_f32_16x16x32_bf16 v[88:91], v[152:155], v[216:219], v[88:91]
	v_mfma_f32_16x16x32_bf16 v[84:87], v[160:163], v[216:219], v[84:87]
	v_mfma_f32_16x16x32_bf16 v[72:75], v[152:155], v[228:231], v[72:75]
	v_mfma_f32_16x16x32_bf16 v[68:71], v[160:163], v[228:231], v[68:71]
	s_barrier
	s_add_i32 s96, s96, s7
	v_lshl_add_u64 v[188:189], s[44:45], 0, v[2:3]
	s_mov_b32 m0, s96
	ds_read_b128 v[164:167], v195 offset:16384
	ds_read_b128 v[168:171], v195 offset:17408
	ds_read_b128 v[182:185], v195 offset:18432
	ds_read_b128 v[208:211], v195 offset:19456
	ds_read_b128 v[212:215], v195 offset:20480
	ds_read_b128 v[216:219], v195 offset:21504
	ds_read_b128 v[220:223], v195 offset:22528
	ds_read_b128 v[228:231], v195 offset:23552
	global_load_lds_dwordx4 v[188:189], off
	s_add_i32 m0, s96, 0x2000
	s_add_u32 s96, s44, 0x40000
	v_lshl_add_u64 v[192:193], s[44:45], 0, v[172:173]
	s_addc_u32 s97, s45, 0
	s_add_i32 vcc_lo, vcc_lo, s7
	global_load_lds_dwordx4 v[192:193], off
	v_lshl_add_u64 v[224:225], s[96:97], 0, v[2:3]
	s_mov_b32 m0, vcc_lo
	v_lshl_add_u64 v[232:233], s[90:91], 0, v[174:175]
	global_load_lds_dwordx4 v[224:225], off
	v_lshl_add_u64 v[224:225], s[96:97], 0, v[172:173]
	s_add_i32 m0, vcc_lo, 0x2000
	s_nop 0
	global_load_lds_dwordx4 v[224:225], off
	v_lshl_add_u64 v[224:225], s[90:91], 0, v[176:177]
	s_mov_b32 m0, s8
	s_nop 0
	global_load_lds_dwordx4 v[224:225], off
	s_mov_b32 m0, s9
	s_nop 0
	global_load_lds_dwordx4 v[232:233], off
	s_cmp_eq_u32 s95, 0
	s_cbranch_scc1 .Lpg8skip5
	s_waitcnt vmcnt(8)
.Lpg8skip5:
	s_waitcnt lgkmcnt(0)
	s_barrier
	s_waitcnt lgkmcnt(0)
	v_mfma_f32_16x16x32_bf16 v[64:67], v[132:135], v[164:167], v[64:67]
	v_mfma_f32_16x16x32_bf16 v[60:63], v[140:143], v[164:167], v[60:63]
	v_mfma_f32_16x16x32_bf16 v[48:51], v[132:135], v[182:185], v[48:51]
	v_mfma_f32_16x16x32_bf16 v[44:47], v[140:143], v[182:185], v[44:47]
	v_mfma_f32_16x16x32_bf16 v[32:35], v[132:135], v[212:215], v[32:35]
	v_mfma_f32_16x16x32_bf16 v[28:31], v[140:143], v[212:215], v[28:31]
	v_mfma_f32_16x16x32_bf16 v[16:19], v[132:135], v[220:223], v[16:19]
	v_mfma_f32_16x16x32_bf16 v[12:15], v[140:143], v[220:223], v[12:15]
	v_mfma_f32_16x16x32_bf16 v[64:67], v[136:139], v[168:171], v[64:67]
	v_mfma_f32_16x16x32_bf16 v[60:63], v[144:147], v[168:171], v[60:63]
	v_mfma_f32_16x16x32_bf16 v[48:51], v[136:139], v[208:211], v[48:51]
	v_mfma_f32_16x16x32_bf16 v[44:47], v[144:147], v[208:211], v[44:47]
	v_mfma_f32_16x16x32_bf16 v[32:35], v[136:139], v[216:219], v[32:35]
	v_mfma_f32_16x16x32_bf16 v[28:31], v[144:147], v[216:219], v[28:31]
	v_mfma_f32_16x16x32_bf16 v[16:19], v[136:139], v[228:231], v[16:19]
	v_mfma_f32_16x16x32_bf16 v[12:15], v[144:147], v[228:231], v[12:15]
	v_mfma_f32_16x16x32_bf16 v[56:59], v[148:151], v[164:167], v[56:59]
	v_mfma_f32_16x16x32_bf16 v[52:55], v[156:159], v[164:167], v[52:55]
	v_mfma_f32_16x16x32_bf16 v[40:43], v[148:151], v[182:185], v[40:43]
	v_mfma_f32_16x16x32_bf16 v[36:39], v[156:159], v[182:185], v[36:39]
	v_mfma_f32_16x16x32_bf16 v[24:27], v[148:151], v[212:215], v[24:27]
	v_mfma_f32_16x16x32_bf16 v[20:23], v[156:159], v[212:215], v[20:23]
	v_mfma_f32_16x16x32_bf16 v[8:11], v[148:151], v[220:223], v[8:11]
	v_mfma_f32_16x16x32_bf16 v[4:7], v[156:159], v[220:223], v[4:7]
	v_mfma_f32_16x16x32_bf16 v[56:59], v[152:155], v[168:171], v[56:59]
	v_mfma_f32_16x16x32_bf16 v[52:55], v[160:163], v[168:171], v[52:55]
	v_mfma_f32_16x16x32_bf16 v[40:43], v[152:155], v[208:211], v[40:43]
	v_mfma_f32_16x16x32_bf16 v[36:39], v[160:163], v[208:211], v[36:39]
	v_mfma_f32_16x16x32_bf16 v[24:27], v[152:155], v[216:219], v[24:27]
	v_mfma_f32_16x16x32_bf16 v[20:23], v[160:163], v[216:219], v[20:23]
	v_mfma_f32_16x16x32_bf16 v[8:11], v[152:155], v[228:231], v[8:11]
	v_mfma_f32_16x16x32_bf16 v[4:7], v[160:163], v[228:231], v[4:7]
	s_barrier
; #define PG8_STAGE(bufoff, gbase, voff) do { _Pragma("unroll") for (int _i = 0; _i < 2; ++_i) \
;         __builtin_amdgcn_global_load_lds((const unsigned*)((const char*)(gbase) + (voff)[_i]), (PG8_LAS unsigned*)(lds + (bufoff) + ldsw + _i * 8192), 16, 0, 0); } while (0)
; #define PG8_LDA(dst, b, h) do { _Pragma("unroll") for (int m = 0; m < 4; ++m) _Pragma("unroll") for (int k = 0; k < 2; ++k) dst[m][k] = *(const PG8_LAS bf16x8*)(lds + PG8_SA(b, h) + aoff + m * 2048 + k * 1024); } while (0)
; #define PG8_LDB(dst, b, h) do { _Pragma("unroll") for (int n = 0; n < 2; ++n) _Pragma("unroll") for (int k = 0; k < 2; ++k) dst[n][k] = *(const PG8_LAS bf16x8*)(lds + PG8_SB(b, h) + boff + n * 2048 + k * 1024); } while (0)
; #define PG8_WAIT_V(n) asm volatile("s_waitcnt vmcnt(" #n ")" ::: "memory")
; #define PG8_WAIT_L(n) asm volatile("s_waitcnt lgkmcnt(" #n ")" ::: "memory")
; #define PG8_BAR __builtin_amdgcn_s_barrier()
; #define PG8_SCHED __builtin_amdgcn_sched_barrier(0)
; template <class Epi, class Sched, bool ALIGN_EPI = false, bool SP2 = false, bool FP8 = false, bool ABLK = false>
; __device__ __forceinline__ void gemm_phase(PG8_LAS unsigned char* lds, const Gemm g, const Sched& S, const Epi& E) {
;     ...
;             PG8_LDB(B0, 1, 0); PG8_LDB(B1, 1, 1); PG8_SCHED; PG8_LDA(At, 1, 0); PG8_STAGE(PG8_SA(0, 1), a2 + hstepA, voffA);
;             PG8_WAIT_V(8); PG8_WAIT_L(0); PG8_BAR; PG8_MMA(0, 0, At, B0); PG8_MMA(0, 1, At, B1); PG8_BAR; PG8_SCHED;
	s_add_i32 s96, 0, 0x18000
	s_add_i32 s97, 0, 0x1c000
	v_add_u32_e32 v144, s96, v191
	v_add_u32_e32 v160, s97, v191
	ds_read_b128 v[132:135], v144
	ds_read_b128 v[136:139], v144 offset:1024
	ds_read_b128 v[140:143], v144 offset:2048
	ds_read_b128 v[144:147], v144 offset:3072
	ds_read_b128 v[148:151], v160
	ds_read_b128 v[152:155], v160 offset:1024
	ds_read_b128 v[156:159], v160 offset:2048
	ds_read_b128 v[160:163], v160 offset:3072
	s_add_u32 s90, s90, 0x40000
	s_addc_u32 s91, s91, 0
	s_mov_b32 m0, s17
	v_lshl_add_u64 v[234:235], s[90:91], 0, v[176:177]
	ds_read_b128 v[164:167], v195 offset:32768
	ds_read_b128 v[168:171], v195 offset:33792
	ds_read_b128 v[182:185], v195 offset:34816
	ds_read_b128 v[208:211], v195 offset:35840
	ds_read_b128 v[212:215], v195 offset:36864
	ds_read_b128 v[216:219], v195 offset:37888
	ds_read_b128 v[220:223], v195 offset:38912
	ds_read_b128 v[228:231], v195 offset:39936
	global_load_lds_dwordx4 v[234:235], off
	v_lshl_add_u64 v[234:235], s[90:91], 0, v[174:175]
	s_mov_b32 m0, s18
	s_nop 0
	global_load_lds_dwordx4 v[234:235], off
	s_waitcnt vmcnt(8)
	s_waitcnt lgkmcnt(0)
	s_barrier
	s_waitcnt lgkmcnt(0)
	v_mfma_f32_16x16x32_bf16 v[128:131], v[132:135], v[164:167], v[128:131]
	v_mfma_f32_16x16x32_bf16 v[124:127], v[140:143], v[164:167], v[124:127]
	v_mfma_f32_16x16x32_bf16 v[112:115], v[132:135], v[182:185], v[112:115]
	v_mfma_f32_16x16x32_bf16 v[108:111], v[140:143], v[182:185], v[108:111]
	v_mfma_f32_16x16x32_bf16 v[96:99], v[132:135], v[212:215], v[96:99]
	v_mfma_f32_16x16x32_bf16 v[92:95], v[140:143], v[212:215], v[92:95]
	v_mfma_f32_16x16x32_bf16 v[80:83], v[132:135], v[220:223], v[80:83]
	v_mfma_f32_16x16x32_bf16 v[76:79], v[140:143], v[220:223], v[76:79]
	v_mfma_f32_16x16x32_bf16 v[128:131], v[136:139], v[168:171], v[128:131]
	v_mfma_f32_16x16x32_bf16 v[124:127], v[144:147], v[168:171], v[124:127]
	v_mfma_f32_16x16x32_bf16 v[112:115], v[136:139], v[208:211], v[112:115]
	v_mfma_f32_16x16x32_bf16 v[108:111], v[144:147], v[208:211], v[108:111]
	v_mfma_f32_16x16x32_bf16 v[96:99], v[136:139], v[216:219], v[96:99]
	v_mfma_f32_16x16x32_bf16 v[92:95], v[144:147], v[216:219], v[92:95]
	v_mfma_f32_16x16x32_bf16 v[80:83], v[136:139], v[228:231], v[80:83]
	v_mfma_f32_16x16x32_bf16 v[76:79], v[144:147], v[228:231], v[76:79]
	v_mfma_f32_16x16x32_bf16 v[120:123], v[148:151], v[164:167], v[120:123]
	v_mfma_f32_16x16x32_bf16 v[116:119], v[156:159], v[164:167], v[116:119]
	v_mfma_f32_16x16x32_bf16 v[104:107], v[148:151], v[182:185], v[104:107]
	v_mfma_f32_16x16x32_bf16 v[100:103], v[156:159], v[182:185], v[100:103]
	v_mfma_f32_16x16x32_bf16 v[88:91], v[148:151], v[212:215], v[88:91]
	v_mfma_f32_16x16x32_bf16 v[84:87], v[156:159], v[212:215], v[84:87]
	v_mfma_f32_16x16x32_bf16 v[72:75], v[148:151], v[220:223], v[72:75]
	v_mfma_f32_16x16x32_bf16 v[68:71], v[156:159], v[220:223], v[68:71]
	v_mfma_f32_16x16x32_bf16 v[120:123], v[152:155], v[168:171], v[120:123]
	v_mfma_f32_16x16x32_bf16 v[116:119], v[160:163], v[168:171], v[116:119]
	v_mfma_f32_16x16x32_bf16 v[104:107], v[152:155], v[208:211], v[104:107]
	v_mfma_f32_16x16x32_bf16 v[100:103], v[160:163], v[208:211], v[100:103]
	v_mfma_f32_16x16x32_bf16 v[88:91], v[152:155], v[216:219], v[88:91]
	v_mfma_f32_16x16x32_bf16 v[84:87], v[160:163], v[216:219], v[84:87]
	v_mfma_f32_16x16x32_bf16 v[72:75], v[152:155], v[228:231], v[72:75]
	v_mfma_f32_16x16x32_bf16 v[68:71], v[160:163], v[228:231], v[68:71]
	s_barrier
; #define PG8_STAGE(bufoff, gbase, voff) do { _Pragma("unroll") for (int _i = 0; _i < 2; ++_i) \
;         __builtin_amdgcn_global_load_lds((const unsigned*)((const char*)(gbase) + (voff)[_i]), (PG8_LAS unsigned*)(lds + (bufoff) + ldsw + _i * 8192), 16, 0, 0); } while (0)
; #define PG8_LDA(dst, b, h) do { _Pragma("unroll") for (int m = 0; m < 4; ++m) _Pragma("unroll") for (int k = 0; k < 2; ++k) dst[m][k] = *(const PG8_LAS bf16x8*)(lds + PG8_SA(b, h) + aoff + m * 2048 + k * 1024); } while (0)
; #define PG8_WAIT_V(n) asm volatile("s_waitcnt vmcnt(" #n ")" ::: "memory")
; #define PG8_WAIT_L(n) asm volatile("s_waitcnt lgkmcnt(" #n ")" ::: "memory")
; #define PG8_BAR __builtin_amdgcn_s_barrier()
; #define PG8_SCHED __builtin_amdgcn_sched_barrier(0)
;     __device__ __forceinline__ void operator()(const f32x4 (&acc)[2][2][4][2], const Unit& u, int wr, int wc, int fr, int fq) const {
;         if (u.pm >= TILE_X) { const EpiWin W{ws, ss, qscale}; const Unit v{u.pm - TILE_X, u.pn - tin}; W(acc, v, wr, wc, fr, fq); }
; template <class Epi, class Sched, bool ALIGN_EPI = false, bool SP2 = false, bool FP8 = false, bool ABLK = false>
; __device__ __forceinline__ void gemm_phase(PG8_LAS unsigned char* lds, const Gemm g, const Sched& S, const Epi& E) {
;     ...
;             PG8_LDA(At, 1, 1); PG8_STAGE(PG8_SB(1, 0), b3, voffB); PG8_STAGE(PG8_SB(1, 1), b3 + hstep, voffB); PG8_STAGE(PG8_SA(1, 0), a3, voffA);
;             PG8_WAIT_V(8); PG8_WAIT_L(0); PG8_BAR; PG8_MMA(1, 0, At, B0); PG8_MMA(1, 1, At, B1); PG8_BAR; PG8_SCHED;
	s_add_i32 s90, s96, s7
	v_lshl_add_u64 v[188:189], v[188:189], 0, s[34:35]
	s_mov_b32 m0, s90
	ds_read_b128 v[164:167], v195 offset:49152
	ds_read_b128 v[168:171], v195 offset:50176
	ds_read_b128 v[182:185], v195 offset:51200
	ds_read_b128 v[208:211], v195 offset:52224
	ds_read_b128 v[212:215], v195 offset:53248
	ds_read_b128 v[216:219], v195 offset:54272
	ds_read_b128 v[220:223], v195 offset:55296
	ds_read_b128 v[228:231], v195 offset:56320
	global_load_lds_dwordx4 v[188:189], off
	s_add_i32 m0, s90, 0x2000
	s_add_u32 s44, s44, 0x40080
	v_lshl_add_u64 v[188:189], v[192:193], 0, s[34:35]
	s_addc_u32 s45, s45, 0
	s_add_i32 s90, s97, s7
	global_load_lds_dwordx4 v[188:189], off
	v_lshl_add_u64 v[188:189], s[44:45], 0, v[2:3]
	s_mov_b32 m0, s90
	s_nop 0
	global_load_lds_dwordx4 v[188:189], off
	v_lshl_add_u64 v[188:189], s[44:45], 0, v[172:173]
	s_add_i32 m0, s90, 0x2000
	s_nop 0
	global_load_lds_dwordx4 v[188:189], off
	v_lshl_add_u64 v[188:189], v[224:225], 0, s[34:35]
	s_mov_b32 m0, s19
	s_nop 0
	global_load_lds_dwordx4 v[188:189], off
	v_lshl_add_u64 v[188:189], v[232:233], 0, s[34:35]
	s_mov_b32 m0, s20
	s_nop 0
	global_load_lds_dwordx4 v[188:189], off
	s_waitcnt vmcnt(8)
	s_waitcnt lgkmcnt(0)
	s_barrier
	s_waitcnt lgkmcnt(0)
	v_mfma_f32_16x16x32_bf16 v[64:67], v[132:135], v[164:167], v[64:67]
	v_mfma_f32_16x16x32_bf16 v[60:63], v[140:143], v[164:167], v[60:63]
	v_mfma_f32_16x16x32_bf16 v[48:51], v[132:135], v[182:185], v[48:51]
	v_mfma_f32_16x16x32_bf16 v[44:47], v[140:143], v[182:185], v[44:47]
	v_mfma_f32_16x16x32_bf16 v[32:35], v[132:135], v[212:215], v[32:35]
	v_mfma_f32_16x16x32_bf16 v[28:31], v[140:143], v[212:215], v[28:31]
	v_mfma_f32_16x16x32_bf16 v[16:19], v[132:135], v[220:223], v[16:19]
	v_mfma_f32_16x16x32_bf16 v[12:15], v[140:143], v[220:223], v[12:15]
	v_mfma_f32_16x16x32_bf16 v[64:67], v[136:139], v[168:171], v[64:67]
	v_mfma_f32_16x16x32_bf16 v[60:63], v[144:147], v[168:171], v[60:63]
	v_mfma_f32_16x16x32_bf16 v[48:51], v[136:139], v[208:211], v[48:51]
	v_mfma_f32_16x16x32_bf16 v[44:47], v[144:147], v[208:211], v[44:47]
	v_mfma_f32_16x16x32_bf16 v[32:35], v[136:139], v[216:219], v[32:35]
	v_mfma_f32_16x16x32_bf16 v[28:31], v[144:147], v[216:219], v[28:31]
	v_mfma_f32_16x16x32_bf16 v[16:19], v[136:139], v[228:231], v[16:19]
	v_mfma_f32_16x16x32_bf16 v[12:15], v[144:147], v[228:231], v[12:15]
	v_mfma_f32_16x16x32_bf16 v[56:59], v[148:151], v[164:167], v[56:59]
	v_mfma_f32_16x16x32_bf16 v[52:55], v[156:159], v[164:167], v[52:55]
	v_mfma_f32_16x16x32_bf16 v[40:43], v[148:151], v[182:185], v[40:43]
	v_mfma_f32_16x16x32_bf16 v[36:39], v[156:159], v[182:185], v[36:39]
	v_mfma_f32_16x16x32_bf16 v[24:27], v[148:151], v[212:215], v[24:27]
	v_mfma_f32_16x16x32_bf16 v[20:23], v[156:159], v[212:215], v[20:23]
	v_mfma_f32_16x16x32_bf16 v[8:11], v[148:151], v[220:223], v[8:11]
	v_mfma_f32_16x16x32_bf16 v[4:7], v[156:159], v[220:223], v[4:7]
	v_mfma_f32_16x16x32_bf16 v[56:59], v[152:155], v[168:171], v[56:59]
	v_mfma_f32_16x16x32_bf16 v[52:55], v[160:163], v[168:171], v[52:55]
	v_mfma_f32_16x16x32_bf16 v[40:43], v[152:155], v[208:211], v[40:43]
	v_mfma_f32_16x16x32_bf16 v[36:39], v[160:163], v[208:211], v[36:39]
	v_mfma_f32_16x16x32_bf16 v[24:27], v[152:155], v[216:219], v[24:27]
	v_mfma_f32_16x16x32_bf16 v[20:23], v[160:163], v[216:219], v[20:23]
	v_mfma_f32_16x16x32_bf16 v[8:11], v[152:155], v[228:231], v[8:11]
	v_mfma_f32_16x16x32_bf16 v[4:7], v[160:163], v[228:231], v[4:7]
	s_barrier
	s_add_u32 s42, s42, 0x100
	s_addc_u32 s43, s43, 0
	s_add_u32 s92, s92, 0x100
	s_addc_u32 s94, s94, 0
	s_cmp_gt_u32 s95, 13
	s_mov_b32 s44, s95
	s_cbranch_scc0 .LBB0_600
	s_waitcnt vmcnt(0)
	s_and_b64 vcc, exec, s[64:65]
	s_cbranch_vccnz .LBB0_604
	s_cmpk_lt_i32 s73, 0xf4
	s_mov_b64 s[4:5], -1
	s_cbranch_scc1 .LBB0_605

; #define PG8_STAGE(bufoff, gbase, voff) do { _Pragma("unroll") for (int _i = 0; _i < 2; ++_i) \
;         __builtin_amdgcn_global_load_lds((const unsigned*)((const char*)(gbase) + (voff)[_i]), (PG8_LAS unsigned*)(lds + (bufoff) + ldsw + _i * 8192), 16, 0, 0); } while (0)
; #define PG8_LDA(dst, b, h) do { _Pragma("unroll") for (int m = 0; m < 4; ++m) _Pragma("unroll") for (int k = 0; k < 2; ++k) dst[m][k] = *(const PG8_LAS bf16x8*)(lds + PG8_SA(b, h) + aoff + m * 2048 + k * 1024); } while (0)
; #define PG8_WAIT_V8_UNLESS_FIRST(t) asm volatile("s_cmp_eq_u32 %0, 0\n\ts_cbranch_scc1 .Lpg8skip%=\n\ts_waitcnt vmcnt(8)\n.Lpg8skip%=:" :: "s"(t) : "scc", "memory")
; #define PG8_WAIT_L(n) asm volatile("s_waitcnt lgkmcnt(" #n ")" ::: "memory")
; #define PG8_BAR __builtin_amdgcn_s_barrier()
; #define PG8_SCHED __builtin_amdgcn_sched_barrier(0)
; template <class Epi, class Sched, bool ALIGN_EPI = false, bool SP2 = false, bool FP8 = false, bool ABLK = false>
; __device__ __forceinline__ void gemm_phase(PG8_LAS unsigned char* lds, const Gemm g, const Sched& S, const Epi& E) {
;     ...
;             PG8_WAIT_V8_UNLESS_FIRST(t); PG8_WAIT_L(0); PG8_BAR; PG8_MMA(0, 0, At, B0); PG8_MMA(0, 1, At, B1); PG8_BAR; PG8_SCHED;
;             PG8_LDA(At, 0, 1); PG8_STAGE(PG8_SB(0, 0), b2, voffB); PG8_STAGE(PG8_SB(0, 1), b2 + hstep, voffB); PG8_STAGE(PG8_SA(0, 0), a2, voffA);
;             PG8_WAIT_V8_UNLESS_FIRST(t); PG8_WAIT_L(0); PG8_BAR; PG8_MMA(1, 0, At, B0); PG8_MMA(1, 1, At, B1); PG8_BAR; PG8_SCHED;
.Lpg8skip6:
	s_waitcnt lgkmcnt(0)
	s_barrier
	s_waitcnt lgkmcnt(0)
	v_mfma_f32_16x16x32_bf16 v[152:155], v[124:127], v[174:177], v[152:155]
	v_mfma_f32_16x16x32_bf16 v[148:151], v[132:135], v[174:177], v[148:151]
	v_mfma_f32_16x16x32_bf16 v[112:115], v[124:127], v[182:185], v[112:115]
	v_mfma_f32_16x16x32_bf16 v[108:111], v[132:135], v[182:185], v[108:111]
	v_mfma_f32_16x16x32_bf16 v[96:99], v[124:127], v[190:193], v[96:99]
	v_mfma_f32_16x16x32_bf16 v[92:95], v[132:135], v[190:193], v[92:95]
	v_mfma_f32_16x16x32_bf16 v[80:83], v[124:127], v[214:217], v[80:83]
	v_mfma_f32_16x16x32_bf16 v[76:79], v[132:135], v[214:217], v[76:79]
	v_mfma_f32_16x16x32_bf16 v[152:155], v[128:131], v[178:181], v[152:155]
	v_mfma_f32_16x16x32_bf16 v[148:151], v[136:139], v[178:181], v[148:151]
	v_mfma_f32_16x16x32_bf16 v[112:115], v[128:131], v[186:189], v[112:115]
	v_mfma_f32_16x16x32_bf16 v[108:111], v[136:139], v[186:189], v[108:111]
	v_mfma_f32_16x16x32_bf16 v[96:99], v[128:131], v[210:213], v[96:99]
	v_mfma_f32_16x16x32_bf16 v[92:95], v[136:139], v[210:213], v[92:95]
	v_mfma_f32_16x16x32_bf16 v[80:83], v[128:131], v[218:221], v[80:83]
	v_mfma_f32_16x16x32_bf16 v[76:79], v[136:139], v[218:221], v[76:79]
	v_mfma_f32_16x16x32_bf16 v[120:123], v[140:143], v[174:177], v[120:123]
	v_mfma_f32_16x16x32_bf16 v[116:119], v[156:159], v[174:177], v[116:119]
	v_mfma_f32_16x16x32_bf16 v[104:107], v[140:143], v[182:185], v[104:107]
	v_mfma_f32_16x16x32_bf16 v[100:103], v[156:159], v[182:185], v[100:103]
	v_mfma_f32_16x16x32_bf16 v[88:91], v[140:143], v[190:193], v[88:91]
	v_mfma_f32_16x16x32_bf16 v[84:87], v[156:159], v[190:193], v[84:87]
	v_mfma_f32_16x16x32_bf16 v[72:75], v[140:143], v[214:217], v[72:75]
	v_mfma_f32_16x16x32_bf16 v[68:71], v[156:159], v[214:217], v[68:71]
	v_mfma_f32_16x16x32_bf16 v[120:123], v[144:147], v[178:181], v[120:123]
	v_mfma_f32_16x16x32_bf16 v[116:119], v[170:173], v[178:181], v[116:119]
	v_mfma_f32_16x16x32_bf16 v[104:107], v[144:147], v[186:189], v[104:107]
	v_mfma_f32_16x16x32_bf16 v[100:103], v[170:173], v[186:189], v[100:103]
	v_mfma_f32_16x16x32_bf16 v[88:91], v[144:147], v[210:213], v[88:91]
	v_mfma_f32_16x16x32_bf16 v[84:87], v[170:173], v[210:213], v[84:87]
	v_mfma_f32_16x16x32_bf16 v[72:75], v[144:147], v[218:221], v[72:75]
	v_mfma_f32_16x16x32_bf16 v[68:71], v[170:173], v[218:221], v[68:71]
	s_barrier
	s_add_i32 s73, s73, s17
	v_lshl_add_u64 v[204:205], s[60:61], 0, v[2:3]
	s_mov_b32 m0, s73
	ds_read_b128 v[174:177], v208 offset:16384
	ds_read_b128 v[178:181], v208 offset:17408
	ds_read_b128 v[182:185], v208 offset:18432
	ds_read_b128 v[186:189], v208 offset:19456
	ds_read_b128 v[190:193], v208 offset:20480
	ds_read_b128 v[210:213], v208 offset:21504
	ds_read_b128 v[214:217], v208 offset:22528
	ds_read_b128 v[218:221], v208 offset:23552
	global_load_lds_dwordx4 v[204:205], off
	s_add_i32 m0, s73, 0x2000
	s_add_u32 s74, s60, 0x40000
	v_lshl_add_u64 v[206:207], s[60:61], 0, v[160:161]
	s_addc_u32 s75, s61, 0
	s_add_i32 s73, s76, s17
	global_load_lds_dwordx4 v[206:207], off
	v_lshl_add_u64 v[222:223], s[74:75], 0, v[2:3]
	s_mov_b32 m0, s73
	v_lshl_add_u64 v[224:225], s[62:63], 0, v[162:163]
	global_load_lds_dwordx4 v[222:223], off
	v_lshl_add_u64 v[222:223], s[74:75], 0, v[160:161]
	s_add_i32 m0, s73, 0x2000
	s_nop 0
	global_load_lds_dwordx4 v[222:223], off
	v_lshl_add_u64 v[222:223], s[62:63], 0, v[164:165]
	s_mov_b32 m0, s18
	s_nop 0
	global_load_lds_dwordx4 v[222:223], off
	s_mov_b32 m0, s19
	s_nop 0
	global_load_lds_dwordx4 v[224:225], off
	s_cmp_eq_u32 s72, 0
	s_cbranch_scc1 .Lpg8skip7
	s_waitcnt vmcnt(8)
.Lpg8skip7:
	s_waitcnt lgkmcnt(0)
	s_barrier
	s_waitcnt lgkmcnt(0)
	v_mfma_f32_16x16x32_bf16 v[64:67], v[124:127], v[174:177], v[64:67]
	v_mfma_f32_16x16x32_bf16 v[60:63], v[132:135], v[174:177], v[60:63]
	v_mfma_f32_16x16x32_bf16 v[48:51], v[124:127], v[182:185], v[48:51]
	v_mfma_f32_16x16x32_bf16 v[44:47], v[132:135], v[182:185], v[44:47]
	v_mfma_f32_16x16x32_bf16 v[32:35], v[124:127], v[190:193], v[32:35]
	v_mfma_f32_16x16x32_bf16 v[28:31], v[132:135], v[190:193], v[28:31]
	v_mfma_f32_16x16x32_bf16 v[16:19], v[124:127], v[214:217], v[16:19]
	v_mfma_f32_16x16x32_bf16 v[12:15], v[132:135], v[214:217], v[12:15]
	v_mfma_f32_16x16x32_bf16 v[64:67], v[128:131], v[178:181], v[64:67]
	v_mfma_f32_16x16x32_bf16 v[60:63], v[136:139], v[178:181], v[60:63]
	v_mfma_f32_16x16x32_bf16 v[48:51], v[128:131], v[186:189], v[48:51]
	v_mfma_f32_16x16x32_bf16 v[44:47], v[136:139], v[186:189], v[44:47]
	v_mfma_f32_16x16x32_bf16 v[32:35], v[128:131], v[210:213], v[32:35]
	v_mfma_f32_16x16x32_bf16 v[28:31], v[136:139], v[210:213], v[28:31]
	v_mfma_f32_16x16x32_bf16 v[16:19], v[128:131], v[218:221], v[16:19]
	v_mfma_f32_16x16x32_bf16 v[12:15], v[136:139], v[218:221], v[12:15]
	v_mfma_f32_16x16x32_bf16 v[56:59], v[140:143], v[174:177], v[56:59]
	v_mfma_f32_16x16x32_bf16 v[52:55], v[156:159], v[174:177], v[52:55]
	v_mfma_f32_16x16x32_bf16 v[40:43], v[140:143], v[182:185], v[40:43]
	v_mfma_f32_16x16x32_bf16 v[36:39], v[156:159], v[182:185], v[36:39]
	v_mfma_f32_16x16x32_bf16 v[24:27], v[140:143], v[190:193], v[24:27]
	v_mfma_f32_16x16x32_bf16 v[20:23], v[156:159], v[190:193], v[20:23]
	v_mfma_f32_16x16x32_bf16 v[8:11], v[140:143], v[214:217], v[8:11]
	v_mfma_f32_16x16x32_bf16 v[4:7], v[156:159], v[214:217], v[4:7]
	v_mfma_f32_16x16x32_bf16 v[56:59], v[144:147], v[178:181], v[56:59]
	v_mfma_f32_16x16x32_bf16 v[52:55], v[170:173], v[178:181], v[52:55]
	v_mfma_f32_16x16x32_bf16 v[40:43], v[144:147], v[186:189], v[40:43]
	v_mfma_f32_16x16x32_bf16 v[36:39], v[170:173], v[186:189], v[36:39]
	v_mfma_f32_16x16x32_bf16 v[24:27], v[144:147], v[210:213], v[24:27]
	v_mfma_f32_16x16x32_bf16 v[20:23], v[170:173], v[210:213], v[20:23]
	v_mfma_f32_16x16x32_bf16 v[8:11], v[144:147], v[218:221], v[8:11]
	v_mfma_f32_16x16x32_bf16 v[4:7], v[170:173], v[218:221], v[4:7]
	s_barrier
; #define PG8_STAGE(bufoff, gbase, voff) do { _Pragma("unroll") for (int _i = 0; _i < 2; ++_i) \
;         __builtin_amdgcn_global_load_lds((const unsigned*)((const char*)(gbase) + (voff)[_i]), (PG8_LAS unsigned*)(lds + (bufoff) + ldsw + _i * 8192), 16, 0, 0); } while (0)
; #define PG8_LDA(dst, b, h) do { _Pragma("unroll") for (int m = 0; m < 4; ++m) _Pragma("unroll") for (int k = 0; k < 2; ++k) dst[m][k] = *(const PG8_LAS bf16x8*)(lds + PG8_SA(b, h) + aoff + m * 2048 + k * 1024); } while (0)
; #define PG8_LDB(dst, b, h) do { _Pragma("unroll") for (int n = 0; n < 2; ++n) _Pragma("unroll") for (int k = 0; k < 2; ++k) dst[n][k] = *(const PG8_LAS bf16x8*)(lds + PG8_SB(b, h) + boff + n * 2048 + k * 1024); } while (0)
; #define PG8_WAIT_V(n) asm volatile("s_waitcnt vmcnt(" #n ")" ::: "memory")
; #define PG8_WAIT_L(n) asm volatile("s_waitcnt lgkmcnt(" #n ")" ::: "memory")
; #define PG8_BAR __builtin_amdgcn_s_barrier()
; #define PG8_SCHED __builtin_amdgcn_sched_barrier(0)
; template <class Epi, class Sched, bool ALIGN_EPI = false, bool SP2 = false, bool FP8 = false, bool ABLK = false>
; __device__ __forceinline__ void gemm_phase(PG8_LAS unsigned char* lds, const Gemm g, const Sched& S, const Epi& E) {
;     ...
;             PG8_LDB(B0, 1, 0); PG8_LDB(B1, 1, 1); PG8_SCHED; PG8_LDA(At, 1, 0); PG8_STAGE(PG8_SA(0, 1), a2 + hstepA, voffA);
;             PG8_WAIT_V(8); PG8_WAIT_L(0); PG8_BAR; PG8_MMA(0, 0, At, B0); PG8_MMA(0, 1, At, B1); PG8_BAR; PG8_SCHED;
	s_add_i32 s73, 0, 0x18000
	s_add_i32 s74, 0, 0x1c000
	v_add_u32_e32 v136, s73, v195
	v_add_u32_e32 v170, s74, v195
	ds_read_b128 v[124:127], v136
	ds_read_b128 v[128:131], v136 offset:1024
	ds_read_b128 v[132:135], v136 offset:2048
	ds_read_b128 v[136:139], v136 offset:3072
	ds_read_b128 v[140:143], v170
	ds_read_b128 v[144:147], v170 offset:1024
	ds_read_b128 v[156:159], v170 offset:2048
	ds_read_b128 v[170:173], v170 offset:3072
	s_add_u32 s62, s62, 0x40000
	s_addc_u32 s63, s63, 0
	s_mov_b32 m0, s20
	v_lshl_add_u64 v[228:229], s[62:63], 0, v[164:165]
	ds_read_b128 v[174:177], v208 offset:32768
	ds_read_b128 v[178:181], v208 offset:33792
	ds_read_b128 v[182:185], v208 offset:34816
	ds_read_b128 v[186:189], v208 offset:35840
	ds_read_b128 v[190:193], v208 offset:36864
	ds_read_b128 v[210:213], v208 offset:37888
	ds_read_b128 v[214:217], v208 offset:38912
	ds_read_b128 v[218:221], v208 offset:39936
	global_load_lds_dwordx4 v[228:229], off
	v_lshl_add_u64 v[228:229], s[62:63], 0, v[162:163]
	s_mov_b32 m0, s21
	s_nop 0
	global_load_lds_dwordx4 v[228:229], off
	s_waitcnt vmcnt(8)
	s_waitcnt lgkmcnt(0)
	s_barrier
	s_waitcnt lgkmcnt(0)
	v_mfma_f32_16x16x32_bf16 v[152:155], v[124:127], v[174:177], v[152:155]
	v_mfma_f32_16x16x32_bf16 v[148:151], v[132:135], v[174:177], v[148:151]
	v_mfma_f32_16x16x32_bf16 v[112:115], v[124:127], v[182:185], v[112:115]
	v_mfma_f32_16x16x32_bf16 v[108:111], v[132:135], v[182:185], v[108:111]
	v_mfma_f32_16x16x32_bf16 v[96:99], v[124:127], v[190:193], v[96:99]
	v_mfma_f32_16x16x32_bf16 v[92:95], v[132:135], v[190:193], v[92:95]
	v_mfma_f32_16x16x32_bf16 v[80:83], v[124:127], v[214:217], v[80:83]
	v_mfma_f32_16x16x32_bf16 v[76:79], v[132:135], v[214:217], v[76:79]
	v_mfma_f32_16x16x32_bf16 v[152:155], v[128:131], v[178:181], v[152:155]
	v_mfma_f32_16x16x32_bf16 v[148:151], v[136:139], v[178:181], v[148:151]
	v_mfma_f32_16x16x32_bf16 v[112:115], v[128:131], v[186:189], v[112:115]
	v_mfma_f32_16x16x32_bf16 v[108:111], v[136:139], v[186:189], v[108:111]
	v_mfma_f32_16x16x32_bf16 v[96:99], v[128:131], v[210:213], v[96:99]
	v_mfma_f32_16x16x32_bf16 v[92:95], v[136:139], v[210:213], v[92:95]
	v_mfma_f32_16x16x32_bf16 v[80:83], v[128:131], v[218:221], v[80:83]
	v_mfma_f32_16x16x32_bf16 v[76:79], v[136:139], v[218:221], v[76:79]
	v_mfma_f32_16x16x32_bf16 v[120:123], v[140:143], v[174:177], v[120:123]
	v_mfma_f32_16x16x32_bf16 v[116:119], v[156:159], v[174:177], v[116:119]
	v_mfma_f32_16x16x32_bf16 v[104:107], v[140:143], v[182:185], v[104:107]
	v_mfma_f32_16x16x32_bf16 v[100:103], v[156:159], v[182:185], v[100:103]
	v_mfma_f32_16x16x32_bf16 v[88:91], v[140:143], v[190:193], v[88:91]
	v_mfma_f32_16x16x32_bf16 v[84:87], v[156:159], v[190:193], v[84:87]
	v_mfma_f32_16x16x32_bf16 v[72:75], v[140:143], v[214:217], v[72:75]
	v_mfma_f32_16x16x32_bf16 v[68:71], v[156:159], v[214:217], v[68:71]
	v_mfma_f32_16x16x32_bf16 v[120:123], v[144:147], v[178:181], v[120:123]
	v_mfma_f32_16x16x32_bf16 v[116:119], v[170:173], v[178:181], v[116:119]
	v_mfma_f32_16x16x32_bf16 v[104:107], v[144:147], v[186:189], v[104:107]
	v_mfma_f32_16x16x32_bf16 v[100:103], v[170:173], v[186:189], v[100:103]
	v_mfma_f32_16x16x32_bf16 v[88:91], v[144:147], v[210:213], v[88:91]
	v_mfma_f32_16x16x32_bf16 v[84:87], v[170:173], v[210:213], v[84:87]
	v_mfma_f32_16x16x32_bf16 v[72:75], v[144:147], v[218:221], v[72:75]
	v_mfma_f32_16x16x32_bf16 v[68:71], v[170:173], v[218:221], v[68:71]
	s_barrier
; #define PG8_STAGE(bufoff, gbase, voff) do { _Pragma("unroll") for (int _i = 0; _i < 2; ++_i) \
;         __builtin_amdgcn_global_load_lds((const unsigned*)((const char*)(gbase) + (voff)[_i]), (PG8_LAS unsigned*)(lds + (bufoff) + ldsw + _i * 8192), 16, 0, 0); } while (0)
; #define PG8_LDA(dst, b, h) do { _Pragma("unroll") for (int m = 0; m < 4; ++m) _Pragma("unroll") for (int k = 0; k < 2; ++k) dst[m][k] = *(const PG8_LAS bf16x8*)(lds + PG8_SA(b, h) + aoff + m * 2048 + k * 1024); } while (0)
; #define PG8_WAIT_V(n) asm volatile("s_waitcnt vmcnt(" #n ")" ::: "memory")
; #define PG8_WAIT_L(n) asm volatile("s_waitcnt lgkmcnt(" #n ")" ::: "memory")
; #define PG8_BAR __builtin_amdgcn_s_barrier()
; #define PG8_SCHED __builtin_amdgcn_sched_barrier(0)
; template <class Epi, class Sched, bool ALIGN_EPI = false, bool SP2 = false, bool FP8 = false, bool ABLK = false>
; __device__ __forceinline__ void gemm_phase(PG8_LAS unsigned char* lds, const Gemm g, const Sched& S, const Epi& E) {
;     ...
;             PG8_LDA(At, 1, 1); PG8_STAGE(PG8_SB(1, 0), b3, voffB); PG8_STAGE(PG8_SB(1, 1), b3 + hstep, voffB); PG8_STAGE(PG8_SA(1, 0), a3, voffA);
;             PG8_WAIT_V(8); PG8_WAIT_L(0); PG8_BAR; PG8_MMA(1, 0, At, B0); PG8_MMA(1, 1, At, B1); PG8_BAR; PG8_SCHED;
;     ...
;         if constexpr (SP2) PG8_WAIT_V(0);
;         if constexpr (FP8) asm volatile("s_nop 15\n\ts_nop 15" ::: "memory");
;         if constexpr (ALIGN_EPI) { if (wr == 0) PG8_BAR; }
	s_add_i32 s62, s73, s17
	v_lshl_add_u64 v[204:205], v[204:205], 0, s[34:35]
	s_mov_b32 m0, s62
	ds_read_b128 v[174:177], v208 offset:49152
	ds_read_b128 v[178:181], v208 offset:50176
	ds_read_b128 v[182:185], v208 offset:51200
	ds_read_b128 v[186:189], v208 offset:52224
	ds_read_b128 v[190:193], v208 offset:53248
	ds_read_b128 v[210:213], v208 offset:54272
	ds_read_b128 v[214:217], v208 offset:55296
	ds_read_b128 v[218:221], v208 offset:56320
	global_load_lds_dwordx4 v[204:205], off
	s_add_i32 m0, s62, 0x2000
	s_add_u32 s60, s60, 0x40080
	v_lshl_add_u64 v[204:205], v[206:207], 0, s[34:35]
	s_addc_u32 s61, s61, 0
	s_add_i32 s62, s74, s17
	global_load_lds_dwordx4 v[204:205], off
	v_lshl_add_u64 v[204:205], s[60:61], 0, v[2:3]
	s_mov_b32 m0, s62
	s_nop 0
	global_load_lds_dwordx4 v[204:205], off
	v_lshl_add_u64 v[204:205], s[60:61], 0, v[160:161]
	s_add_i32 m0, s62, 0x2000
	s_nop 0
	global_load_lds_dwordx4 v[204:205], off
	v_lshl_add_u64 v[204:205], v[222:223], 0, s[34:35]
	s_mov_b32 m0, s65
	s_nop 0
	global_load_lds_dwordx4 v[204:205], off
	v_lshl_add_u64 v[204:205], v[224:225], 0, s[34:35]
	s_mov_b32 m0, s66
	s_nop 0
	global_load_lds_dwordx4 v[204:205], off
	s_waitcnt vmcnt(8)
	s_waitcnt lgkmcnt(0)
	s_barrier
	s_waitcnt lgkmcnt(0)
	v_mfma_f32_16x16x32_bf16 v[64:67], v[124:127], v[174:177], v[64:67]
	v_mfma_f32_16x16x32_bf16 v[60:63], v[132:135], v[174:177], v[60:63]
	v_mfma_f32_16x16x32_bf16 v[48:51], v[124:127], v[182:185], v[48:51]
	v_mfma_f32_16x16x32_bf16 v[44:47], v[132:135], v[182:185], v[44:47]
	v_mfma_f32_16x16x32_bf16 v[32:35], v[124:127], v[190:193], v[32:35]
	v_mfma_f32_16x16x32_bf16 v[28:31], v[132:135], v[190:193], v[28:31]
	v_mfma_f32_16x16x32_bf16 v[16:19], v[124:127], v[214:217], v[16:19]
	v_mfma_f32_16x16x32_bf16 v[12:15], v[132:135], v[214:217], v[12:15]
	v_mfma_f32_16x16x32_bf16 v[64:67], v[128:131], v[178:181], v[64:67]
	v_mfma_f32_16x16x32_bf16 v[60:63], v[136:139], v[178:181], v[60:63]
	v_mfma_f32_16x16x32_bf16 v[48:51], v[128:131], v[186:189], v[48:51]
	v_mfma_f32_16x16x32_bf16 v[44:47], v[136:139], v[186:189], v[44:47]
	v_mfma_f32_16x16x32_bf16 v[32:35], v[128:131], v[210:213], v[32:35]
	v_mfma_f32_16x16x32_bf16 v[28:31], v[136:139], v[210:213], v[28:31]
	v_mfma_f32_16x16x32_bf16 v[16:19], v[128:131], v[218:221], v[16:19]
	v_mfma_f32_16x16x32_bf16 v[12:15], v[136:139], v[218:221], v[12:15]
	v_mfma_f32_16x16x32_bf16 v[56:59], v[140:143], v[174:177], v[56:59]
	v_mfma_f32_16x16x32_bf16 v[52:55], v[156:159], v[174:177], v[52:55]
	v_mfma_f32_16x16x32_bf16 v[40:43], v[140:143], v[182:185], v[40:43]
	v_mfma_f32_16x16x32_bf16 v[36:39], v[156:159], v[182:185], v[36:39]
	v_mfma_f32_16x16x32_bf16 v[24:27], v[140:143], v[190:193], v[24:27]
	v_mfma_f32_16x16x32_bf16 v[20:23], v[156:159], v[190:193], v[20:23]
	v_mfma_f32_16x16x32_bf16 v[8:11], v[140:143], v[214:217], v[8:11]
	v_mfma_f32_16x16x32_bf16 v[4:7], v[156:159], v[214:217], v[4:7]
	v_mfma_f32_16x16x32_bf16 v[56:59], v[144:147], v[178:181], v[56:59]
	v_mfma_f32_16x16x32_bf16 v[52:55], v[170:173], v[178:181], v[52:55]
	v_mfma_f32_16x16x32_bf16 v[40:43], v[144:147], v[186:189], v[40:43]
	v_mfma_f32_16x16x32_bf16 v[36:39], v[170:173], v[186:189], v[36:39]
	v_mfma_f32_16x16x32_bf16 v[24:27], v[144:147], v[210:213], v[24:27]
	v_mfma_f32_16x16x32_bf16 v[20:23], v[170:173], v[210:213], v[20:23]
	v_mfma_f32_16x16x32_bf16 v[8:11], v[144:147], v[218:221], v[8:11]
	v_mfma_f32_16x16x32_bf16 v[4:7], v[170:173], v[218:221], v[4:7]
	s_barrier
	s_add_u32 s42, s42, 0x100
	s_addc_u32 s43, s43, 0
	s_add_u32 s70, s70, 0x100
	s_addc_u32 s71, s71, 0
	s_cmp_gt_u32 s72, 13
	s_mov_b32 s60, s72
	s_cbranch_scc0 .LBB0_1411
	s_waitcnt vmcnt(0)
	s_and_b64 vcc, exec, s[50:51]
	s_cbranch_vccz .LBB0_1414
	s_barrier

; #define PG8_STAGE(bufoff, gbase, voff) do { _Pragma("unroll") for (int _i = 0; _i < 2; ++_i) \
;         __builtin_amdgcn_global_load_lds((const unsigned*)((const char*)(gbase) + (voff)[_i]), (PG8_LAS unsigned*)(lds + (bufoff) + ldsw + _i * 8192), 16, 0, 0); } while (0)
; #define PG8_LDA(dst, b, h) do { _Pragma("unroll") for (int m = 0; m < 4; ++m) _Pragma("unroll") for (int k = 0; k < 2; ++k) dst[m][k] = *(const PG8_LAS bf16x8*)(lds + PG8_SA(b, h) + aoff + m * 2048 + k * 1024); } while (0)
; #define PG8_LDB(dst, b, h) do { _Pragma("unroll") for (int n = 0; n < 2; ++n) _Pragma("unroll") for (int k = 0; k < 2; ++k) dst[n][k] = *(const PG8_LAS bf16x8*)(lds + PG8_SB(b, h) + boff + n * 2048 + k * 1024); } while (0)
; #define PG8_WAIT_V(n) asm volatile("s_waitcnt vmcnt(" #n ")" ::: "memory")
; #define PG8_WAIT_V8_UNLESS_FIRST(t) asm volatile("s_cmp_eq_u32 %0, 0\n\ts_cbranch_scc1 .Lpg8skip%=\n\ts_waitcnt vmcnt(8)\n.Lpg8skip%=:" :: "s"(t) : "scc", "memory")
; #define PG8_WAIT_L(n) asm volatile("s_waitcnt lgkmcnt(" #n ")" ::: "memory")
; #define PG8_BAR __builtin_amdgcn_s_barrier()
; #define PG8_SCHED __builtin_amdgcn_sched_barrier(0)
; template <class Epi, class Sched, bool ALIGN_EPI = false, bool SP2 = false, bool FP8 = false, bool ABLK = false>
; __device__ __forceinline__ void gemm_phase(PG8_LAS unsigned char* lds, const Gemm g, const Sched& S, const Epi& E) {
;     ...
;             PG8_WAIT_V8_UNLESS_FIRST(t); PG8_WAIT_L(0); PG8_BAR; PG8_MMA(0, 0, At, B0); PG8_MMA(0, 1, At, B1); PG8_BAR; PG8_SCHED;
;             PG8_LDA(At, 0, 1); PG8_STAGE(PG8_SB(0, 0), b2, voffB); PG8_STAGE(PG8_SB(0, 1), b2 + hstep, voffB); PG8_STAGE(PG8_SA(0, 0), a2, voffA);
;             PG8_WAIT_V8_UNLESS_FIRST(t); PG8_WAIT_L(0); PG8_BAR; PG8_MMA(1, 0, At, B0); PG8_MMA(1, 1, At, B1); PG8_BAR; PG8_SCHED;
;             PG8_LDB(B0, 1, 0); PG8_LDB(B1, 1, 1); PG8_SCHED; PG8_LDA(At, 1, 0); PG8_STAGE(PG8_SA(0, 1), a2 + hstepA, voffA);
;             PG8_WAIT_V(8); PG8_WAIT_L(0); PG8_BAR; PG8_MMA(0, 0, At, B0); PG8_MMA(0, 1, At, B1); PG8_BAR; PG8_SCHED;
.Lpg8skip8:
	s_waitcnt lgkmcnt(0)
	s_barrier
	s_waitcnt lgkmcnt(0)
	v_mfma_scale_f32_16x16x128_f8f6f4 v[160:163], v[28:35], v[174:181], v[160:163], v245, v245 op_sel_hi:[0,0,0]
	v_mfma_scale_f32_16x16x128_f8f6f4 v[156:159], v[20:27], v[174:181], v[156:159], v245, v245 op_sel_hi:[0,0,0]
	v_mfma_scale_f32_16x16x128_f8f6f4 v[144:147], v[28:35], v[186:193], v[144:147], v245, v245 op_sel_hi:[0,0,0]
	v_mfma_scale_f32_16x16x128_f8f6f4 v[140:143], v[20:27], v[186:193], v[140:143], v245, v245 op_sel_hi:[0,0,0]
	v_mfma_scale_f32_16x16x128_f8f6f4 v[128:131], v[28:35], v[208:215], v[128:131], v245, v245 op_sel_hi:[0,0,0]
	v_mfma_scale_f32_16x16x128_f8f6f4 v[124:127], v[20:27], v[208:215], v[124:127], v245, v245 op_sel_hi:[0,0,0]
	v_mfma_scale_f32_16x16x128_f8f6f4 v[112:115], v[28:35], v[216:223], v[112:115], v245, v245 op_sel_hi:[0,0,0]
	v_mfma_scale_f32_16x16x128_f8f6f4 v[108:111], v[20:27], v[216:223], v[108:111], v245, v245 op_sel_hi:[0,0,0]
	v_mfma_scale_f32_16x16x128_f8f6f4 v[152:155], v[12:19], v[174:181], v[152:155], v245, v245 op_sel_hi:[0,0,0]
	v_mfma_scale_f32_16x16x128_f8f6f4 v[148:151], v[4:11], v[174:181], v[148:151], v245, v245 op_sel_hi:[0,0,0]
	v_mfma_scale_f32_16x16x128_f8f6f4 v[136:139], v[12:19], v[186:193], v[136:139], v245, v245 op_sel_hi:[0,0,0]
	v_mfma_scale_f32_16x16x128_f8f6f4 v[132:135], v[4:11], v[186:193], v[132:135], v245, v245 op_sel_hi:[0,0,0]
	v_mfma_scale_f32_16x16x128_f8f6f4 v[120:123], v[12:19], v[208:215], v[120:123], v245, v245 op_sel_hi:[0,0,0]
	v_mfma_scale_f32_16x16x128_f8f6f4 v[116:119], v[4:11], v[208:215], v[116:119], v245, v245 op_sel_hi:[0,0,0]
	v_mfma_scale_f32_16x16x128_f8f6f4 v[104:107], v[12:19], v[216:223], v[104:107], v245, v245 op_sel_hi:[0,0,0]
	v_mfma_scale_f32_16x16x128_f8f6f4 v[100:103], v[4:11], v[216:223], v[100:103], v245, v245 op_sel_hi:[0,0,0]
	s_barrier
	s_add_i32 s70, s70, s17
	v_lshl_add_u64 v[174:175], s[58:59], 0, v[2:3]
	s_mov_b32 m0, s70
	ds_read_b128 v[186:189], v184 offset:16384
	ds_read_b128 v[190:193], v184 offset:17408
	ds_read_b128 v[208:211], v184 offset:18432
	ds_read_b128 v[212:215], v184 offset:19456
	ds_read_b128 v[216:219], v184 offset:20480
	ds_read_b128 v[220:223], v184 offset:21504
	ds_read_b128 v[228:231], v184 offset:22528
	ds_read_b128 v[232:235], v184 offset:23552
	global_load_lds_dwordx4 v[174:175], off
	s_add_i32 m0, s70, 0x2000
	s_add_u32 s72, s58, 0x20000
	v_lshl_add_u64 v[176:177], s[58:59], 0, v[164:165]
	s_addc_u32 s73, s59, 0
	s_add_i32 s70, s71, s17
	global_load_lds_dwordx4 v[176:177], off
	v_lshl_add_u64 v[178:179], s[72:73], 0, v[2:3]
	s_mov_b32 m0, s70
	v_lshl_add_u64 v[180:181], s[60:61], 0, v[166:167]
	global_load_lds_dwordx4 v[178:179], off
	v_lshl_add_u64 v[178:179], s[72:73], 0, v[164:165]
	s_add_i32 m0, s70, 0x2000
	s_nop 0
	global_load_lds_dwordx4 v[178:179], off
	v_lshl_add_u64 v[178:179], s[60:61], 0, v[168:169]
	s_mov_b32 m0, s18
	s_nop 0
	global_load_lds_dwordx4 v[178:179], off
	s_mov_b32 m0, s19
	s_nop 0
	global_load_lds_dwordx4 v[180:181], off
	s_cmp_eq_u32 s69, 0
	s_cbranch_scc1 .Lpg8skip9
	s_waitcnt vmcnt(8)
.Lpg8skip9:
	s_waitcnt lgkmcnt(0)
	s_barrier
	s_waitcnt lgkmcnt(0)
	v_mfma_scale_f32_16x16x128_f8f6f4 v[96:99], v[28:35], v[186:193], v[96:99], v245, v245 op_sel_hi:[0,0,0]
	v_mfma_scale_f32_16x16x128_f8f6f4 v[92:95], v[20:27], v[186:193], v[92:95], v245, v245 op_sel_hi:[0,0,0]
	v_mfma_scale_f32_16x16x128_f8f6f4 v[80:83], v[28:35], v[208:215], v[80:83], v245, v245 op_sel_hi:[0,0,0]
	v_mfma_scale_f32_16x16x128_f8f6f4 v[76:79], v[20:27], v[208:215], v[76:79], v245, v245 op_sel_hi:[0,0,0]
	v_mfma_scale_f32_16x16x128_f8f6f4 v[64:67], v[28:35], v[216:223], v[64:67], v245, v245 op_sel_hi:[0,0,0]
	v_mfma_scale_f32_16x16x128_f8f6f4 v[60:63], v[20:27], v[216:223], v[60:63], v245, v245 op_sel_hi:[0,0,0]
	v_mfma_scale_f32_16x16x128_f8f6f4 v[48:51], v[28:35], v[228:235], v[48:51], v245, v245 op_sel_hi:[0,0,0]
	v_mfma_scale_f32_16x16x128_f8f6f4 v[44:47], v[20:27], v[228:235], v[44:47], v245, v245 op_sel_hi:[0,0,0]
	v_mfma_scale_f32_16x16x128_f8f6f4 v[88:91], v[12:19], v[186:193], v[88:91], v245, v245 op_sel_hi:[0,0,0]
	v_mfma_scale_f32_16x16x128_f8f6f4 v[84:87], v[4:11], v[186:193], v[84:87], v245, v245 op_sel_hi:[0,0,0]
	v_mfma_scale_f32_16x16x128_f8f6f4 v[72:75], v[12:19], v[208:215], v[72:75], v245, v245 op_sel_hi:[0,0,0]
	v_mfma_scale_f32_16x16x128_f8f6f4 v[68:71], v[4:11], v[208:215], v[68:71], v245, v245 op_sel_hi:[0,0,0]
	v_mfma_scale_f32_16x16x128_f8f6f4 v[56:59], v[12:19], v[216:223], v[56:59], v245, v245 op_sel_hi:[0,0,0]
	v_mfma_scale_f32_16x16x128_f8f6f4 v[52:55], v[4:11], v[216:223], v[52:55], v245, v245 op_sel_hi:[0,0,0]
	v_mfma_scale_f32_16x16x128_f8f6f4 v[40:43], v[12:19], v[228:235], v[40:43], v245, v245 op_sel_hi:[0,0,0]
	v_mfma_scale_f32_16x16x128_f8f6f4 v[36:39], v[4:11], v[228:235], v[36:39], v245, v245 op_sel_hi:[0,0,0]
	s_barrier
	s_add_i32 s70, 0, 0x18000
	s_add_i32 s71, 0, 0x1c000
	v_add_u32_e32 v16, s70, v183
	v_add_u32_e32 v32, s71, v183
	ds_read_b128 v[4:7], v16
	ds_read_b128 v[8:11], v16 offset:1024
	ds_read_b128 v[12:15], v16 offset:2048
	ds_read_b128 v[16:19], v16 offset:3072
	ds_read_b128 v[20:23], v32
	ds_read_b128 v[24:27], v32 offset:1024
	ds_read_b128 v[28:31], v32 offset:2048
	ds_read_b128 v[32:35], v32 offset:3072
	s_add_u32 s60, s60, 0x20000
	s_addc_u32 s61, s61, 0
	s_mov_b32 m0, s20
	v_lshl_add_u64 v[194:195], s[60:61], 0, v[168:169]
	ds_read_b128 v[186:189], v184 offset:32768
	ds_read_b128 v[190:193], v184 offset:33792
	ds_read_b128 v[208:211], v184 offset:34816
	ds_read_b128 v[212:215], v184 offset:35840
	ds_read_b128 v[216:219], v184 offset:36864
	ds_read_b128 v[220:223], v184 offset:37888
	ds_read_b128 v[228:231], v184 offset:38912
	ds_read_b128 v[232:235], v184 offset:39936
	global_load_lds_dwordx4 v[194:195], off
	v_lshl_add_u64 v[194:195], s[60:61], 0, v[166:167]
	s_mov_b32 m0, s21
	s_nop 0
	global_load_lds_dwordx4 v[194:195], off
	s_waitcnt vmcnt(8)
	s_waitcnt lgkmcnt(0)
	s_barrier
; #define PG8_STAGE(bufoff, gbase, voff) do { _Pragma("unroll") for (int _i = 0; _i < 2; ++_i) \
;         __builtin_amdgcn_global_load_lds((const unsigned*)((const char*)(gbase) + (voff)[_i]), (PG8_LAS unsigned*)(lds + (bufoff) + ldsw + _i * 8192), 16, 0, 0); } while (0)
; #define PG8_LDA(dst, b, h) do { _Pragma("unroll") for (int m = 0; m < 4; ++m) _Pragma("unroll") for (int k = 0; k < 2; ++k) dst[m][k] = *(const PG8_LAS bf16x8*)(lds + PG8_SA(b, h) + aoff + m * 2048 + k * 1024); } while (0)
; #define PG8_WAIT_V(n) asm volatile("s_waitcnt vmcnt(" #n ")" ::: "memory")
; #define PG8_WAIT_L(n) asm volatile("s_waitcnt lgkmcnt(" #n ")" ::: "memory")
; #define PG8_BAR __builtin_amdgcn_s_barrier()
; #define PG8_SCHED __builtin_amdgcn_sched_barrier(0)
; template <class Epi, class Sched, bool ALIGN_EPI = false, bool SP2 = false, bool FP8 = false, bool ABLK = false>
; __device__ __forceinline__ void gemm_phase(PG8_LAS unsigned char* lds, const Gemm g, const Sched& S, const Epi& E) {
;     ...
;             PG8_WAIT_V(8); PG8_WAIT_L(0); PG8_BAR; PG8_MMA(0, 0, At, B0); PG8_MMA(0, 1, At, B1); PG8_BAR; PG8_SCHED;
;             PG8_LDA(At, 1, 1); PG8_STAGE(PG8_SB(1, 0), b3, voffB); PG8_STAGE(PG8_SB(1, 1), b3 + hstep, voffB); PG8_STAGE(PG8_SA(1, 0), a3, voffA);
;             PG8_WAIT_V(8); PG8_WAIT_L(0); PG8_BAR; PG8_MMA(1, 0, At, B0); PG8_MMA(1, 1, At, B1); PG8_BAR; PG8_SCHED;
;     ...
;         if constexpr (SP2) PG8_WAIT_V(0);
;         if constexpr (FP8) asm volatile("s_nop 15\n\ts_nop 15" ::: "memory");
;         if constexpr (ALIGN_EPI) { if (wr == 0) PG8_BAR; }
	s_waitcnt lgkmcnt(0)
	v_mfma_scale_f32_16x16x128_f8f6f4 v[160:163], v[4:11], v[186:193], v[160:163], v245, v245 op_sel_hi:[0,0,0]
	v_mfma_scale_f32_16x16x128_f8f6f4 v[156:159], v[12:19], v[186:193], v[156:159], v245, v245 op_sel_hi:[0,0,0]
	v_mfma_scale_f32_16x16x128_f8f6f4 v[144:147], v[4:11], v[208:215], v[144:147], v245, v245 op_sel_hi:[0,0,0]
	v_mfma_scale_f32_16x16x128_f8f6f4 v[140:143], v[12:19], v[208:215], v[140:143], v245, v245 op_sel_hi:[0,0,0]
	v_mfma_scale_f32_16x16x128_f8f6f4 v[128:131], v[4:11], v[216:223], v[128:131], v245, v245 op_sel_hi:[0,0,0]
	v_mfma_scale_f32_16x16x128_f8f6f4 v[124:127], v[12:19], v[216:223], v[124:127], v245, v245 op_sel_hi:[0,0,0]
	v_mfma_scale_f32_16x16x128_f8f6f4 v[112:115], v[4:11], v[228:235], v[112:115], v245, v245 op_sel_hi:[0,0,0]
	v_mfma_scale_f32_16x16x128_f8f6f4 v[108:111], v[12:19], v[228:235], v[108:111], v245, v245 op_sel_hi:[0,0,0]
	v_mfma_scale_f32_16x16x128_f8f6f4 v[152:155], v[20:27], v[186:193], v[152:155], v245, v245 op_sel_hi:[0,0,0]
	v_mfma_scale_f32_16x16x128_f8f6f4 v[148:151], v[28:35], v[186:193], v[148:151], v245, v245 op_sel_hi:[0,0,0]
	v_mfma_scale_f32_16x16x128_f8f6f4 v[136:139], v[20:27], v[208:215], v[136:139], v245, v245 op_sel_hi:[0,0,0]
	v_mfma_scale_f32_16x16x128_f8f6f4 v[132:135], v[28:35], v[208:215], v[132:135], v245, v245 op_sel_hi:[0,0,0]
	v_mfma_scale_f32_16x16x128_f8f6f4 v[120:123], v[20:27], v[216:223], v[120:123], v245, v245 op_sel_hi:[0,0,0]
	v_mfma_scale_f32_16x16x128_f8f6f4 v[116:119], v[28:35], v[216:223], v[116:119], v245, v245 op_sel_hi:[0,0,0]
	v_mfma_scale_f32_16x16x128_f8f6f4 v[104:107], v[20:27], v[228:235], v[104:107], v245, v245 op_sel_hi:[0,0,0]
	v_mfma_scale_f32_16x16x128_f8f6f4 v[100:103], v[28:35], v[228:235], v[100:103], v245, v245 op_sel_hi:[0,0,0]
	s_barrier
	s_add_i32 s60, s70, s17
	v_lshl_add_u64 v[174:175], v[174:175], 0, s[34:35]
	s_mov_b32 m0, s60
	ds_read_b128 v[186:189], v184 offset:49152
	ds_read_b128 v[190:193], v184 offset:50176
	ds_read_b128 v[208:211], v184 offset:51200
	ds_read_b128 v[212:215], v184 offset:52224
	ds_read_b128 v[216:219], v184 offset:53248
	ds_read_b128 v[220:223], v184 offset:54272
	ds_read_b128 v[228:231], v184 offset:55296
	ds_read_b128 v[232:235], v184 offset:56320
	global_load_lds_dwordx4 v[174:175], off
	s_add_i32 m0, s60, 0x2000
	s_add_u32 s58, s58, 0x20080
	v_lshl_add_u64 v[174:175], v[176:177], 0, s[34:35]
	s_addc_u32 s59, s59, 0
	s_add_i32 s60, s71, s17
	global_load_lds_dwordx4 v[174:175], off
	v_lshl_add_u64 v[174:175], s[58:59], 0, v[2:3]
	s_mov_b32 m0, s60
	s_nop 0
	global_load_lds_dwordx4 v[174:175], off
	v_lshl_add_u64 v[174:175], s[58:59], 0, v[164:165]
	s_add_i32 m0, s60, 0x2000
	s_nop 0
	global_load_lds_dwordx4 v[174:175], off
	v_lshl_add_u64 v[174:175], v[178:179], 0, s[34:35]
	s_mov_b32 m0, s62
	s_nop 0
	global_load_lds_dwordx4 v[174:175], off
	v_lshl_add_u64 v[174:175], v[180:181], 0, s[34:35]
	s_mov_b32 m0, s63
	s_nop 0
	global_load_lds_dwordx4 v[174:175], off
	s_waitcnt vmcnt(8)
	s_waitcnt lgkmcnt(0)
	s_barrier
	s_waitcnt lgkmcnt(0)
	v_mfma_scale_f32_16x16x128_f8f6f4 v[96:99], v[4:11], v[186:193], v[96:99], v245, v245 op_sel_hi:[0,0,0]
	v_mfma_scale_f32_16x16x128_f8f6f4 v[92:95], v[12:19], v[186:193], v[92:95], v245, v245 op_sel_hi:[0,0,0]
	v_mfma_scale_f32_16x16x128_f8f6f4 v[80:83], v[4:11], v[208:215], v[80:83], v245, v245 op_sel_hi:[0,0,0]
	v_mfma_scale_f32_16x16x128_f8f6f4 v[76:79], v[12:19], v[208:215], v[76:79], v245, v245 op_sel_hi:[0,0,0]
	v_mfma_scale_f32_16x16x128_f8f6f4 v[64:67], v[4:11], v[216:223], v[64:67], v245, v245 op_sel_hi:[0,0,0]
	v_mfma_scale_f32_16x16x128_f8f6f4 v[60:63], v[12:19], v[216:223], v[60:63], v245, v245 op_sel_hi:[0,0,0]
	v_mfma_scale_f32_16x16x128_f8f6f4 v[48:51], v[4:11], v[228:235], v[48:51], v245, v245 op_sel_hi:[0,0,0]
	v_mfma_scale_f32_16x16x128_f8f6f4 v[44:47], v[12:19], v[228:235], v[44:47], v245, v245 op_sel_hi:[0,0,0]
	v_mfma_scale_f32_16x16x128_f8f6f4 v[88:91], v[20:27], v[186:193], v[88:91], v245, v245 op_sel_hi:[0,0,0]
	v_mfma_scale_f32_16x16x128_f8f6f4 v[84:87], v[28:35], v[186:193], v[84:87], v245, v245 op_sel_hi:[0,0,0]
	v_mfma_scale_f32_16x16x128_f8f6f4 v[72:75], v[20:27], v[208:215], v[72:75], v245, v245 op_sel_hi:[0,0,0]
	v_mfma_scale_f32_16x16x128_f8f6f4 v[68:71], v[28:35], v[208:215], v[68:71], v245, v245 op_sel_hi:[0,0,0]
	v_mfma_scale_f32_16x16x128_f8f6f4 v[56:59], v[20:27], v[216:223], v[56:59], v245, v245 op_sel_hi:[0,0,0]
	v_mfma_scale_f32_16x16x128_f8f6f4 v[52:55], v[28:35], v[216:223], v[52:55], v245, v245 op_sel_hi:[0,0,0]
	v_mfma_scale_f32_16x16x128_f8f6f4 v[40:43], v[20:27], v[228:235], v[40:43], v245, v245 op_sel_hi:[0,0,0]
	v_mfma_scale_f32_16x16x128_f8f6f4 v[36:39], v[28:35], v[228:235], v[36:39], v245, v245 op_sel_hi:[0,0,0]
	s_barrier
	s_add_u32 s56, s56, 0x100
	s_addc_u32 s57, s57, 0
	s_add_u32 s67, s67, 0x100
	s_addc_u32 s68, s68, 0
	s_cmp_gt_u32 s69, 5
	s_mov_b32 s58, s69
	s_cbranch_scc0 .LBB0_1498
	s_waitcnt vmcnt(0)
	s_nop 15
	s_nop 15
	s_and_b64 vcc, exec, s[46:47]
	s_cbranch_vccz .LBB0_1501
	s_barrier

; #define PG8_STAGE(bufoff, gbase, voff) do { _Pragma("unroll") for (int _i = 0; _i < 2; ++_i) \
;         __builtin_amdgcn_global_load_lds((const unsigned*)((const char*)(gbase) + (voff)[_i]), (PG8_LAS unsigned*)(lds + (bufoff) + ldsw + _i * 8192), 16, 0, 0); } while (0)
; #define PG8_LDA(dst, b, h) do { _Pragma("unroll") for (int m = 0; m < 4; ++m) _Pragma("unroll") for (int k = 0; k < 2; ++k) dst[m][k] = *(const PG8_LAS bf16x8*)(lds + PG8_SA(b, h) + aoff + m * 2048 + k * 1024); } while (0)
; #define PG8_LDB(dst, b, h) do { _Pragma("unroll") for (int n = 0; n < 2; ++n) _Pragma("unroll") for (int k = 0; k < 2; ++k) dst[n][k] = *(const PG8_LAS bf16x8*)(lds + PG8_SB(b, h) + boff + n * 2048 + k * 1024); } while (0)
; #define PG8_WAIT_V(n) asm volatile("s_waitcnt vmcnt(" #n ")" ::: "memory")
; #define PG8_WAIT_V8_UNLESS_FIRST(t) asm volatile("s_cmp_eq_u32 %0, 0\n\ts_cbranch_scc1 .Lpg8skip%=\n\ts_waitcnt vmcnt(8)\n.Lpg8skip%=:" :: "s"(t) : "scc", "memory")
; #define PG8_WAIT_L(n) asm volatile("s_waitcnt lgkmcnt(" #n ")" ::: "memory")
; #define PG8_BAR __builtin_amdgcn_s_barrier()
; #define PG8_SCHED __builtin_amdgcn_sched_barrier(0)
; template <class Epi, class Sched, bool ALIGN_EPI = false, bool SP2 = false, bool FP8 = false, bool ABLK = false>
; __device__ __forceinline__ void gemm_phase(PG8_LAS unsigned char* lds, const Gemm g, const Sched& S, const Epi& E) {
;     ...
;             PG8_WAIT_V8_UNLESS_FIRST(t); PG8_WAIT_L(0); PG8_BAR; PG8_MMA(0, 0, At, B0); PG8_MMA(0, 1, At, B1); PG8_BAR; PG8_SCHED;
;             PG8_LDA(At, 0, 1); PG8_STAGE(PG8_SB(0, 0), b2, voffB); PG8_STAGE(PG8_SB(0, 1), b2 + hstep, voffB); PG8_STAGE(PG8_SA(0, 0), a2, voffA);
;             PG8_WAIT_V8_UNLESS_FIRST(t); PG8_WAIT_L(0); PG8_BAR; PG8_MMA(1, 0, At, B0); PG8_MMA(1, 1, At, B1); PG8_BAR; PG8_SCHED;
;             PG8_LDB(B0, 1, 0); PG8_LDB(B1, 1, 1); PG8_SCHED; PG8_LDA(At, 1, 0); PG8_STAGE(PG8_SA(0, 1), a2 + hstepA, voffA);
;             PG8_WAIT_V(8); PG8_WAIT_L(0); PG8_BAR; PG8_MMA(0, 0, At, B0); PG8_MMA(0, 1, At, B1); PG8_BAR; PG8_SCHED;
.Lpg8skip10:
	s_waitcnt lgkmcnt(0)
	s_barrier
	s_waitcnt lgkmcnt(0)
	v_mfma_scale_f32_16x16x128_f8f6f4 v[160:163], v[28:35], v[174:181], v[160:163], v245, v245 op_sel_hi:[0,0,0]
	v_mfma_scale_f32_16x16x128_f8f6f4 v[156:159], v[20:27], v[174:181], v[156:159], v245, v245 op_sel_hi:[0,0,0]
	v_mfma_scale_f32_16x16x128_f8f6f4 v[144:147], v[28:35], v[182:189], v[144:147], v245, v245 op_sel_hi:[0,0,0]
	v_mfma_scale_f32_16x16x128_f8f6f4 v[140:143], v[20:27], v[182:189], v[140:143], v245, v245 op_sel_hi:[0,0,0]
	v_mfma_scale_f32_16x16x128_f8f6f4 v[128:131], v[28:35], v[210:217], v[128:131], v245, v245 op_sel_hi:[0,0,0]
	v_mfma_scale_f32_16x16x128_f8f6f4 v[124:127], v[20:27], v[210:217], v[124:127], v245, v245 op_sel_hi:[0,0,0]
	v_mfma_scale_f32_16x16x128_f8f6f4 v[112:115], v[28:35], v[218:225], v[112:115], v245, v245 op_sel_hi:[0,0,0]
	v_mfma_scale_f32_16x16x128_f8f6f4 v[108:111], v[20:27], v[218:225], v[108:111], v245, v245 op_sel_hi:[0,0,0]
	v_mfma_scale_f32_16x16x128_f8f6f4 v[152:155], v[12:19], v[174:181], v[152:155], v245, v245 op_sel_hi:[0,0,0]
	v_mfma_scale_f32_16x16x128_f8f6f4 v[148:151], v[4:11], v[174:181], v[148:151], v245, v245 op_sel_hi:[0,0,0]
	v_mfma_scale_f32_16x16x128_f8f6f4 v[136:139], v[12:19], v[182:189], v[136:139], v245, v245 op_sel_hi:[0,0,0]
	v_mfma_scale_f32_16x16x128_f8f6f4 v[132:135], v[4:11], v[182:189], v[132:135], v245, v245 op_sel_hi:[0,0,0]
	v_mfma_scale_f32_16x16x128_f8f6f4 v[120:123], v[12:19], v[210:217], v[120:123], v245, v245 op_sel_hi:[0,0,0]
	v_mfma_scale_f32_16x16x128_f8f6f4 v[116:119], v[4:11], v[210:217], v[116:119], v245, v245 op_sel_hi:[0,0,0]
	v_mfma_scale_f32_16x16x128_f8f6f4 v[104:107], v[12:19], v[218:225], v[104:107], v245, v245 op_sel_hi:[0,0,0]
	v_mfma_scale_f32_16x16x128_f8f6f4 v[100:103], v[4:11], v[218:225], v[100:103], v245, v245 op_sel_hi:[0,0,0]
	s_barrier
	s_add_i32 s73, s73, s17
	v_lshl_add_u64 v[174:175], s[60:61], 0, v[2:3]
	s_mov_b32 m0, s73
	ds_read_b128 v[182:185], v208 offset:16384
	ds_read_b128 v[186:189], v208 offset:17408
	ds_read_b128 v[210:213], v208 offset:18432
	ds_read_b128 v[214:217], v208 offset:19456
	ds_read_b128 v[218:221], v208 offset:20480
	ds_read_b128 v[222:225], v208 offset:21504
	ds_read_b128 v[228:231], v208 offset:22528
	ds_read_b128 v[232:235], v208 offset:23552
	global_load_lds_dwordx4 v[174:175], off
	s_add_i32 m0, s73, 0x2000
	s_add_u32 s76, s60, 0x20000
	v_lshl_add_u64 v[176:177], s[60:61], 0, v[164:165]
	s_addc_u32 s77, s61, 0
	s_add_i32 s73, s74, s17
	global_load_lds_dwordx4 v[176:177], off
	v_lshl_add_u64 v[178:179], s[76:77], 0, v[2:3]
	s_mov_b32 m0, s73
	v_lshl_add_u64 v[180:181], s[62:63], 0, v[166:167]
	global_load_lds_dwordx4 v[178:179], off
	v_lshl_add_u64 v[178:179], s[76:77], 0, v[164:165]
	s_add_i32 m0, s73, 0x2000
	s_nop 0
	global_load_lds_dwordx4 v[178:179], off
	v_lshl_add_u64 v[178:179], s[62:63], 0, v[168:169]
	s_mov_b32 m0, s18
	s_nop 0
	global_load_lds_dwordx4 v[178:179], off
	s_mov_b32 m0, s19
	s_nop 0
	global_load_lds_dwordx4 v[180:181], off
	s_cmp_eq_u32 s72, 0
	s_cbranch_scc1 .Lpg8skip11
	s_waitcnt vmcnt(8)
.Lpg8skip11:
	s_waitcnt lgkmcnt(0)
	s_barrier
	s_waitcnt lgkmcnt(0)
	v_mfma_scale_f32_16x16x128_f8f6f4 v[96:99], v[28:35], v[182:189], v[96:99], v245, v245 op_sel_hi:[0,0,0]
	v_mfma_scale_f32_16x16x128_f8f6f4 v[92:95], v[20:27], v[182:189], v[92:95], v245, v245 op_sel_hi:[0,0,0]
	v_mfma_scale_f32_16x16x128_f8f6f4 v[80:83], v[28:35], v[210:217], v[80:83], v245, v245 op_sel_hi:[0,0,0]
	v_mfma_scale_f32_16x16x128_f8f6f4 v[76:79], v[20:27], v[210:217], v[76:79], v245, v245 op_sel_hi:[0,0,0]
	v_mfma_scale_f32_16x16x128_f8f6f4 v[64:67], v[28:35], v[218:225], v[64:67], v245, v245 op_sel_hi:[0,0,0]
	v_mfma_scale_f32_16x16x128_f8f6f4 v[60:63], v[20:27], v[218:225], v[60:63], v245, v245 op_sel_hi:[0,0,0]
	v_mfma_scale_f32_16x16x128_f8f6f4 v[48:51], v[28:35], v[228:235], v[48:51], v245, v245 op_sel_hi:[0,0,0]
	v_mfma_scale_f32_16x16x128_f8f6f4 v[44:47], v[20:27], v[228:235], v[44:47], v245, v245 op_sel_hi:[0,0,0]
	v_mfma_scale_f32_16x16x128_f8f6f4 v[88:91], v[12:19], v[182:189], v[88:91], v245, v245 op_sel_hi:[0,0,0]
	v_mfma_scale_f32_16x16x128_f8f6f4 v[84:87], v[4:11], v[182:189], v[84:87], v245, v245 op_sel_hi:[0,0,0]
	v_mfma_scale_f32_16x16x128_f8f6f4 v[72:75], v[12:19], v[210:217], v[72:75], v245, v245 op_sel_hi:[0,0,0]
	v_mfma_scale_f32_16x16x128_f8f6f4 v[68:71], v[4:11], v[210:217], v[68:71], v245, v245 op_sel_hi:[0,0,0]
	v_mfma_scale_f32_16x16x128_f8f6f4 v[56:59], v[12:19], v[218:225], v[56:59], v245, v245 op_sel_hi:[0,0,0]
	v_mfma_scale_f32_16x16x128_f8f6f4 v[52:55], v[4:11], v[218:225], v[52:55], v245, v245 op_sel_hi:[0,0,0]
	v_mfma_scale_f32_16x16x128_f8f6f4 v[40:43], v[12:19], v[228:235], v[40:43], v245, v245 op_sel_hi:[0,0,0]
	v_mfma_scale_f32_16x16x128_f8f6f4 v[36:39], v[4:11], v[228:235], v[36:39], v245, v245 op_sel_hi:[0,0,0]
	s_barrier
	s_add_i32 s73, 0, 0x18000
	s_add_i32 s74, 0, 0x1c000
	v_add_u32_e32 v16, s73, v195
	v_add_u32_e32 v32, s74, v195
	ds_read_b128 v[4:7], v16
	ds_read_b128 v[8:11], v16 offset:1024
	ds_read_b128 v[12:15], v16 offset:2048
	ds_read_b128 v[16:19], v16 offset:3072
	ds_read_b128 v[20:23], v32
	ds_read_b128 v[24:27], v32 offset:1024
	ds_read_b128 v[28:31], v32 offset:2048
	ds_read_b128 v[32:35], v32 offset:3072
	s_add_u32 s62, s62, 0x20000
	s_addc_u32 s63, s63, 0
	s_mov_b32 m0, s20
	v_lshl_add_u64 v[190:191], s[62:63], 0, v[168:169]
	ds_read_b128 v[182:185], v208 offset:32768
	ds_read_b128 v[186:189], v208 offset:33792
	ds_read_b128 v[210:213], v208 offset:34816
	ds_read_b128 v[214:217], v208 offset:35840
	ds_read_b128 v[218:221], v208 offset:36864
	ds_read_b128 v[222:225], v208 offset:37888
	ds_read_b128 v[228:231], v208 offset:38912
	ds_read_b128 v[232:235], v208 offset:39936
	global_load_lds_dwordx4 v[190:191], off
	v_lshl_add_u64 v[190:191], s[62:63], 0, v[166:167]
	s_mov_b32 m0, s21
	s_nop 0
	global_load_lds_dwordx4 v[190:191], off
	s_waitcnt vmcnt(8)
	s_waitcnt lgkmcnt(0)
	s_barrier
; #define PG8_STAGE(bufoff, gbase, voff) do { _Pragma("unroll") for (int _i = 0; _i < 2; ++_i) \
;         __builtin_amdgcn_global_load_lds((const unsigned*)((const char*)(gbase) + (voff)[_i]), (PG8_LAS unsigned*)(lds + (bufoff) + ldsw + _i * 8192), 16, 0, 0); } while (0)
; #define PG8_LDA(dst, b, h) do { _Pragma("unroll") for (int m = 0; m < 4; ++m) _Pragma("unroll") for (int k = 0; k < 2; ++k) dst[m][k] = *(const PG8_LAS bf16x8*)(lds + PG8_SA(b, h) + aoff + m * 2048 + k * 1024); } while (0)
; #define PG8_WAIT_V(n) asm volatile("s_waitcnt vmcnt(" #n ")" ::: "memory")
; #define PG8_WAIT_L(n) asm volatile("s_waitcnt lgkmcnt(" #n ")" ::: "memory")
; #define PG8_BAR __builtin_amdgcn_s_barrier()
; #define PG8_SCHED __builtin_amdgcn_sched_barrier(0)
; template <class Epi, class Sched, bool ALIGN_EPI = false, bool SP2 = false, bool FP8 = false, bool ABLK = false>
; __device__ __forceinline__ void gemm_phase(PG8_LAS unsigned char* lds, const Gemm g, const Sched& S, const Epi& E) {
;     ...
;             PG8_WAIT_V(8); PG8_WAIT_L(0); PG8_BAR; PG8_MMA(0, 0, At, B0); PG8_MMA(0, 1, At, B1); PG8_BAR; PG8_SCHED;
;             PG8_LDA(At, 1, 1); PG8_STAGE(PG8_SB(1, 0), b3, voffB); PG8_STAGE(PG8_SB(1, 1), b3 + hstep, voffB); PG8_STAGE(PG8_SA(1, 0), a3, voffA);
;             PG8_WAIT_V(8); PG8_WAIT_L(0); PG8_BAR; PG8_MMA(1, 0, At, B0); PG8_MMA(1, 1, At, B1); PG8_BAR; PG8_SCHED;
;     ...
;         if constexpr (SP2) PG8_WAIT_V(0);
;         if constexpr (FP8) asm volatile("s_nop 15\n\ts_nop 15" ::: "memory");
;         if constexpr (ALIGN_EPI) { if (wr == 0) PG8_BAR; }
	s_waitcnt lgkmcnt(0)
	v_mfma_scale_f32_16x16x128_f8f6f4 v[160:163], v[4:11], v[182:189], v[160:163], v245, v245 op_sel_hi:[0,0,0]
	v_mfma_scale_f32_16x16x128_f8f6f4 v[156:159], v[12:19], v[182:189], v[156:159], v245, v245 op_sel_hi:[0,0,0]
	v_mfma_scale_f32_16x16x128_f8f6f4 v[144:147], v[4:11], v[210:217], v[144:147], v245, v245 op_sel_hi:[0,0,0]
	v_mfma_scale_f32_16x16x128_f8f6f4 v[140:143], v[12:19], v[210:217], v[140:143], v245, v245 op_sel_hi:[0,0,0]
	v_mfma_scale_f32_16x16x128_f8f6f4 v[128:131], v[4:11], v[218:225], v[128:131], v245, v245 op_sel_hi:[0,0,0]
	v_mfma_scale_f32_16x16x128_f8f6f4 v[124:127], v[12:19], v[218:225], v[124:127], v245, v245 op_sel_hi:[0,0,0]
	v_mfma_scale_f32_16x16x128_f8f6f4 v[112:115], v[4:11], v[228:235], v[112:115], v245, v245 op_sel_hi:[0,0,0]
	v_mfma_scale_f32_16x16x128_f8f6f4 v[108:111], v[12:19], v[228:235], v[108:111], v245, v245 op_sel_hi:[0,0,0]
	v_mfma_scale_f32_16x16x128_f8f6f4 v[152:155], v[20:27], v[182:189], v[152:155], v245, v245 op_sel_hi:[0,0,0]
	v_mfma_scale_f32_16x16x128_f8f6f4 v[148:151], v[28:35], v[182:189], v[148:151], v245, v245 op_sel_hi:[0,0,0]
	v_mfma_scale_f32_16x16x128_f8f6f4 v[136:139], v[20:27], v[210:217], v[136:139], v245, v245 op_sel_hi:[0,0,0]
	v_mfma_scale_f32_16x16x128_f8f6f4 v[132:135], v[28:35], v[210:217], v[132:135], v245, v245 op_sel_hi:[0,0,0]
	v_mfma_scale_f32_16x16x128_f8f6f4 v[120:123], v[20:27], v[218:225], v[120:123], v245, v245 op_sel_hi:[0,0,0]
	v_mfma_scale_f32_16x16x128_f8f6f4 v[116:119], v[28:35], v[218:225], v[116:119], v245, v245 op_sel_hi:[0,0,0]
	v_mfma_scale_f32_16x16x128_f8f6f4 v[104:107], v[20:27], v[228:235], v[104:107], v245, v245 op_sel_hi:[0,0,0]
	v_mfma_scale_f32_16x16x128_f8f6f4 v[100:103], v[28:35], v[228:235], v[100:103], v245, v245 op_sel_hi:[0,0,0]
	s_barrier
	s_add_i32 s62, s73, s17
	v_lshl_add_u64 v[174:175], v[174:175], 0, s[34:35]
	s_mov_b32 m0, s62
	ds_read_b128 v[182:185], v208 offset:49152
	ds_read_b128 v[186:189], v208 offset:50176
	ds_read_b128 v[210:213], v208 offset:51200
	ds_read_b128 v[214:217], v208 offset:52224
	ds_read_b128 v[218:221], v208 offset:53248
	ds_read_b128 v[222:225], v208 offset:54272
	ds_read_b128 v[228:231], v208 offset:55296
	ds_read_b128 v[232:235], v208 offset:56320
	global_load_lds_dwordx4 v[174:175], off
	s_add_i32 m0, s62, 0x2000
	s_add_u32 s60, s60, 0x20080
	v_lshl_add_u64 v[174:175], v[176:177], 0, s[34:35]
	s_addc_u32 s61, s61, 0
	s_add_i32 s62, s74, s17
	global_load_lds_dwordx4 v[174:175], off
	v_lshl_add_u64 v[174:175], s[60:61], 0, v[2:3]
	s_mov_b32 m0, s62
	s_nop 0
	global_load_lds_dwordx4 v[174:175], off
	v_lshl_add_u64 v[174:175], s[60:61], 0, v[164:165]
	s_add_i32 m0, s62, 0x2000
	s_nop 0
	global_load_lds_dwordx4 v[174:175], off
	v_lshl_add_u64 v[174:175], v[178:179], 0, s[34:35]
	s_mov_b32 m0, s65
	s_nop 0
	global_load_lds_dwordx4 v[174:175], off
	v_lshl_add_u64 v[174:175], v[180:181], 0, s[34:35]
	s_mov_b32 m0, s66
	s_nop 0
	global_load_lds_dwordx4 v[174:175], off
	s_waitcnt vmcnt(8)
	s_waitcnt lgkmcnt(0)
	s_barrier
	s_waitcnt lgkmcnt(0)
	v_mfma_scale_f32_16x16x128_f8f6f4 v[96:99], v[4:11], v[182:189], v[96:99], v245, v245 op_sel_hi:[0,0,0]
	v_mfma_scale_f32_16x16x128_f8f6f4 v[92:95], v[12:19], v[182:189], v[92:95], v245, v245 op_sel_hi:[0,0,0]
	v_mfma_scale_f32_16x16x128_f8f6f4 v[80:83], v[4:11], v[210:217], v[80:83], v245, v245 op_sel_hi:[0,0,0]
	v_mfma_scale_f32_16x16x128_f8f6f4 v[76:79], v[12:19], v[210:217], v[76:79], v245, v245 op_sel_hi:[0,0,0]
	v_mfma_scale_f32_16x16x128_f8f6f4 v[64:67], v[4:11], v[218:225], v[64:67], v245, v245 op_sel_hi:[0,0,0]
	v_mfma_scale_f32_16x16x128_f8f6f4 v[60:63], v[12:19], v[218:225], v[60:63], v245, v245 op_sel_hi:[0,0,0]
	v_mfma_scale_f32_16x16x128_f8f6f4 v[48:51], v[4:11], v[228:235], v[48:51], v245, v245 op_sel_hi:[0,0,0]
	v_mfma_scale_f32_16x16x128_f8f6f4 v[44:47], v[12:19], v[228:235], v[44:47], v245, v245 op_sel_hi:[0,0,0]
	v_mfma_scale_f32_16x16x128_f8f6f4 v[88:91], v[20:27], v[182:189], v[88:91], v245, v245 op_sel_hi:[0,0,0]
	v_mfma_scale_f32_16x16x128_f8f6f4 v[84:87], v[28:35], v[182:189], v[84:87], v245, v245 op_sel_hi:[0,0,0]
	v_mfma_scale_f32_16x16x128_f8f6f4 v[72:75], v[20:27], v[210:217], v[72:75], v245, v245 op_sel_hi:[0,0,0]
	v_mfma_scale_f32_16x16x128_f8f6f4 v[68:71], v[28:35], v[210:217], v[68:71], v245, v245 op_sel_hi:[0,0,0]
	v_mfma_scale_f32_16x16x128_f8f6f4 v[56:59], v[20:27], v[218:225], v[56:59], v245, v245 op_sel_hi:[0,0,0]
	v_mfma_scale_f32_16x16x128_f8f6f4 v[52:55], v[28:35], v[218:225], v[52:55], v245, v245 op_sel_hi:[0,0,0]
	v_mfma_scale_f32_16x16x128_f8f6f4 v[40:43], v[20:27], v[228:235], v[40:43], v245, v245 op_sel_hi:[0,0,0]
	v_mfma_scale_f32_16x16x128_f8f6f4 v[36:39], v[28:35], v[228:235], v[36:39], v245, v245 op_sel_hi:[0,0,0]
	s_barrier
	s_add_u32 s42, s42, 0x100
	s_addc_u32 s43, s43, 0
	s_add_u32 s70, s70, 0x100
	s_addc_u32 s71, s71, 0
	s_cmp_gt_u32 s72, 5
	s_mov_b32 s60, s72
	s_cbranch_scc0 .LBB0_1587
	s_waitcnt vmcnt(0)
	s_nop 15
	s_nop 15
	s_and_b64 vcc, exec, s[50:51]
	s_cbranch_vccz .LBB0_1590
	s_barrier

; #define PG8_STAGE(bufoff, gbase, voff) do { _Pragma("unroll") for (int _i = 0; _i < 2; ++_i) \
;         __builtin_amdgcn_global_load_lds((const unsigned*)((const char*)(gbase) + (voff)[_i]), (PG8_LAS unsigned*)(lds + (bufoff) + ldsw + _i * 8192), 16, 0, 0); } while (0)
; #define PG8_LDA(dst, b, h) do { _Pragma("unroll") for (int m = 0; m < 4; ++m) _Pragma("unroll") for (int k = 0; k < 2; ++k) dst[m][k] = *(const PG8_LAS bf16x8*)(lds + PG8_SA(b, h) + aoff + m * 2048 + k * 1024); } while (0)
; #define PG8_LDB(dst, b, h) do { _Pragma("unroll") for (int n = 0; n < 2; ++n) _Pragma("unroll") for (int k = 0; k < 2; ++k) dst[n][k] = *(const PG8_LAS bf16x8*)(lds + PG8_SB(b, h) + boff + n * 2048 + k * 1024); } while (0)
; #define PG8_WAIT_V(n) asm volatile("s_waitcnt vmcnt(" #n ")" ::: "memory")
; #define PG8_WAIT_V8_UNLESS_FIRST(t) asm volatile("s_cmp_eq_u32 %0, 0\n\ts_cbranch_scc1 .Lpg8skip%=\n\ts_waitcnt vmcnt(8)\n.Lpg8skip%=:" :: "s"(t) : "scc", "memory")
; #define PG8_WAIT_L(n) asm volatile("s_waitcnt lgkmcnt(" #n ")" ::: "memory")
; #define PG8_BAR __builtin_amdgcn_s_barrier()
; #define PG8_SCHED __builtin_amdgcn_sched_barrier(0)
; template <class Epi, class Sched, bool ALIGN_EPI = false, bool SP2 = false, bool FP8 = false, bool ABLK = false>
; __device__ __forceinline__ void gemm_phase(PG8_LAS unsigned char* lds, const Gemm g, const Sched& S, const Epi& E) {
;     ...
;             PG8_WAIT_V8_UNLESS_FIRST(t); PG8_WAIT_L(0); PG8_BAR; PG8_MMA(0, 0, At, B0); PG8_MMA(0, 1, At, B1); PG8_BAR; PG8_SCHED;
;             PG8_LDA(At, 0, 1); PG8_STAGE(PG8_SB(0, 0), b2, voffB); PG8_STAGE(PG8_SB(0, 1), b2 + hstep, voffB); PG8_STAGE(PG8_SA(0, 0), a2, voffA);
;             PG8_WAIT_V8_UNLESS_FIRST(t); PG8_WAIT_L(0); PG8_BAR; PG8_MMA(1, 0, At, B0); PG8_MMA(1, 1, At, B1); PG8_BAR; PG8_SCHED;
;             PG8_LDB(B0, 1, 0); PG8_LDB(B1, 1, 1); PG8_SCHED; PG8_LDA(At, 1, 0); PG8_STAGE(PG8_SA(0, 1), a2 + hstepA, voffA);
;             PG8_WAIT_V(8); PG8_WAIT_L(0); PG8_BAR; PG8_MMA(0, 0, At, B0); PG8_MMA(0, 1, At, B1); PG8_BAR; PG8_SCHED;
.Lpg8skip12:
	s_waitcnt lgkmcnt(0)
	s_barrier
	s_waitcnt lgkmcnt(0)
	v_mfma_scale_f32_16x16x128_f8f6f4 v[160:163], v[28:35], v[174:181], v[160:163], v245, v245 op_sel_hi:[0,0,0]
	v_mfma_scale_f32_16x16x128_f8f6f4 v[156:159], v[20:27], v[174:181], v[156:159], v245, v245 op_sel_hi:[0,0,0]
	v_mfma_scale_f32_16x16x128_f8f6f4 v[144:147], v[28:35], v[186:193], v[144:147], v245, v245 op_sel_hi:[0,0,0]
	v_mfma_scale_f32_16x16x128_f8f6f4 v[140:143], v[20:27], v[186:193], v[140:143], v245, v245 op_sel_hi:[0,0,0]
	v_mfma_scale_f32_16x16x128_f8f6f4 v[128:131], v[28:35], v[208:215], v[128:131], v245, v245 op_sel_hi:[0,0,0]
	v_mfma_scale_f32_16x16x128_f8f6f4 v[124:127], v[20:27], v[208:215], v[124:127], v245, v245 op_sel_hi:[0,0,0]
	v_mfma_scale_f32_16x16x128_f8f6f4 v[112:115], v[28:35], v[216:223], v[112:115], v245, v245 op_sel_hi:[0,0,0]
	v_mfma_scale_f32_16x16x128_f8f6f4 v[108:111], v[20:27], v[216:223], v[108:111], v245, v245 op_sel_hi:[0,0,0]
	v_mfma_scale_f32_16x16x128_f8f6f4 v[152:155], v[12:19], v[174:181], v[152:155], v245, v245 op_sel_hi:[0,0,0]
	v_mfma_scale_f32_16x16x128_f8f6f4 v[148:151], v[4:11], v[174:181], v[148:151], v245, v245 op_sel_hi:[0,0,0]
	v_mfma_scale_f32_16x16x128_f8f6f4 v[136:139], v[12:19], v[186:193], v[136:139], v245, v245 op_sel_hi:[0,0,0]
	v_mfma_scale_f32_16x16x128_f8f6f4 v[132:135], v[4:11], v[186:193], v[132:135], v245, v245 op_sel_hi:[0,0,0]
	v_mfma_scale_f32_16x16x128_f8f6f4 v[120:123], v[12:19], v[208:215], v[120:123], v245, v245 op_sel_hi:[0,0,0]
	v_mfma_scale_f32_16x16x128_f8f6f4 v[116:119], v[4:11], v[208:215], v[116:119], v245, v245 op_sel_hi:[0,0,0]
	v_mfma_scale_f32_16x16x128_f8f6f4 v[104:107], v[12:19], v[216:223], v[104:107], v245, v245 op_sel_hi:[0,0,0]
	v_mfma_scale_f32_16x16x128_f8f6f4 v[100:103], v[4:11], v[216:223], v[100:103], v245, v245 op_sel_hi:[0,0,0]
	s_barrier
	s_add_i32 s76, s76, s19
	v_lshl_add_u64 v[174:175], s[62:63], 0, v[2:3]
	s_mov_b32 m0, s76
	ds_read_b128 v[186:189], v184 offset:16384
	ds_read_b128 v[190:193], v184 offset:17408
	ds_read_b128 v[208:211], v184 offset:18432
	ds_read_b128 v[212:215], v184 offset:19456
	ds_read_b128 v[216:219], v184 offset:20480
	ds_read_b128 v[220:223], v184 offset:21504
	ds_read_b128 v[228:231], v184 offset:22528
	ds_read_b128 v[232:235], v184 offset:23552
	global_load_lds_dwordx4 v[174:175], off
	s_add_i32 m0, s76, 0x2000
	s_add_u32 s84, s62, 0x20000
	v_lshl_add_u64 v[176:177], s[62:63], 0, v[164:165]
	s_addc_u32 s85, s63, 0
	s_add_i32 s76, s77, s19
	global_load_lds_dwordx4 v[176:177], off
	v_lshl_add_u64 v[178:179], s[84:85], 0, v[2:3]
	s_mov_b32 m0, s76
	v_lshl_add_u64 v[180:181], s[64:65], 0, v[166:167]
	global_load_lds_dwordx4 v[178:179], off
	v_lshl_add_u64 v[178:179], s[84:85], 0, v[164:165]
	s_add_i32 m0, s76, 0x2000
	s_nop 0
	global_load_lds_dwordx4 v[178:179], off
	v_lshl_add_u64 v[178:179], s[64:65], 0, v[168:169]
	s_mov_b32 m0, s20
	s_nop 0
	global_load_lds_dwordx4 v[178:179], off
	s_mov_b32 m0, s21
	s_nop 0
	global_load_lds_dwordx4 v[180:181], off
	s_cmp_eq_u32 s75, 0
	s_cbranch_scc1 .Lpg8skip13
	s_waitcnt vmcnt(8)
.Lpg8skip13:
	s_waitcnt lgkmcnt(0)
	s_barrier
	s_waitcnt lgkmcnt(0)
	v_mfma_scale_f32_16x16x128_f8f6f4 v[96:99], v[28:35], v[186:193], v[96:99], v245, v245 op_sel_hi:[0,0,0]
	v_mfma_scale_f32_16x16x128_f8f6f4 v[92:95], v[20:27], v[186:193], v[92:95], v245, v245 op_sel_hi:[0,0,0]
	v_mfma_scale_f32_16x16x128_f8f6f4 v[80:83], v[28:35], v[208:215], v[80:83], v245, v245 op_sel_hi:[0,0,0]
	v_mfma_scale_f32_16x16x128_f8f6f4 v[76:79], v[20:27], v[208:215], v[76:79], v245, v245 op_sel_hi:[0,0,0]
	v_mfma_scale_f32_16x16x128_f8f6f4 v[64:67], v[28:35], v[216:223], v[64:67], v245, v245 op_sel_hi:[0,0,0]
	v_mfma_scale_f32_16x16x128_f8f6f4 v[60:63], v[20:27], v[216:223], v[60:63], v245, v245 op_sel_hi:[0,0,0]
	v_mfma_scale_f32_16x16x128_f8f6f4 v[48:51], v[28:35], v[228:235], v[48:51], v245, v245 op_sel_hi:[0,0,0]
	v_mfma_scale_f32_16x16x128_f8f6f4 v[44:47], v[20:27], v[228:235], v[44:47], v245, v245 op_sel_hi:[0,0,0]
	v_mfma_scale_f32_16x16x128_f8f6f4 v[88:91], v[12:19], v[186:193], v[88:91], v245, v245 op_sel_hi:[0,0,0]
	v_mfma_scale_f32_16x16x128_f8f6f4 v[84:87], v[4:11], v[186:193], v[84:87], v245, v245 op_sel_hi:[0,0,0]
	v_mfma_scale_f32_16x16x128_f8f6f4 v[72:75], v[12:19], v[208:215], v[72:75], v245, v245 op_sel_hi:[0,0,0]
	v_mfma_scale_f32_16x16x128_f8f6f4 v[68:71], v[4:11], v[208:215], v[68:71], v245, v245 op_sel_hi:[0,0,0]
	v_mfma_scale_f32_16x16x128_f8f6f4 v[56:59], v[12:19], v[216:223], v[56:59], v245, v245 op_sel_hi:[0,0,0]
	v_mfma_scale_f32_16x16x128_f8f6f4 v[52:55], v[4:11], v[216:223], v[52:55], v245, v245 op_sel_hi:[0,0,0]
	v_mfma_scale_f32_16x16x128_f8f6f4 v[40:43], v[12:19], v[228:235], v[40:43], v245, v245 op_sel_hi:[0,0,0]
	v_mfma_scale_f32_16x16x128_f8f6f4 v[36:39], v[4:11], v[228:235], v[36:39], v245, v245 op_sel_hi:[0,0,0]
	s_barrier
	s_add_i32 s76, 0, 0x18000
	s_add_i32 s77, 0, 0x1c000
	v_add_u32_e32 v16, s76, v183
	v_add_u32_e32 v32, s77, v183
	ds_read_b128 v[4:7], v16
	ds_read_b128 v[8:11], v16 offset:1024
	ds_read_b128 v[12:15], v16 offset:2048
	ds_read_b128 v[16:19], v16 offset:3072
	ds_read_b128 v[20:23], v32
	ds_read_b128 v[24:27], v32 offset:1024
	ds_read_b128 v[28:31], v32 offset:2048
	ds_read_b128 v[32:35], v32 offset:3072
	s_add_u32 s64, s64, 0x20000
	s_addc_u32 s65, s65, 0
	s_mov_b32 m0, s22
	v_lshl_add_u64 v[194:195], s[64:65], 0, v[168:169]
	ds_read_b128 v[186:189], v184 offset:32768
	ds_read_b128 v[190:193], v184 offset:33792
	ds_read_b128 v[208:211], v184 offset:34816
	ds_read_b128 v[212:215], v184 offset:35840
	ds_read_b128 v[216:219], v184 offset:36864
	ds_read_b128 v[220:223], v184 offset:37888
	ds_read_b128 v[228:231], v184 offset:38912
	ds_read_b128 v[232:235], v184 offset:39936
	global_load_lds_dwordx4 v[194:195], off
	v_lshl_add_u64 v[194:195], s[64:65], 0, v[166:167]
	s_mov_b32 m0, s23
	s_nop 0
	global_load_lds_dwordx4 v[194:195], off
	s_waitcnt vmcnt(8)
	s_waitcnt lgkmcnt(0)
	s_barrier
; #define PG8_STAGE(bufoff, gbase, voff) do { _Pragma("unroll") for (int _i = 0; _i < 2; ++_i) \
;         __builtin_amdgcn_global_load_lds((const unsigned*)((const char*)(gbase) + (voff)[_i]), (PG8_LAS unsigned*)(lds + (bufoff) + ldsw + _i * 8192), 16, 0, 0); } while (0)
; #define PG8_LDA(dst, b, h) do { _Pragma("unroll") for (int m = 0; m < 4; ++m) _Pragma("unroll") for (int k = 0; k < 2; ++k) dst[m][k] = *(const PG8_LAS bf16x8*)(lds + PG8_SA(b, h) + aoff + m * 2048 + k * 1024); } while (0)
; #define PG8_WAIT_V(n) asm volatile("s_waitcnt vmcnt(" #n ")" ::: "memory")
; #define PG8_WAIT_L(n) asm volatile("s_waitcnt lgkmcnt(" #n ")" ::: "memory")
; #define PG8_BAR __builtin_amdgcn_s_barrier()
; #define PG8_SCHED __builtin_amdgcn_sched_barrier(0)
; template <class Epi, class Sched, bool ALIGN_EPI = false, bool SP2 = false, bool FP8 = false, bool ABLK = false>
; __device__ __forceinline__ void gemm_phase(PG8_LAS unsigned char* lds, const Gemm g, const Sched& S, const Epi& E) {
;     ...
;             PG8_WAIT_V(8); PG8_WAIT_L(0); PG8_BAR; PG8_MMA(0, 0, At, B0); PG8_MMA(0, 1, At, B1); PG8_BAR; PG8_SCHED;
;             PG8_LDA(At, 1, 1); PG8_STAGE(PG8_SB(1, 0), b3, voffB); PG8_STAGE(PG8_SB(1, 1), b3 + hstep, voffB); PG8_STAGE(PG8_SA(1, 0), a3, voffA);
;             PG8_WAIT_V(8); PG8_WAIT_L(0); PG8_BAR; PG8_MMA(1, 0, At, B0); PG8_MMA(1, 1, At, B1); PG8_BAR; PG8_SCHED;
;     ...
;         if constexpr (SP2) PG8_WAIT_V(0);
;         if constexpr (FP8) asm volatile("s_nop 15\n\ts_nop 15" ::: "memory");
;         if constexpr (ALIGN_EPI) { if (wr == 0) PG8_BAR; }
	s_waitcnt lgkmcnt(0)
	v_mfma_scale_f32_16x16x128_f8f6f4 v[160:163], v[4:11], v[186:193], v[160:163], v245, v245 op_sel_hi:[0,0,0]
	v_mfma_scale_f32_16x16x128_f8f6f4 v[156:159], v[12:19], v[186:193], v[156:159], v245, v245 op_sel_hi:[0,0,0]
	v_mfma_scale_f32_16x16x128_f8f6f4 v[144:147], v[4:11], v[208:215], v[144:147], v245, v245 op_sel_hi:[0,0,0]
	v_mfma_scale_f32_16x16x128_f8f6f4 v[140:143], v[12:19], v[208:215], v[140:143], v245, v245 op_sel_hi:[0,0,0]
	v_mfma_scale_f32_16x16x128_f8f6f4 v[128:131], v[4:11], v[216:223], v[128:131], v245, v245 op_sel_hi:[0,0,0]
	v_mfma_scale_f32_16x16x128_f8f6f4 v[124:127], v[12:19], v[216:223], v[124:127], v245, v245 op_sel_hi:[0,0,0]
	v_mfma_scale_f32_16x16x128_f8f6f4 v[112:115], v[4:11], v[228:235], v[112:115], v245, v245 op_sel_hi:[0,0,0]
	v_mfma_scale_f32_16x16x128_f8f6f4 v[108:111], v[12:19], v[228:235], v[108:111], v245, v245 op_sel_hi:[0,0,0]
	v_mfma_scale_f32_16x16x128_f8f6f4 v[152:155], v[20:27], v[186:193], v[152:155], v245, v245 op_sel_hi:[0,0,0]
	v_mfma_scale_f32_16x16x128_f8f6f4 v[148:151], v[28:35], v[186:193], v[148:151], v245, v245 op_sel_hi:[0,0,0]
	v_mfma_scale_f32_16x16x128_f8f6f4 v[136:139], v[20:27], v[208:215], v[136:139], v245, v245 op_sel_hi:[0,0,0]
	v_mfma_scale_f32_16x16x128_f8f6f4 v[132:135], v[28:35], v[208:215], v[132:135], v245, v245 op_sel_hi:[0,0,0]
	v_mfma_scale_f32_16x16x128_f8f6f4 v[120:123], v[20:27], v[216:223], v[120:123], v245, v245 op_sel_hi:[0,0,0]
	v_mfma_scale_f32_16x16x128_f8f6f4 v[116:119], v[28:35], v[216:223], v[116:119], v245, v245 op_sel_hi:[0,0,0]
	v_mfma_scale_f32_16x16x128_f8f6f4 v[104:107], v[20:27], v[228:235], v[104:107], v245, v245 op_sel_hi:[0,0,0]
	v_mfma_scale_f32_16x16x128_f8f6f4 v[100:103], v[28:35], v[228:235], v[100:103], v245, v245 op_sel_hi:[0,0,0]
	s_barrier
	s_add_i32 s64, s76, s19
	v_lshl_add_u64 v[174:175], v[174:175], 0, s[34:35]
	s_mov_b32 m0, s64
	ds_read_b128 v[186:189], v184 offset:49152
	ds_read_b128 v[190:193], v184 offset:50176
	ds_read_b128 v[208:211], v184 offset:51200
	ds_read_b128 v[212:215], v184 offset:52224
	ds_read_b128 v[216:219], v184 offset:53248
	ds_read_b128 v[220:223], v184 offset:54272
	ds_read_b128 v[228:231], v184 offset:55296
	ds_read_b128 v[232:235], v184 offset:56320
	global_load_lds_dwordx4 v[174:175], off
	s_add_i32 m0, s64, 0x2000
	s_add_u32 s62, s62, 0x20080
	v_lshl_add_u64 v[174:175], v[176:177], 0, s[34:35]
	s_addc_u32 s63, s63, 0
	s_add_i32 s64, s77, s19
	global_load_lds_dwordx4 v[174:175], off
	v_lshl_add_u64 v[174:175], s[62:63], 0, v[2:3]
	s_mov_b32 m0, s64
	s_nop 0
	global_load_lds_dwordx4 v[174:175], off
	v_lshl_add_u64 v[174:175], s[62:63], 0, v[164:165]
	s_add_i32 m0, s64, 0x2000
	s_nop 0
	global_load_lds_dwordx4 v[174:175], off
	v_lshl_add_u64 v[174:175], v[178:179], 0, s[34:35]
	s_mov_b32 m0, s67
	s_nop 0
	global_load_lds_dwordx4 v[174:175], off
	v_lshl_add_u64 v[174:175], v[180:181], 0, s[34:35]
	s_mov_b32 m0, s68
	s_nop 0
	global_load_lds_dwordx4 v[174:175], off
	s_waitcnt vmcnt(8)
	s_waitcnt lgkmcnt(0)
	s_barrier
	s_waitcnt lgkmcnt(0)
	v_mfma_scale_f32_16x16x128_f8f6f4 v[96:99], v[4:11], v[186:193], v[96:99], v245, v245 op_sel_hi:[0,0,0]
	v_mfma_scale_f32_16x16x128_f8f6f4 v[92:95], v[12:19], v[186:193], v[92:95], v245, v245 op_sel_hi:[0,0,0]
	v_mfma_scale_f32_16x16x128_f8f6f4 v[80:83], v[4:11], v[208:215], v[80:83], v245, v245 op_sel_hi:[0,0,0]
	v_mfma_scale_f32_16x16x128_f8f6f4 v[76:79], v[12:19], v[208:215], v[76:79], v245, v245 op_sel_hi:[0,0,0]
	v_mfma_scale_f32_16x16x128_f8f6f4 v[64:67], v[4:11], v[216:223], v[64:67], v245, v245 op_sel_hi:[0,0,0]
	v_mfma_scale_f32_16x16x128_f8f6f4 v[60:63], v[12:19], v[216:223], v[60:63], v245, v245 op_sel_hi:[0,0,0]
	v_mfma_scale_f32_16x16x128_f8f6f4 v[48:51], v[4:11], v[228:235], v[48:51], v245, v245 op_sel_hi:[0,0,0]
	v_mfma_scale_f32_16x16x128_f8f6f4 v[44:47], v[12:19], v[228:235], v[44:47], v245, v245 op_sel_hi:[0,0,0]
	v_mfma_scale_f32_16x16x128_f8f6f4 v[88:91], v[20:27], v[186:193], v[88:91], v245, v245 op_sel_hi:[0,0,0]
	v_mfma_scale_f32_16x16x128_f8f6f4 v[84:87], v[28:35], v[186:193], v[84:87], v245, v245 op_sel_hi:[0,0,0]
	v_mfma_scale_f32_16x16x128_f8f6f4 v[72:75], v[20:27], v[208:215], v[72:75], v245, v245 op_sel_hi:[0,0,0]
	v_mfma_scale_f32_16x16x128_f8f6f4 v[68:71], v[28:35], v[208:215], v[68:71], v245, v245 op_sel_hi:[0,0,0]
	v_mfma_scale_f32_16x16x128_f8f6f4 v[56:59], v[20:27], v[216:223], v[56:59], v245, v245 op_sel_hi:[0,0,0]
	v_mfma_scale_f32_16x16x128_f8f6f4 v[52:55], v[28:35], v[216:223], v[52:55], v245, v245 op_sel_hi:[0,0,0]
	v_mfma_scale_f32_16x16x128_f8f6f4 v[40:43], v[20:27], v[228:235], v[40:43], v245, v245 op_sel_hi:[0,0,0]
	v_mfma_scale_f32_16x16x128_f8f6f4 v[36:39], v[28:35], v[228:235], v[36:39], v245, v245 op_sel_hi:[0,0,0]
	s_barrier
	s_add_u32 s60, s60, 0x100
	s_addc_u32 s61, s61, 0
	s_add_u32 s73, s73, 0x100
	s_addc_u32 s74, s74, 0
	s_cmp_gt_u32 s75, 5
	s_mov_b32 s62, s75
	s_cbranch_scc0 .LBB0_1671
	s_waitcnt vmcnt(0)
	s_nop 15
	s_nop 15
	s_and_b64 vcc, exec, s[50:51]
	s_cbranch_vccz .LBB0_1674
	s_barrier

; #define PG8_STAGE(bufoff, gbase, voff) do { _Pragma("unroll") for (int _i = 0; _i < 2; ++_i) \
;         __builtin_amdgcn_global_load_lds((const unsigned*)((const char*)(gbase) + (voff)[_i]), (PG8_LAS unsigned*)(lds + (bufoff) + ldsw + _i * 8192), 16, 0, 0); } while (0)
; #define PG8_LDA(dst, b, h) do { _Pragma("unroll") for (int m = 0; m < 4; ++m) _Pragma("unroll") for (int k = 0; k < 2; ++k) dst[m][k] = *(const PG8_LAS bf16x8*)(lds + PG8_SA(b, h) + aoff + m * 2048 + k * 1024); } while (0)
; #define PG8_LDB(dst, b, h) do { _Pragma("unroll") for (int n = 0; n < 2; ++n) _Pragma("unroll") for (int k = 0; k < 2; ++k) dst[n][k] = *(const PG8_LAS bf16x8*)(lds + PG8_SB(b, h) + boff + n * 2048 + k * 1024); } while (0)
; #define PG8_WAIT_V(n) asm volatile("s_waitcnt vmcnt(" #n ")" ::: "memory")
; #define PG8_WAIT_V8_UNLESS_FIRST(t) asm volatile("s_cmp_eq_u32 %0, 0\n\ts_cbranch_scc1 .Lpg8skip%=\n\ts_waitcnt vmcnt(8)\n.Lpg8skip%=:" :: "s"(t) : "scc", "memory")
; #define PG8_WAIT_L(n) asm volatile("s_waitcnt lgkmcnt(" #n ")" ::: "memory")
; #define PG8_BAR __builtin_amdgcn_s_barrier()
; #define PG8_SCHED __builtin_amdgcn_sched_barrier(0)
; template <class Epi, class Sched, bool ALIGN_EPI = false, bool SP2 = false, bool FP8 = false, bool ABLK = false>
; __device__ __forceinline__ void gemm_phase(PG8_LAS unsigned char* lds, const Gemm g, const Sched& S, const Epi& E) {
;     ...
;             PG8_WAIT_V8_UNLESS_FIRST(t); PG8_WAIT_L(0); PG8_BAR; PG8_MMA(0, 0, At, B0); PG8_MMA(0, 1, At, B1); PG8_BAR; PG8_SCHED;
;             PG8_LDA(At, 0, 1); PG8_STAGE(PG8_SB(0, 0), b2, voffB); PG8_STAGE(PG8_SB(0, 1), b2 + hstep, voffB); PG8_STAGE(PG8_SA(0, 0), a2, voffA);
;             PG8_WAIT_V8_UNLESS_FIRST(t); PG8_WAIT_L(0); PG8_BAR; PG8_MMA(1, 0, At, B0); PG8_MMA(1, 1, At, B1); PG8_BAR; PG8_SCHED;
;             PG8_LDB(B0, 1, 0); PG8_LDB(B1, 1, 1); PG8_SCHED; PG8_LDA(At, 1, 0); PG8_STAGE(PG8_SA(0, 1), a2 + hstepA, voffA);
;             PG8_WAIT_V(8); PG8_WAIT_L(0); PG8_BAR; PG8_MMA(0, 0, At, B0); PG8_MMA(0, 1, At, B1); PG8_BAR; PG8_SCHED;
.Lpg8skip14:
	s_waitcnt lgkmcnt(0)
	s_barrier
	s_waitcnt lgkmcnt(0)
	v_mfma_scale_f32_16x16x128_f8f6f4 v[160:163], v[28:35], v[174:181], v[160:163], v245, v245 op_sel_hi:[0,0,0]
	v_mfma_scale_f32_16x16x128_f8f6f4 v[156:159], v[20:27], v[174:181], v[156:159], v245, v245 op_sel_hi:[0,0,0]
	v_mfma_scale_f32_16x16x128_f8f6f4 v[144:147], v[28:35], v[186:193], v[144:147], v245, v245 op_sel_hi:[0,0,0]
	v_mfma_scale_f32_16x16x128_f8f6f4 v[140:143], v[20:27], v[186:193], v[140:143], v245, v245 op_sel_hi:[0,0,0]
	v_mfma_scale_f32_16x16x128_f8f6f4 v[128:131], v[28:35], v[208:215], v[128:131], v245, v245 op_sel_hi:[0,0,0]
	v_mfma_scale_f32_16x16x128_f8f6f4 v[124:127], v[20:27], v[208:215], v[124:127], v245, v245 op_sel_hi:[0,0,0]
	v_mfma_scale_f32_16x16x128_f8f6f4 v[112:115], v[28:35], v[216:223], v[112:115], v245, v245 op_sel_hi:[0,0,0]
	v_mfma_scale_f32_16x16x128_f8f6f4 v[108:111], v[20:27], v[216:223], v[108:111], v245, v245 op_sel_hi:[0,0,0]
	v_mfma_scale_f32_16x16x128_f8f6f4 v[152:155], v[12:19], v[174:181], v[152:155], v245, v245 op_sel_hi:[0,0,0]
	v_mfma_scale_f32_16x16x128_f8f6f4 v[148:151], v[4:11], v[174:181], v[148:151], v245, v245 op_sel_hi:[0,0,0]
	v_mfma_scale_f32_16x16x128_f8f6f4 v[136:139], v[12:19], v[186:193], v[136:139], v245, v245 op_sel_hi:[0,0,0]
	v_mfma_scale_f32_16x16x128_f8f6f4 v[132:135], v[4:11], v[186:193], v[132:135], v245, v245 op_sel_hi:[0,0,0]
	v_mfma_scale_f32_16x16x128_f8f6f4 v[120:123], v[12:19], v[208:215], v[120:123], v245, v245 op_sel_hi:[0,0,0]
	v_mfma_scale_f32_16x16x128_f8f6f4 v[116:119], v[4:11], v[208:215], v[116:119], v245, v245 op_sel_hi:[0,0,0]
	v_mfma_scale_f32_16x16x128_f8f6f4 v[104:107], v[12:19], v[216:223], v[104:107], v245, v245 op_sel_hi:[0,0,0]
	v_mfma_scale_f32_16x16x128_f8f6f4 v[100:103], v[4:11], v[216:223], v[100:103], v245, v245 op_sel_hi:[0,0,0]
	s_barrier
	s_add_i32 s72, s72, s17
	v_lshl_add_u64 v[174:175], s[58:59], 0, v[2:3]
	s_mov_b32 m0, s72
	ds_read_b128 v[186:189], v184 offset:16384
	ds_read_b128 v[190:193], v184 offset:17408
	ds_read_b128 v[208:211], v184 offset:18432
	ds_read_b128 v[212:215], v184 offset:19456
	ds_read_b128 v[216:219], v184 offset:20480
	ds_read_b128 v[220:223], v184 offset:21504
	ds_read_b128 v[228:231], v184 offset:22528
	ds_read_b128 v[232:235], v184 offset:23552
	global_load_lds_dwordx4 v[174:175], off
	s_add_i32 m0, s72, 0x2000
	s_add_u32 s74, s58, 0x20000
	v_lshl_add_u64 v[176:177], s[58:59], 0, v[164:165]
	s_addc_u32 s75, s59, 0
	s_add_i32 s72, s73, s17
	global_load_lds_dwordx4 v[176:177], off
	v_lshl_add_u64 v[178:179], s[74:75], 0, v[2:3]
	s_mov_b32 m0, s72
	v_lshl_add_u64 v[180:181], s[60:61], 0, v[166:167]
	global_load_lds_dwordx4 v[178:179], off
	v_lshl_add_u64 v[178:179], s[74:75], 0, v[164:165]
	s_add_i32 m0, s72, 0x2000
	s_nop 0
	global_load_lds_dwordx4 v[178:179], off
	v_lshl_add_u64 v[178:179], s[60:61], 0, v[168:169]
	s_mov_b32 m0, s18
	s_nop 0
	global_load_lds_dwordx4 v[178:179], off
	s_mov_b32 m0, s19
	s_nop 0
	global_load_lds_dwordx4 v[180:181], off
	s_cmp_eq_u32 s71, 0
	s_cbranch_scc1 .Lpg8skip15
	s_waitcnt vmcnt(8)
.Lpg8skip15:
	s_waitcnt lgkmcnt(0)
	s_barrier
	s_waitcnt lgkmcnt(0)
	v_mfma_scale_f32_16x16x128_f8f6f4 v[96:99], v[28:35], v[186:193], v[96:99], v245, v245 op_sel_hi:[0,0,0]
	v_mfma_scale_f32_16x16x128_f8f6f4 v[92:95], v[20:27], v[186:193], v[92:95], v245, v245 op_sel_hi:[0,0,0]
	v_mfma_scale_f32_16x16x128_f8f6f4 v[80:83], v[28:35], v[208:215], v[80:83], v245, v245 op_sel_hi:[0,0,0]
	v_mfma_scale_f32_16x16x128_f8f6f4 v[76:79], v[20:27], v[208:215], v[76:79], v245, v245 op_sel_hi:[0,0,0]
	v_mfma_scale_f32_16x16x128_f8f6f4 v[64:67], v[28:35], v[216:223], v[64:67], v245, v245 op_sel_hi:[0,0,0]
	v_mfma_scale_f32_16x16x128_f8f6f4 v[60:63], v[20:27], v[216:223], v[60:63], v245, v245 op_sel_hi:[0,0,0]
	v_mfma_scale_f32_16x16x128_f8f6f4 v[48:51], v[28:35], v[228:235], v[48:51], v245, v245 op_sel_hi:[0,0,0]
	v_mfma_scale_f32_16x16x128_f8f6f4 v[44:47], v[20:27], v[228:235], v[44:47], v245, v245 op_sel_hi:[0,0,0]
	v_mfma_scale_f32_16x16x128_f8f6f4 v[88:91], v[12:19], v[186:193], v[88:91], v245, v245 op_sel_hi:[0,0,0]
	v_mfma_scale_f32_16x16x128_f8f6f4 v[84:87], v[4:11], v[186:193], v[84:87], v245, v245 op_sel_hi:[0,0,0]
	v_mfma_scale_f32_16x16x128_f8f6f4 v[72:75], v[12:19], v[208:215], v[72:75], v245, v245 op_sel_hi:[0,0,0]
	v_mfma_scale_f32_16x16x128_f8f6f4 v[68:71], v[4:11], v[208:215], v[68:71], v245, v245 op_sel_hi:[0,0,0]
	v_mfma_scale_f32_16x16x128_f8f6f4 v[56:59], v[12:19], v[216:223], v[56:59], v245, v245 op_sel_hi:[0,0,0]
	v_mfma_scale_f32_16x16x128_f8f6f4 v[52:55], v[4:11], v[216:223], v[52:55], v245, v245 op_sel_hi:[0,0,0]
	v_mfma_scale_f32_16x16x128_f8f6f4 v[40:43], v[12:19], v[228:235], v[40:43], v245, v245 op_sel_hi:[0,0,0]
	v_mfma_scale_f32_16x16x128_f8f6f4 v[36:39], v[4:11], v[228:235], v[36:39], v245, v245 op_sel_hi:[0,0,0]
	s_barrier
	s_add_i32 s72, 0, 0x18000
	s_add_i32 s73, 0, 0x1c000
	v_add_u32_e32 v16, s72, v183
	v_add_u32_e32 v32, s73, v183
	ds_read_b128 v[4:7], v16
	ds_read_b128 v[8:11], v16 offset:1024
	ds_read_b128 v[12:15], v16 offset:2048
	ds_read_b128 v[16:19], v16 offset:3072
	ds_read_b128 v[20:23], v32
	ds_read_b128 v[24:27], v32 offset:1024
	ds_read_b128 v[28:31], v32 offset:2048
	ds_read_b128 v[32:35], v32 offset:3072
	s_add_u32 s60, s60, 0x20000
	s_addc_u32 s61, s61, 0
	s_mov_b32 m0, s20
	v_lshl_add_u64 v[194:195], s[60:61], 0, v[168:169]
	ds_read_b128 v[186:189], v184 offset:32768
	ds_read_b128 v[190:193], v184 offset:33792
	ds_read_b128 v[208:211], v184 offset:34816
	ds_read_b128 v[212:215], v184 offset:35840
	ds_read_b128 v[216:219], v184 offset:36864
	ds_read_b128 v[220:223], v184 offset:37888
	ds_read_b128 v[228:231], v184 offset:38912
	ds_read_b128 v[232:235], v184 offset:39936
	global_load_lds_dwordx4 v[194:195], off
	v_lshl_add_u64 v[194:195], s[60:61], 0, v[166:167]
	s_mov_b32 m0, s21
	s_nop 0
	global_load_lds_dwordx4 v[194:195], off
	s_waitcnt vmcnt(8)
	s_waitcnt lgkmcnt(0)
	s_barrier
; #define PG8_STAGE(bufoff, gbase, voff) do { _Pragma("unroll") for (int _i = 0; _i < 2; ++_i) \
;         __builtin_amdgcn_global_load_lds((const unsigned*)((const char*)(gbase) + (voff)[_i]), (PG8_LAS unsigned*)(lds + (bufoff) + ldsw + _i * 8192), 16, 0, 0); } while (0)
; #define PG8_LDA(dst, b, h) do { _Pragma("unroll") for (int m = 0; m < 4; ++m) _Pragma("unroll") for (int k = 0; k < 2; ++k) dst[m][k] = *(const PG8_LAS bf16x8*)(lds + PG8_SA(b, h) + aoff + m * 2048 + k * 1024); } while (0)
; #define PG8_WAIT_V(n) asm volatile("s_waitcnt vmcnt(" #n ")" ::: "memory")
; #define PG8_WAIT_L(n) asm volatile("s_waitcnt lgkmcnt(" #n ")" ::: "memory")
; #define PG8_BAR __builtin_amdgcn_s_barrier()
; #define PG8_SCHED __builtin_amdgcn_sched_barrier(0)
; template <class Epi, class Sched, bool ALIGN_EPI = false, bool SP2 = false, bool FP8 = false, bool ABLK = false>
; __device__ __forceinline__ void gemm_phase(PG8_LAS unsigned char* lds, const Gemm g, const Sched& S, const Epi& E) {
;     ...
;             PG8_WAIT_V(8); PG8_WAIT_L(0); PG8_BAR; PG8_MMA(0, 0, At, B0); PG8_MMA(0, 1, At, B1); PG8_BAR; PG8_SCHED;
;             PG8_LDA(At, 1, 1); PG8_STAGE(PG8_SB(1, 0), b3, voffB); PG8_STAGE(PG8_SB(1, 1), b3 + hstep, voffB); PG8_STAGE(PG8_SA(1, 0), a3, voffA);
;             PG8_WAIT_V(8); PG8_WAIT_L(0); PG8_BAR; PG8_MMA(1, 0, At, B0); PG8_MMA(1, 1, At, B1); PG8_BAR; PG8_SCHED;
;     ...
;         if constexpr (SP2) PG8_WAIT_V(0);
;         if constexpr (FP8) asm volatile("s_nop 15\n\ts_nop 15" ::: "memory");
;         if constexpr (ALIGN_EPI) { if (wr == 0) PG8_BAR; }
	s_waitcnt lgkmcnt(0)
	v_mfma_scale_f32_16x16x128_f8f6f4 v[160:163], v[4:11], v[186:193], v[160:163], v245, v245 op_sel_hi:[0,0,0]
	v_mfma_scale_f32_16x16x128_f8f6f4 v[156:159], v[12:19], v[186:193], v[156:159], v245, v245 op_sel_hi:[0,0,0]
	v_mfma_scale_f32_16x16x128_f8f6f4 v[144:147], v[4:11], v[208:215], v[144:147], v245, v245 op_sel_hi:[0,0,0]
	v_mfma_scale_f32_16x16x128_f8f6f4 v[140:143], v[12:19], v[208:215], v[140:143], v245, v245 op_sel_hi:[0,0,0]
	v_mfma_scale_f32_16x16x128_f8f6f4 v[128:131], v[4:11], v[216:223], v[128:131], v245, v245 op_sel_hi:[0,0,0]
	v_mfma_scale_f32_16x16x128_f8f6f4 v[124:127], v[12:19], v[216:223], v[124:127], v245, v245 op_sel_hi:[0,0,0]
	v_mfma_scale_f32_16x16x128_f8f6f4 v[112:115], v[4:11], v[228:235], v[112:115], v245, v245 op_sel_hi:[0,0,0]
	v_mfma_scale_f32_16x16x128_f8f6f4 v[108:111], v[12:19], v[228:235], v[108:111], v245, v245 op_sel_hi:[0,0,0]
	v_mfma_scale_f32_16x16x128_f8f6f4 v[152:155], v[20:27], v[186:193], v[152:155], v245, v245 op_sel_hi:[0,0,0]
	v_mfma_scale_f32_16x16x128_f8f6f4 v[148:151], v[28:35], v[186:193], v[148:151], v245, v245 op_sel_hi:[0,0,0]
	v_mfma_scale_f32_16x16x128_f8f6f4 v[136:139], v[20:27], v[208:215], v[136:139], v245, v245 op_sel_hi:[0,0,0]
	v_mfma_scale_f32_16x16x128_f8f6f4 v[132:135], v[28:35], v[208:215], v[132:135], v245, v245 op_sel_hi:[0,0,0]
	v_mfma_scale_f32_16x16x128_f8f6f4 v[120:123], v[20:27], v[216:223], v[120:123], v245, v245 op_sel_hi:[0,0,0]
	v_mfma_scale_f32_16x16x128_f8f6f4 v[116:119], v[28:35], v[216:223], v[116:119], v245, v245 op_sel_hi:[0,0,0]
	v_mfma_scale_f32_16x16x128_f8f6f4 v[104:107], v[20:27], v[228:235], v[104:107], v245, v245 op_sel_hi:[0,0,0]
	v_mfma_scale_f32_16x16x128_f8f6f4 v[100:103], v[28:35], v[228:235], v[100:103], v245, v245 op_sel_hi:[0,0,0]
	s_barrier
	s_add_i32 s60, s72, s17
	v_lshl_add_u64 v[174:175], v[174:175], 0, s[34:35]
	s_mov_b32 m0, s60
	ds_read_b128 v[186:189], v184 offset:49152
	ds_read_b128 v[190:193], v184 offset:50176
	ds_read_b128 v[208:211], v184 offset:51200
	ds_read_b128 v[212:215], v184 offset:52224
	ds_read_b128 v[216:219], v184 offset:53248
	ds_read_b128 v[220:223], v184 offset:54272
	ds_read_b128 v[228:231], v184 offset:55296
	ds_read_b128 v[232:235], v184 offset:56320
	global_load_lds_dwordx4 v[174:175], off
	s_add_i32 m0, s60, 0x2000
	s_add_u32 s58, s58, 0x20080
	v_lshl_add_u64 v[174:175], v[176:177], 0, s[34:35]
	s_addc_u32 s59, s59, 0
	s_add_i32 s60, s73, s17
	global_load_lds_dwordx4 v[174:175], off
	v_lshl_add_u64 v[174:175], s[58:59], 0, v[2:3]
	s_mov_b32 m0, s60
	s_nop 0
	global_load_lds_dwordx4 v[174:175], off
	v_lshl_add_u64 v[174:175], s[58:59], 0, v[164:165]
	s_add_i32 m0, s60, 0x2000
	s_nop 0
	global_load_lds_dwordx4 v[174:175], off
	v_lshl_add_u64 v[174:175], v[178:179], 0, s[34:35]
	s_mov_b32 m0, s63
	s_nop 0
	global_load_lds_dwordx4 v[174:175], off
	v_lshl_add_u64 v[174:175], v[180:181], 0, s[34:35]
	s_mov_b32 m0, s64
	s_nop 0
	global_load_lds_dwordx4 v[174:175], off
	s_waitcnt vmcnt(8)
	s_waitcnt lgkmcnt(0)
	s_barrier
	s_waitcnt lgkmcnt(0)
	v_mfma_scale_f32_16x16x128_f8f6f4 v[96:99], v[4:11], v[186:193], v[96:99], v245, v245 op_sel_hi:[0,0,0]
	v_mfma_scale_f32_16x16x128_f8f6f4 v[92:95], v[12:19], v[186:193], v[92:95], v245, v245 op_sel_hi:[0,0,0]
	v_mfma_scale_f32_16x16x128_f8f6f4 v[80:83], v[4:11], v[208:215], v[80:83], v245, v245 op_sel_hi:[0,0,0]
	v_mfma_scale_f32_16x16x128_f8f6f4 v[76:79], v[12:19], v[208:215], v[76:79], v245, v245 op_sel_hi:[0,0,0]
	v_mfma_scale_f32_16x16x128_f8f6f4 v[64:67], v[4:11], v[216:223], v[64:67], v245, v245 op_sel_hi:[0,0,0]
	v_mfma_scale_f32_16x16x128_f8f6f4 v[60:63], v[12:19], v[216:223], v[60:63], v245, v245 op_sel_hi:[0,0,0]
	v_mfma_scale_f32_16x16x128_f8f6f4 v[48:51], v[4:11], v[228:235], v[48:51], v245, v245 op_sel_hi:[0,0,0]
	v_mfma_scale_f32_16x16x128_f8f6f4 v[44:47], v[12:19], v[228:235], v[44:47], v245, v245 op_sel_hi:[0,0,0]
	v_mfma_scale_f32_16x16x128_f8f6f4 v[88:91], v[20:27], v[186:193], v[88:91], v245, v245 op_sel_hi:[0,0,0]
	v_mfma_scale_f32_16x16x128_f8f6f4 v[84:87], v[28:35], v[186:193], v[84:87], v245, v245 op_sel_hi:[0,0,0]
	v_mfma_scale_f32_16x16x128_f8f6f4 v[72:75], v[20:27], v[208:215], v[72:75], v245, v245 op_sel_hi:[0,0,0]
	v_mfma_scale_f32_16x16x128_f8f6f4 v[68:71], v[28:35], v[208:215], v[68:71], v245, v245 op_sel_hi:[0,0,0]
	v_mfma_scale_f32_16x16x128_f8f6f4 v[56:59], v[20:27], v[216:223], v[56:59], v245, v245 op_sel_hi:[0,0,0]
	v_mfma_scale_f32_16x16x128_f8f6f4 v[52:55], v[28:35], v[216:223], v[52:55], v245, v245 op_sel_hi:[0,0,0]
	v_mfma_scale_f32_16x16x128_f8f6f4 v[40:43], v[20:27], v[228:235], v[40:43], v245, v245 op_sel_hi:[0,0,0]
	v_mfma_scale_f32_16x16x128_f8f6f4 v[36:39], v[28:35], v[228:235], v[36:39], v245, v245 op_sel_hi:[0,0,0]
	s_barrier
	s_add_u32 s56, s56, 0x100
	s_addc_u32 s57, s57, 0
	s_add_u32 s69, s69, 0x100
	s_addc_u32 s70, s70, 0
	s_cmp_gt_u32 s71, 5
	s_mov_b32 s58, s71
	s_cbranch_scc0 .LBB0_1689
	s_waitcnt vmcnt(0)
	s_nop 15
	s_nop 15
	s_and_b64 vcc, exec, s[46:47]
	s_cbranch_vccz .LBB0_1692
	s_barrier

; #define PG8_STAGE(bufoff, gbase, voff) do { _Pragma("unroll") for (int _i = 0; _i < 2; ++_i) \
;         __builtin_amdgcn_global_load_lds((const unsigned*)((const char*)(gbase) + (voff)[_i]), (PG8_LAS unsigned*)(lds + (bufoff) + ldsw + _i * 8192), 16, 0, 0); } while (0)
; #define PG8_LDA(dst, b, h) do { _Pragma("unroll") for (int m = 0; m < 4; ++m) _Pragma("unroll") for (int k = 0; k < 2; ++k) dst[m][k] = *(const PG8_LAS bf16x8*)(lds + PG8_SA(b, h) + aoff + m * 2048 + k * 1024); } while (0)
; #define PG8_WAIT_V8_UNLESS_FIRST(t) asm volatile("s_cmp_eq_u32 %0, 0\n\ts_cbranch_scc1 .Lpg8skip%=\n\ts_waitcnt vmcnt(8)\n.Lpg8skip%=:" :: "s"(t) : "scc", "memory")
; #define PG8_WAIT_L(n) asm volatile("s_waitcnt lgkmcnt(" #n ")" ::: "memory")
; #define PG8_BAR __builtin_amdgcn_s_barrier()
; #define PG8_SCHED __builtin_amdgcn_sched_barrier(0)
; template <class Epi, class Sched, bool ALIGN_EPI = false, bool SP2 = false, bool FP8 = false, bool ABLK = false>
; __device__ __forceinline__ void gemm_phase(PG8_LAS unsigned char* lds, const Gemm g, const Sched& S, const Epi& E) {
;     ...
;             PG8_WAIT_V8_UNLESS_FIRST(t); PG8_WAIT_L(0); PG8_BAR; PG8_MMA(0, 0, At, B0); PG8_MMA(0, 1, At, B1); PG8_BAR; PG8_SCHED;
;             PG8_LDA(At, 0, 1); PG8_STAGE(PG8_SB(0, 0), b2, voffB); PG8_STAGE(PG8_SB(0, 1), b2 + hstep, voffB); PG8_STAGE(PG8_SA(0, 0), a2, voffA);
;             PG8_WAIT_V8_UNLESS_FIRST(t); PG8_WAIT_L(0); PG8_BAR; PG8_MMA(1, 0, At, B0); PG8_MMA(1, 1, At, B1); PG8_BAR; PG8_SCHED;
.Lpg8skip16:
	s_waitcnt lgkmcnt(0)
	s_barrier
	s_waitcnt lgkmcnt(0)
	v_mfma_f32_16x16x32_bf16 v[132:135], v[124:127], v[180:183], v[132:135]
	v_mfma_f32_16x16x32_bf16 v[128:131], v[140:143], v[180:183], v[128:131]
	v_mfma_f32_16x16x32_bf16 v[112:115], v[124:127], v[188:191], v[112:115]
	v_mfma_f32_16x16x32_bf16 v[104:107], v[140:143], v[188:191], v[104:107]
	v_mfma_f32_16x16x32_bf16 v[96:99], v[124:127], v[208:211], v[96:99]
	v_mfma_f32_16x16x32_bf16 v[88:91], v[140:143], v[208:211], v[88:91]
	v_mfma_f32_16x16x32_bf16 v[80:83], v[124:127], v[216:219], v[80:83]
	v_mfma_f32_16x16x32_bf16 v[72:75], v[140:143], v[216:219], v[72:75]
	v_mfma_f32_16x16x32_bf16 v[132:135], v[136:139], v[184:187], v[132:135]
	v_mfma_f32_16x16x32_bf16 v[128:131], v[144:147], v[184:187], v[128:131]
	v_mfma_f32_16x16x32_bf16 v[112:115], v[136:139], v[192:195], v[112:115]
	v_mfma_f32_16x16x32_bf16 v[104:107], v[144:147], v[192:195], v[104:107]
	v_mfma_f32_16x16x32_bf16 v[96:99], v[136:139], v[212:215], v[96:99]
	v_mfma_f32_16x16x32_bf16 v[88:91], v[144:147], v[212:215], v[88:91]
	v_mfma_f32_16x16x32_bf16 v[80:83], v[136:139], v[220:223], v[80:83]
	v_mfma_f32_16x16x32_bf16 v[72:75], v[144:147], v[220:223], v[72:75]
	v_mfma_f32_16x16x32_bf16 v[120:123], v[148:151], v[180:183], v[120:123]
	v_mfma_f32_16x16x32_bf16 v[116:119], v[172:175], v[180:183], v[116:119]
	v_mfma_f32_16x16x32_bf16 v[108:111], v[148:151], v[188:191], v[108:111]
	v_mfma_f32_16x16x32_bf16 v[100:103], v[172:175], v[188:191], v[100:103]
	v_mfma_f32_16x16x32_bf16 v[92:95], v[148:151], v[208:211], v[92:95]
	v_mfma_f32_16x16x32_bf16 v[84:87], v[172:175], v[208:211], v[84:87]
	v_mfma_f32_16x16x32_bf16 v[76:79], v[148:151], v[216:219], v[76:79]
	v_mfma_f32_16x16x32_bf16 v[68:71], v[172:175], v[216:219], v[68:71]
	v_mfma_f32_16x16x32_bf16 v[120:123], v[152:155], v[184:187], v[120:123]
	v_mfma_f32_16x16x32_bf16 v[116:119], v[176:179], v[184:187], v[116:119]
	v_mfma_f32_16x16x32_bf16 v[108:111], v[152:155], v[192:195], v[108:111]
	v_mfma_f32_16x16x32_bf16 v[100:103], v[176:179], v[192:195], v[100:103]
	v_mfma_f32_16x16x32_bf16 v[92:95], v[152:155], v[212:215], v[92:95]
	v_mfma_f32_16x16x32_bf16 v[84:87], v[176:179], v[212:215], v[84:87]
	v_mfma_f32_16x16x32_bf16 v[76:79], v[152:155], v[220:223], v[76:79]
	v_mfma_f32_16x16x32_bf16 v[68:71], v[176:179], v[220:223], v[68:71]
	s_barrier
	s_add_i32 s74, s74, s19
	v_lshl_add_u64 v[166:167], s[60:61], 0, v[2:3]
	s_mov_b32 m0, s74
	ds_read_b128 v[180:183], v170 offset:16384
	ds_read_b128 v[184:187], v170 offset:17408
	ds_read_b128 v[188:191], v170 offset:18432
	ds_read_b128 v[192:195], v170 offset:19456
	ds_read_b128 v[208:211], v170 offset:20480
	ds_read_b128 v[212:215], v170 offset:21504
	ds_read_b128 v[216:219], v170 offset:22528
	ds_read_b128 v[220:223], v170 offset:23552
	global_load_lds_dwordx4 v[166:167], off
	s_add_i32 m0, s74, 0x2000
	s_add_u32 s74, s60, 0x40000
	v_lshl_add_u64 v[204:205], s[60:61], 0, v[156:157]
	s_addc_u32 s75, s61, 0
	s_add_i32 s76, s76, s19
	global_load_lds_dwordx4 v[204:205], off
	v_lshl_add_u64 v[206:207], s[74:75], 0, v[2:3]
	s_mov_b32 m0, s76
	v_lshl_add_u64 v[224:225], s[62:63], 0, v[158:159]
	global_load_lds_dwordx4 v[206:207], off
	v_lshl_add_u64 v[206:207], s[74:75], 0, v[156:157]
	s_add_i32 m0, s76, 0x2000
	s_nop 0
	global_load_lds_dwordx4 v[206:207], off
	v_lshl_add_u64 v[206:207], s[62:63], 0, v[160:161]
	s_mov_b32 m0, s20
	s_nop 0
	global_load_lds_dwordx4 v[206:207], off
	s_mov_b32 m0, s21
	s_nop 0
	global_load_lds_dwordx4 v[224:225], off
	s_cmp_eq_u32 s73, 0
	s_cbranch_scc1 .Lpg8skip17
	s_waitcnt vmcnt(8)
.Lpg8skip17:
	s_waitcnt lgkmcnt(0)
	s_barrier
	s_waitcnt lgkmcnt(0)
	v_mfma_f32_16x16x32_bf16 v[64:67], v[124:127], v[180:183], v[64:67]
	v_mfma_f32_16x16x32_bf16 v[56:59], v[140:143], v[180:183], v[56:59]
	v_mfma_f32_16x16x32_bf16 v[48:51], v[124:127], v[188:191], v[48:51]
	v_mfma_f32_16x16x32_bf16 v[40:43], v[140:143], v[188:191], v[40:43]
	v_mfma_f32_16x16x32_bf16 v[32:35], v[124:127], v[208:211], v[32:35]
	v_mfma_f32_16x16x32_bf16 v[24:27], v[140:143], v[208:211], v[24:27]
	v_mfma_f32_16x16x32_bf16 v[16:19], v[124:127], v[216:219], v[16:19]
	v_mfma_f32_16x16x32_bf16 v[8:11], v[140:143], v[216:219], v[8:11]
	v_mfma_f32_16x16x32_bf16 v[64:67], v[136:139], v[184:187], v[64:67]
	v_mfma_f32_16x16x32_bf16 v[56:59], v[144:147], v[184:187], v[56:59]
	v_mfma_f32_16x16x32_bf16 v[48:51], v[136:139], v[192:195], v[48:51]
	v_mfma_f32_16x16x32_bf16 v[40:43], v[144:147], v[192:195], v[40:43]
	v_mfma_f32_16x16x32_bf16 v[32:35], v[136:139], v[212:215], v[32:35]
	v_mfma_f32_16x16x32_bf16 v[24:27], v[144:147], v[212:215], v[24:27]
	v_mfma_f32_16x16x32_bf16 v[16:19], v[136:139], v[220:223], v[16:19]
	v_mfma_f32_16x16x32_bf16 v[8:11], v[144:147], v[220:223], v[8:11]
	v_mfma_f32_16x16x32_bf16 v[60:63], v[148:151], v[180:183], v[60:63]
	v_mfma_f32_16x16x32_bf16 v[52:55], v[172:175], v[180:183], v[52:55]
	v_mfma_f32_16x16x32_bf16 v[44:47], v[148:151], v[188:191], v[44:47]
	v_mfma_f32_16x16x32_bf16 v[36:39], v[172:175], v[188:191], v[36:39]
	v_mfma_f32_16x16x32_bf16 v[28:31], v[148:151], v[208:211], v[28:31]
	v_mfma_f32_16x16x32_bf16 v[20:23], v[172:175], v[208:211], v[20:23]
	v_mfma_f32_16x16x32_bf16 v[12:15], v[148:151], v[216:219], v[12:15]
	v_mfma_f32_16x16x32_bf16 v[4:7], v[172:175], v[216:219], v[4:7]
	v_mfma_f32_16x16x32_bf16 v[60:63], v[152:155], v[184:187], v[60:63]
	v_mfma_f32_16x16x32_bf16 v[52:55], v[176:179], v[184:187], v[52:55]
	v_mfma_f32_16x16x32_bf16 v[44:47], v[152:155], v[192:195], v[44:47]
	v_mfma_f32_16x16x32_bf16 v[36:39], v[176:179], v[192:195], v[36:39]
	v_mfma_f32_16x16x32_bf16 v[28:31], v[152:155], v[212:215], v[28:31]
	v_mfma_f32_16x16x32_bf16 v[20:23], v[176:179], v[212:215], v[20:23]
	v_mfma_f32_16x16x32_bf16 v[12:15], v[152:155], v[220:223], v[12:15]
	v_mfma_f32_16x16x32_bf16 v[4:7], v[176:179], v[220:223], v[4:7]
	s_barrier
; #define PG8_STAGE(bufoff, gbase, voff) do { _Pragma("unroll") for (int _i = 0; _i < 2; ++_i) \
;         __builtin_amdgcn_global_load_lds((const unsigned*)((const char*)(gbase) + (voff)[_i]), (PG8_LAS unsigned*)(lds + (bufoff) + ldsw + _i * 8192), 16, 0, 0); } while (0)
; #define PG8_LDA(dst, b, h) do { _Pragma("unroll") for (int m = 0; m < 4; ++m) _Pragma("unroll") for (int k = 0; k < 2; ++k) dst[m][k] = *(const PG8_LAS bf16x8*)(lds + PG8_SA(b, h) + aoff + m * 2048 + k * 1024); } while (0)
; #define PG8_LDB(dst, b, h) do { _Pragma("unroll") for (int n = 0; n < 2; ++n) _Pragma("unroll") for (int k = 0; k < 2; ++k) dst[n][k] = *(const PG8_LAS bf16x8*)(lds + PG8_SB(b, h) + boff + n * 2048 + k * 1024); } while (0)
; #define PG8_WAIT_V(n) asm volatile("s_waitcnt vmcnt(" #n ")" ::: "memory")
; #define PG8_WAIT_L(n) asm volatile("s_waitcnt lgkmcnt(" #n ")" ::: "memory")
; #define PG8_BAR __builtin_amdgcn_s_barrier()
; #define PG8_SCHED __builtin_amdgcn_sched_barrier(0)
; template <class Epi, class Sched, bool ALIGN_EPI = false, bool SP2 = false, bool FP8 = false, bool ABLK = false>
; __device__ __forceinline__ void gemm_phase(PG8_LAS unsigned char* lds, const Gemm g, const Sched& S, const Epi& E) {
;     ...
;             PG8_LDB(B0, 1, 0); PG8_LDB(B1, 1, 1); PG8_SCHED; PG8_LDA(At, 1, 0); PG8_STAGE(PG8_SA(0, 1), a2 + hstepA, voffA);
;             PG8_WAIT_V(8); PG8_WAIT_L(0); PG8_BAR; PG8_MMA(0, 0, At, B0); PG8_MMA(0, 1, At, B1); PG8_BAR; PG8_SCHED;
	s_add_i32 s74, 0, 0x18000
	s_add_i32 s75, 0, 0x1c000
	v_add_u32_e32 v144, s74, v169
	v_add_u32_e32 v171, s75, v169
	ds_read_b128 v[124:127], v144
	ds_read_b128 v[136:139], v144 offset:1024
	ds_read_b128 v[140:143], v144 offset:2048
	ds_read_b128 v[144:147], v144 offset:3072
	ds_read_b128 v[148:151], v171
	ds_read_b128 v[152:155], v171 offset:1024
	ds_read_b128 v[172:175], v171 offset:2048
	ds_read_b128 v[176:179], v171 offset:3072
	s_add_u32 s62, s62, 0x40000
	s_addc_u32 s63, s63, 0
	s_mov_b32 m0, s22
	v_lshl_add_u64 v[228:229], s[62:63], 0, v[160:161]
	ds_read_b128 v[180:183], v170 offset:32768
	ds_read_b128 v[184:187], v170 offset:33792
	ds_read_b128 v[188:191], v170 offset:34816
	ds_read_b128 v[192:195], v170 offset:35840
	ds_read_b128 v[208:211], v170 offset:36864
	ds_read_b128 v[212:215], v170 offset:37888
	ds_read_b128 v[216:219], v170 offset:38912
	ds_read_b128 v[220:223], v170 offset:39936
	global_load_lds_dwordx4 v[228:229], off
	v_lshl_add_u64 v[228:229], s[62:63], 0, v[158:159]
	s_mov_b32 m0, s23
	s_nop 0
	global_load_lds_dwordx4 v[228:229], off
	s_waitcnt vmcnt(8)
	s_waitcnt lgkmcnt(0)
	s_barrier
	s_waitcnt lgkmcnt(0)
	v_mfma_f32_16x16x32_bf16 v[132:135], v[124:127], v[180:183], v[132:135]
	v_mfma_f32_16x16x32_bf16 v[128:131], v[140:143], v[180:183], v[128:131]
	v_mfma_f32_16x16x32_bf16 v[112:115], v[124:127], v[188:191], v[112:115]
	v_mfma_f32_16x16x32_bf16 v[104:107], v[140:143], v[188:191], v[104:107]
	v_mfma_f32_16x16x32_bf16 v[96:99], v[124:127], v[208:211], v[96:99]
	v_mfma_f32_16x16x32_bf16 v[88:91], v[140:143], v[208:211], v[88:91]
	v_mfma_f32_16x16x32_bf16 v[80:83], v[124:127], v[216:219], v[80:83]
	v_mfma_f32_16x16x32_bf16 v[72:75], v[140:143], v[216:219], v[72:75]
	v_mfma_f32_16x16x32_bf16 v[132:135], v[136:139], v[184:187], v[132:135]
	v_mfma_f32_16x16x32_bf16 v[128:131], v[144:147], v[184:187], v[128:131]
	v_mfma_f32_16x16x32_bf16 v[112:115], v[136:139], v[192:195], v[112:115]
	v_mfma_f32_16x16x32_bf16 v[104:107], v[144:147], v[192:195], v[104:107]
	v_mfma_f32_16x16x32_bf16 v[96:99], v[136:139], v[212:215], v[96:99]
	v_mfma_f32_16x16x32_bf16 v[88:91], v[144:147], v[212:215], v[88:91]
	v_mfma_f32_16x16x32_bf16 v[80:83], v[136:139], v[220:223], v[80:83]
	v_mfma_f32_16x16x32_bf16 v[72:75], v[144:147], v[220:223], v[72:75]
	v_mfma_f32_16x16x32_bf16 v[120:123], v[148:151], v[180:183], v[120:123]
	v_mfma_f32_16x16x32_bf16 v[116:119], v[172:175], v[180:183], v[116:119]
	v_mfma_f32_16x16x32_bf16 v[108:111], v[148:151], v[188:191], v[108:111]
	v_mfma_f32_16x16x32_bf16 v[100:103], v[172:175], v[188:191], v[100:103]
	v_mfma_f32_16x16x32_bf16 v[92:95], v[148:151], v[208:211], v[92:95]
	v_mfma_f32_16x16x32_bf16 v[84:87], v[172:175], v[208:211], v[84:87]
	v_mfma_f32_16x16x32_bf16 v[76:79], v[148:151], v[216:219], v[76:79]
	v_mfma_f32_16x16x32_bf16 v[68:71], v[172:175], v[216:219], v[68:71]
	v_mfma_f32_16x16x32_bf16 v[120:123], v[152:155], v[184:187], v[120:123]
	v_mfma_f32_16x16x32_bf16 v[116:119], v[176:179], v[184:187], v[116:119]
	v_mfma_f32_16x16x32_bf16 v[108:111], v[152:155], v[192:195], v[108:111]
	v_mfma_f32_16x16x32_bf16 v[100:103], v[176:179], v[192:195], v[100:103]
	v_mfma_f32_16x16x32_bf16 v[92:95], v[152:155], v[212:215], v[92:95]
	v_mfma_f32_16x16x32_bf16 v[84:87], v[176:179], v[212:215], v[84:87]
	v_mfma_f32_16x16x32_bf16 v[76:79], v[152:155], v[220:223], v[76:79]
	v_mfma_f32_16x16x32_bf16 v[68:71], v[176:179], v[220:223], v[68:71]
	s_barrier
; #define PG8_STAGE(bufoff, gbase, voff) do { _Pragma("unroll") for (int _i = 0; _i < 2; ++_i) \
;         __builtin_amdgcn_global_load_lds((const unsigned*)((const char*)(gbase) + (voff)[_i]), (PG8_LAS unsigned*)(lds + (bufoff) + ldsw + _i * 8192), 16, 0, 0); } while (0)
; #define PG8_LDA(dst, b, h) do { _Pragma("unroll") for (int m = 0; m < 4; ++m) _Pragma("unroll") for (int k = 0; k < 2; ++k) dst[m][k] = *(const PG8_LAS bf16x8*)(lds + PG8_SA(b, h) + aoff + m * 2048 + k * 1024); } while (0)
; #define PG8_WAIT_V(n) asm volatile("s_waitcnt vmcnt(" #n ")" ::: "memory")
; #define PG8_WAIT_L(n) asm volatile("s_waitcnt lgkmcnt(" #n ")" ::: "memory")
; #define PG8_BAR __builtin_amdgcn_s_barrier()
; #define PG8_SCHED __builtin_amdgcn_sched_barrier(0)
; template <class Epi, class Sched, bool ALIGN_EPI = false, bool SP2 = false, bool FP8 = false, bool ABLK = false>
; __device__ __forceinline__ void gemm_phase(PG8_LAS unsigned char* lds, const Gemm g, const Sched& S, const Epi& E) {
;     ...
;             PG8_LDA(At, 1, 1); PG8_STAGE(PG8_SB(1, 0), b3, voffB); PG8_STAGE(PG8_SB(1, 1), b3 + hstep, voffB); PG8_STAGE(PG8_SA(1, 0), a3, voffA);
;             PG8_WAIT_V(8); PG8_WAIT_L(0); PG8_BAR; PG8_MMA(1, 0, At, B0); PG8_MMA(1, 1, At, B1); PG8_BAR; PG8_SCHED;
;     ...
;         if constexpr (SP2) PG8_WAIT_V(0);
;         if constexpr (FP8) asm volatile("s_nop 15\n\ts_nop 15" ::: "memory");
;         if constexpr (ALIGN_EPI) { if (wr == 0) PG8_BAR; }
	s_add_i32 s62, s74, s19
	v_lshl_add_u64 v[166:167], v[166:167], 0, s[34:35]
	s_mov_b32 m0, s62
	ds_read_b128 v[180:183], v170 offset:49152
	ds_read_b128 v[184:187], v170 offset:50176
	ds_read_b128 v[188:191], v170 offset:51200
	ds_read_b128 v[192:195], v170 offset:52224
	ds_read_b128 v[208:211], v170 offset:53248
	ds_read_b128 v[212:215], v170 offset:54272
	ds_read_b128 v[216:219], v170 offset:55296
	ds_read_b128 v[220:223], v170 offset:56320
	global_load_lds_dwordx4 v[166:167], off
	s_add_i32 m0, s62, 0x2000
	s_add_u32 s60, s60, 0x40080
	v_lshl_add_u64 v[166:167], v[204:205], 0, s[34:35]
	s_addc_u32 s61, s61, 0
	s_add_i32 s62, s75, s19
	global_load_lds_dwordx4 v[166:167], off
	v_lshl_add_u64 v[166:167], s[60:61], 0, v[2:3]
	s_mov_b32 m0, s62
	s_nop 0
	global_load_lds_dwordx4 v[166:167], off
	v_lshl_add_u64 v[166:167], s[60:61], 0, v[156:157]
	s_add_i32 m0, s62, 0x2000
	s_nop 0
	global_load_lds_dwordx4 v[166:167], off
	v_lshl_add_u64 v[166:167], v[206:207], 0, s[34:35]
	s_mov_b32 m0, s65
	s_nop 0
	global_load_lds_dwordx4 v[166:167], off
	v_lshl_add_u64 v[166:167], v[224:225], 0, s[34:35]
	s_mov_b32 m0, s66
	s_nop 0
	global_load_lds_dwordx4 v[166:167], off
	s_waitcnt vmcnt(8)
	s_waitcnt lgkmcnt(0)
	s_barrier
	s_waitcnt lgkmcnt(0)
	v_mfma_f32_16x16x32_bf16 v[64:67], v[124:127], v[180:183], v[64:67]
	v_mfma_f32_16x16x32_bf16 v[56:59], v[140:143], v[180:183], v[56:59]
	v_mfma_f32_16x16x32_bf16 v[48:51], v[124:127], v[188:191], v[48:51]
	v_mfma_f32_16x16x32_bf16 v[40:43], v[140:143], v[188:191], v[40:43]
	v_mfma_f32_16x16x32_bf16 v[32:35], v[124:127], v[208:211], v[32:35]
	v_mfma_f32_16x16x32_bf16 v[24:27], v[140:143], v[208:211], v[24:27]
	v_mfma_f32_16x16x32_bf16 v[16:19], v[124:127], v[216:219], v[16:19]
	v_mfma_f32_16x16x32_bf16 v[8:11], v[140:143], v[216:219], v[8:11]
	v_mfma_f32_16x16x32_bf16 v[64:67], v[136:139], v[184:187], v[64:67]
	v_mfma_f32_16x16x32_bf16 v[56:59], v[144:147], v[184:187], v[56:59]
	v_mfma_f32_16x16x32_bf16 v[48:51], v[136:139], v[192:195], v[48:51]
	v_mfma_f32_16x16x32_bf16 v[40:43], v[144:147], v[192:195], v[40:43]
	v_mfma_f32_16x16x32_bf16 v[32:35], v[136:139], v[212:215], v[32:35]
	v_mfma_f32_16x16x32_bf16 v[24:27], v[144:147], v[212:215], v[24:27]
	v_mfma_f32_16x16x32_bf16 v[16:19], v[136:139], v[220:223], v[16:19]
	v_mfma_f32_16x16x32_bf16 v[8:11], v[144:147], v[220:223], v[8:11]
	v_mfma_f32_16x16x32_bf16 v[60:63], v[148:151], v[180:183], v[60:63]
	v_mfma_f32_16x16x32_bf16 v[52:55], v[172:175], v[180:183], v[52:55]
	v_mfma_f32_16x16x32_bf16 v[44:47], v[148:151], v[188:191], v[44:47]
	v_mfma_f32_16x16x32_bf16 v[36:39], v[172:175], v[188:191], v[36:39]
	v_mfma_f32_16x16x32_bf16 v[28:31], v[148:151], v[208:211], v[28:31]
	v_mfma_f32_16x16x32_bf16 v[20:23], v[172:175], v[208:211], v[20:23]
	v_mfma_f32_16x16x32_bf16 v[12:15], v[148:151], v[216:219], v[12:15]
	v_mfma_f32_16x16x32_bf16 v[4:7], v[172:175], v[216:219], v[4:7]
	v_mfma_f32_16x16x32_bf16 v[60:63], v[152:155], v[184:187], v[60:63]
	v_mfma_f32_16x16x32_bf16 v[52:55], v[176:179], v[184:187], v[52:55]
	v_mfma_f32_16x16x32_bf16 v[44:47], v[152:155], v[192:195], v[44:47]
	v_mfma_f32_16x16x32_bf16 v[36:39], v[176:179], v[192:195], v[36:39]
	v_mfma_f32_16x16x32_bf16 v[28:31], v[152:155], v[212:215], v[28:31]
	v_mfma_f32_16x16x32_bf16 v[20:23], v[176:179], v[212:215], v[20:23]
	v_mfma_f32_16x16x32_bf16 v[12:15], v[152:155], v[220:223], v[12:15]
	v_mfma_f32_16x16x32_bf16 v[4:7], v[176:179], v[220:223], v[4:7]
	s_barrier
	s_add_u32 s58, s58, 0x100
	s_addc_u32 s59, s59, 0
	s_add_u32 s71, s71, 0x100
	s_addc_u32 s72, s72, 0
	s_cmp_gt_u32 s73, 13
	s_mov_b32 s60, s73
	s_cbranch_scc0 .LBB0_1709
	s_waitcnt vmcnt(0)
	s_and_b64 vcc, exec, s[48:49]
	s_cbranch_vccz .LBB0_1712
	s_barrier

; #define PG8_STAGE(bufoff, gbase, voff) do { _Pragma("unroll") for (int _i = 0; _i < 2; ++_i) \
;         __builtin_amdgcn_global_load_lds((const unsigned*)((const char*)(gbase) + (voff)[_i]), (PG8_LAS unsigned*)(lds + (bufoff) + ldsw + _i * 8192), 16, 0, 0); } while (0)
; #define PG8_LDA(dst, b, h) do { _Pragma("unroll") for (int m = 0; m < 4; ++m) _Pragma("unroll") for (int k = 0; k < 2; ++k) dst[m][k] = *(const PG8_LAS bf16x8*)(lds + PG8_SA(b, h) + aoff + m * 2048 + k * 1024); } while (0)
; #define PG8_LDB(dst, b, h) do { _Pragma("unroll") for (int n = 0; n < 2; ++n) _Pragma("unroll") for (int k = 0; k < 2; ++k) dst[n][k] = *(const PG8_LAS bf16x8*)(lds + PG8_SB(b, h) + boff + n * 2048 + k * 1024); } while (0)
; #define PG8_WAIT_V(n) asm volatile("s_waitcnt vmcnt(" #n ")" ::: "memory")
; #define PG8_WAIT_V8_UNLESS_FIRST(t) asm volatile("s_cmp_eq_u32 %0, 0\n\ts_cbranch_scc1 .Lpg8skip%=\n\ts_waitcnt vmcnt(8)\n.Lpg8skip%=:" :: "s"(t) : "scc", "memory")
; #define PG8_WAIT_L(n) asm volatile("s_waitcnt lgkmcnt(" #n ")" ::: "memory")
; #define PG8_BAR __builtin_amdgcn_s_barrier()
; #define PG8_SCHED __builtin_amdgcn_sched_barrier(0)
; template <class Epi, class Sched, bool ALIGN_EPI = false, bool SP2 = false, bool FP8 = false, bool ABLK = false>
; __device__ __forceinline__ void gemm_phase(PG8_LAS unsigned char* lds, const Gemm g, const Sched& S, const Epi& E) {
;     ...
;             PG8_WAIT_V8_UNLESS_FIRST(t); PG8_WAIT_L(0); PG8_BAR; PG8_MMA(0, 0, At, B0); PG8_MMA(0, 1, At, B1); PG8_BAR; PG8_SCHED;
;             PG8_LDA(At, 0, 1); PG8_STAGE(PG8_SB(0, 0), b2, voffB); PG8_STAGE(PG8_SB(0, 1), b2 + hstep, voffB); PG8_STAGE(PG8_SA(0, 0), a2, voffA);
;             PG8_WAIT_V8_UNLESS_FIRST(t); PG8_WAIT_L(0); PG8_BAR; PG8_MMA(1, 0, At, B0); PG8_MMA(1, 1, At, B1); PG8_BAR; PG8_SCHED;
;             PG8_LDB(B0, 1, 0); PG8_LDB(B1, 1, 1); PG8_SCHED; PG8_LDA(At, 1, 0); PG8_STAGE(PG8_SA(0, 1), a2 + hstepA, voffA);
;             PG8_WAIT_V(8); PG8_WAIT_L(0); PG8_BAR; PG8_MMA(0, 0, At, B0); PG8_MMA(0, 1, At, B1); PG8_BAR; PG8_SCHED;
.Lpg8skip18:
	s_waitcnt lgkmcnt(0)
	s_barrier
	s_waitcnt lgkmcnt(0)
	v_mfma_scale_f32_16x16x128_f8f6f4 v[160:163], v[28:35], v[186:193], v[160:163], v245, v245 op_sel_hi:[0,0,0]
	v_mfma_scale_f32_16x16x128_f8f6f4 v[156:159], v[20:27], v[186:193], v[156:159], v245, v245 op_sel_hi:[0,0,0]
	v_mfma_scale_f32_16x16x128_f8f6f4 v[144:147], v[28:35], v[208:215], v[144:147], v245, v245 op_sel_hi:[0,0,0]
	v_mfma_scale_f32_16x16x128_f8f6f4 v[140:143], v[20:27], v[208:215], v[140:143], v245, v245 op_sel_hi:[0,0,0]
	v_mfma_scale_f32_16x16x128_f8f6f4 v[128:131], v[28:35], v[216:223], v[128:131], v245, v245 op_sel_hi:[0,0,0]
	v_mfma_scale_f32_16x16x128_f8f6f4 v[124:127], v[20:27], v[216:223], v[124:127], v245, v245 op_sel_hi:[0,0,0]
	v_mfma_scale_f32_16x16x128_f8f6f4 v[112:115], v[28:35], v[228:235], v[112:115], v245, v245 op_sel_hi:[0,0,0]
	v_mfma_scale_f32_16x16x128_f8f6f4 v[108:111], v[20:27], v[228:235], v[108:111], v245, v245 op_sel_hi:[0,0,0]
	v_mfma_scale_f32_16x16x128_f8f6f4 v[152:155], v[12:19], v[186:193], v[152:155], v245, v245 op_sel_hi:[0,0,0]
	v_mfma_scale_f32_16x16x128_f8f6f4 v[148:151], v[4:11], v[186:193], v[148:151], v245, v245 op_sel_hi:[0,0,0]
	v_mfma_scale_f32_16x16x128_f8f6f4 v[136:139], v[12:19], v[208:215], v[136:139], v245, v245 op_sel_hi:[0,0,0]
	v_mfma_scale_f32_16x16x128_f8f6f4 v[132:135], v[4:11], v[208:215], v[132:135], v245, v245 op_sel_hi:[0,0,0]
	v_mfma_scale_f32_16x16x128_f8f6f4 v[120:123], v[12:19], v[216:223], v[120:123], v245, v245 op_sel_hi:[0,0,0]
	v_mfma_scale_f32_16x16x128_f8f6f4 v[116:119], v[4:11], v[216:223], v[116:119], v245, v245 op_sel_hi:[0,0,0]
	v_mfma_scale_f32_16x16x128_f8f6f4 v[104:107], v[12:19], v[228:235], v[104:107], v245, v245 op_sel_hi:[0,0,0]
	v_mfma_scale_f32_16x16x128_f8f6f4 v[100:103], v[4:11], v[228:235], v[100:103], v245, v245 op_sel_hi:[0,0,0]
	s_barrier
	s_add_i32 s72, s72, s17
	v_lshl_add_u64 v[178:179], s[58:59], 0, v[2:3]
	s_mov_b32 m0, s72
	ds_read_b128 v[186:189], v184 offset:16384
	ds_read_b128 v[190:193], v184 offset:17408
	ds_read_b128 v[208:211], v184 offset:18432
	ds_read_b128 v[212:215], v184 offset:19456
	ds_read_b128 v[216:219], v184 offset:20480
	ds_read_b128 v[220:223], v184 offset:21504
	ds_read_b128 v[228:231], v184 offset:22528
	ds_read_b128 v[232:235], v184 offset:23552
	global_load_lds_dwordx4 v[178:179], off
	s_add_i32 m0, s72, 0x2000
	s_add_u32 s72, s58, 0x58000
	v_lshl_add_u64 v[180:181], s[58:59], 0, v[164:165]
	s_addc_u32 s73, s59, 0
	s_add_i32 s71, s71, s17
	global_load_lds_dwordx4 v[180:181], off
	v_lshl_add_u64 v[194:195], s[72:73], 0, v[2:3]
	s_mov_b32 m0, s71
	v_lshl_add_u64 v[204:205], s[60:61], 0, v[166:167]
	global_load_lds_dwordx4 v[194:195], off
	v_lshl_add_u64 v[194:195], s[72:73], 0, v[164:165]
	s_add_i32 m0, s71, 0x2000
	s_nop 0
	global_load_lds_dwordx4 v[194:195], off
	v_lshl_add_u64 v[194:195], s[60:61], 0, v[168:169]
	s_mov_b32 m0, s18
	s_nop 0
	global_load_lds_dwordx4 v[194:195], off
	s_mov_b32 m0, s19
	s_nop 0
	global_load_lds_dwordx4 v[204:205], off
	s_cmp_eq_u32 s70, 0
	s_cbranch_scc1 .Lpg8skip19
	s_waitcnt vmcnt(8)
.Lpg8skip19:
	s_waitcnt lgkmcnt(0)
	s_barrier
	s_waitcnt lgkmcnt(0)
	v_mfma_scale_f32_16x16x128_f8f6f4 v[96:99], v[28:35], v[186:193], v[96:99], v245, v245 op_sel_hi:[0,0,0]
	v_mfma_scale_f32_16x16x128_f8f6f4 v[92:95], v[20:27], v[186:193], v[92:95], v245, v245 op_sel_hi:[0,0,0]
	v_mfma_scale_f32_16x16x128_f8f6f4 v[80:83], v[28:35], v[208:215], v[80:83], v245, v245 op_sel_hi:[0,0,0]
	v_mfma_scale_f32_16x16x128_f8f6f4 v[76:79], v[20:27], v[208:215], v[76:79], v245, v245 op_sel_hi:[0,0,0]
	v_mfma_scale_f32_16x16x128_f8f6f4 v[64:67], v[28:35], v[216:223], v[64:67], v245, v245 op_sel_hi:[0,0,0]
	v_mfma_scale_f32_16x16x128_f8f6f4 v[60:63], v[20:27], v[216:223], v[60:63], v245, v245 op_sel_hi:[0,0,0]
	v_mfma_scale_f32_16x16x128_f8f6f4 v[48:51], v[28:35], v[228:235], v[48:51], v245, v245 op_sel_hi:[0,0,0]
	v_mfma_scale_f32_16x16x128_f8f6f4 v[44:47], v[20:27], v[228:235], v[44:47], v245, v245 op_sel_hi:[0,0,0]
	v_mfma_scale_f32_16x16x128_f8f6f4 v[88:91], v[12:19], v[186:193], v[88:91], v245, v245 op_sel_hi:[0,0,0]
	v_mfma_scale_f32_16x16x128_f8f6f4 v[84:87], v[4:11], v[186:193], v[84:87], v245, v245 op_sel_hi:[0,0,0]
	v_mfma_scale_f32_16x16x128_f8f6f4 v[72:75], v[12:19], v[208:215], v[72:75], v245, v245 op_sel_hi:[0,0,0]
	v_mfma_scale_f32_16x16x128_f8f6f4 v[68:71], v[4:11], v[208:215], v[68:71], v245, v245 op_sel_hi:[0,0,0]
	v_mfma_scale_f32_16x16x128_f8f6f4 v[56:59], v[12:19], v[216:223], v[56:59], v245, v245 op_sel_hi:[0,0,0]
	v_mfma_scale_f32_16x16x128_f8f6f4 v[52:55], v[4:11], v[216:223], v[52:55], v245, v245 op_sel_hi:[0,0,0]
	v_mfma_scale_f32_16x16x128_f8f6f4 v[40:43], v[12:19], v[228:235], v[40:43], v245, v245 op_sel_hi:[0,0,0]
	v_mfma_scale_f32_16x16x128_f8f6f4 v[36:39], v[4:11], v[228:235], v[36:39], v245, v245 op_sel_hi:[0,0,0]
	s_barrier
	s_add_i32 s60, 0, 0x18000
	s_add_i32 s61, 0, 0x1c000
	v_add_u32_e32 v16, s60, v183
	v_add_u32_e32 v32, s61, v183
	ds_read_b128 v[4:7], v16
	ds_read_b128 v[8:11], v16 offset:1024
	ds_read_b128 v[12:15], v16 offset:2048
	ds_read_b128 v[16:19], v16 offset:3072
	ds_read_b128 v[20:23], v32
	ds_read_b128 v[24:27], v32 offset:1024
	ds_read_b128 v[28:31], v32 offset:2048
	ds_read_b128 v[32:35], v32 offset:3072
	s_mov_b32 m0, s20
	v_lshl_add_u64 v[194:195], v[194:195], 0, s[24:25]
	ds_read_b128 v[186:189], v184 offset:32768
	ds_read_b128 v[190:193], v184 offset:33792
	ds_read_b128 v[208:211], v184 offset:34816
	ds_read_b128 v[212:215], v184 offset:35840
	ds_read_b128 v[216:219], v184 offset:36864
	ds_read_b128 v[220:223], v184 offset:37888
	ds_read_b128 v[228:231], v184 offset:38912
	ds_read_b128 v[232:235], v184 offset:39936
	global_load_lds_dwordx4 v[194:195], off
	v_lshl_add_u64 v[194:195], v[204:205], 0, s[24:25]
	s_mov_b32 m0, s21
	s_nop 0
	global_load_lds_dwordx4 v[194:195], off
	s_waitcnt vmcnt(8)
	s_waitcnt lgkmcnt(0)
	s_barrier
; #define PG8_STAGE(bufoff, gbase, voff) do { _Pragma("unroll") for (int _i = 0; _i < 2; ++_i) \
;         __builtin_amdgcn_global_load_lds((const unsigned*)((const char*)(gbase) + (voff)[_i]), (PG8_LAS unsigned*)(lds + (bufoff) + ldsw + _i * 8192), 16, 0, 0); } while (0)
; #define PG8_LDA(dst, b, h) do { _Pragma("unroll") for (int m = 0; m < 4; ++m) _Pragma("unroll") for (int k = 0; k < 2; ++k) dst[m][k] = *(const PG8_LAS bf16x8*)(lds + PG8_SA(b, h) + aoff + m * 2048 + k * 1024); } while (0)
; #define PG8_WAIT_V(n) asm volatile("s_waitcnt vmcnt(" #n ")" ::: "memory")
; #define PG8_WAIT_L(n) asm volatile("s_waitcnt lgkmcnt(" #n ")" ::: "memory")
; #define PG8_BAR __builtin_amdgcn_s_barrier()
; #define PG8_SCHED __builtin_amdgcn_sched_barrier(0)
; template <class Epi, class Sched, bool ALIGN_EPI = false, bool SP2 = false, bool FP8 = false, bool ABLK = false>
; __device__ __forceinline__ void gemm_phase(PG8_LAS unsigned char* lds, const Gemm g, const Sched& S, const Epi& E) {
;     ...
;             PG8_WAIT_V(8); PG8_WAIT_L(0); PG8_BAR; PG8_MMA(0, 0, At, B0); PG8_MMA(0, 1, At, B1); PG8_BAR; PG8_SCHED;
;             PG8_LDA(At, 1, 1); PG8_STAGE(PG8_SB(1, 0), b3, voffB); PG8_STAGE(PG8_SB(1, 1), b3 + hstep, voffB); PG8_STAGE(PG8_SA(1, 0), a3, voffA);
;             PG8_WAIT_V(8); PG8_WAIT_L(0); PG8_BAR; PG8_MMA(1, 0, At, B0); PG8_MMA(1, 1, At, B1); PG8_BAR; PG8_SCHED;
;     ...
;         if constexpr (SP2) PG8_WAIT_V(0);
;         if constexpr (FP8) asm volatile("s_nop 15\n\ts_nop 15" ::: "memory");
;         if constexpr (ALIGN_EPI) { if (wr == 0) PG8_BAR; }
	s_waitcnt lgkmcnt(0)
	v_mfma_scale_f32_16x16x128_f8f6f4 v[160:163], v[4:11], v[186:193], v[160:163], v245, v245 op_sel_hi:[0,0,0]
	v_mfma_scale_f32_16x16x128_f8f6f4 v[156:159], v[12:19], v[186:193], v[156:159], v245, v245 op_sel_hi:[0,0,0]
	v_mfma_scale_f32_16x16x128_f8f6f4 v[144:147], v[4:11], v[208:215], v[144:147], v245, v245 op_sel_hi:[0,0,0]
	v_mfma_scale_f32_16x16x128_f8f6f4 v[140:143], v[12:19], v[208:215], v[140:143], v245, v245 op_sel_hi:[0,0,0]
	v_mfma_scale_f32_16x16x128_f8f6f4 v[128:131], v[4:11], v[216:223], v[128:131], v245, v245 op_sel_hi:[0,0,0]
	v_mfma_scale_f32_16x16x128_f8f6f4 v[124:127], v[12:19], v[216:223], v[124:127], v245, v245 op_sel_hi:[0,0,0]
	v_mfma_scale_f32_16x16x128_f8f6f4 v[112:115], v[4:11], v[228:235], v[112:115], v245, v245 op_sel_hi:[0,0,0]
	v_mfma_scale_f32_16x16x128_f8f6f4 v[108:111], v[12:19], v[228:235], v[108:111], v245, v245 op_sel_hi:[0,0,0]
	v_mfma_scale_f32_16x16x128_f8f6f4 v[152:155], v[20:27], v[186:193], v[152:155], v245, v245 op_sel_hi:[0,0,0]
	v_mfma_scale_f32_16x16x128_f8f6f4 v[148:151], v[28:35], v[186:193], v[148:151], v245, v245 op_sel_hi:[0,0,0]
	v_mfma_scale_f32_16x16x128_f8f6f4 v[136:139], v[20:27], v[208:215], v[136:139], v245, v245 op_sel_hi:[0,0,0]
	v_mfma_scale_f32_16x16x128_f8f6f4 v[132:135], v[28:35], v[208:215], v[132:135], v245, v245 op_sel_hi:[0,0,0]
	v_mfma_scale_f32_16x16x128_f8f6f4 v[120:123], v[20:27], v[216:223], v[120:123], v245, v245 op_sel_hi:[0,0,0]
	v_mfma_scale_f32_16x16x128_f8f6f4 v[116:119], v[28:35], v[216:223], v[116:119], v245, v245 op_sel_hi:[0,0,0]
	v_mfma_scale_f32_16x16x128_f8f6f4 v[104:107], v[20:27], v[228:235], v[104:107], v245, v245 op_sel_hi:[0,0,0]
	v_mfma_scale_f32_16x16x128_f8f6f4 v[100:103], v[28:35], v[228:235], v[100:103], v245, v245 op_sel_hi:[0,0,0]
	s_barrier
	s_add_i32 s60, s60, s17
	v_lshl_add_u64 v[178:179], v[178:179], 0, s[34:35]
	s_mov_b32 m0, s60
	ds_read_b128 v[186:189], v184 offset:49152
	ds_read_b128 v[190:193], v184 offset:50176
	ds_read_b128 v[208:211], v184 offset:51200
	ds_read_b128 v[212:215], v184 offset:52224
	ds_read_b128 v[216:219], v184 offset:53248
	ds_read_b128 v[220:223], v184 offset:54272
	ds_read_b128 v[228:231], v184 offset:55296
	ds_read_b128 v[232:235], v184 offset:56320
	global_load_lds_dwordx4 v[178:179], off
	s_add_i32 m0, s60, 0x2000
	s_add_u32 s58, s58, 0x58080
	v_lshl_add_u64 v[178:179], v[180:181], 0, s[34:35]
	s_addc_u32 s59, s59, 0
	s_add_i32 s60, s61, s17
	global_load_lds_dwordx4 v[178:179], off
	v_lshl_add_u64 v[178:179], s[58:59], 0, v[2:3]
	s_mov_b32 m0, s60
	s_nop 0
	global_load_lds_dwordx4 v[178:179], off
	v_lshl_add_u64 v[178:179], s[58:59], 0, v[164:165]
	s_add_i32 m0, s60, 0x2000
	s_nop 0
	global_load_lds_dwordx4 v[178:179], off
	v_lshl_add_u64 v[178:179], s[56:57], 0, v[168:169]
	s_mov_b32 m0, s63
	s_nop 0
	global_load_lds_dwordx4 v[178:179], off
	v_lshl_add_u64 v[178:179], s[56:57], 0, v[166:167]
	s_mov_b32 m0, s64
	s_nop 0
	global_load_lds_dwordx4 v[178:179], off
	s_waitcnt vmcnt(8)
	s_waitcnt lgkmcnt(0)
	s_barrier
	s_waitcnt lgkmcnt(0)
	v_mfma_scale_f32_16x16x128_f8f6f4 v[96:99], v[4:11], v[186:193], v[96:99], v245, v245 op_sel_hi:[0,0,0]
	v_mfma_scale_f32_16x16x128_f8f6f4 v[92:95], v[12:19], v[186:193], v[92:95], v245, v245 op_sel_hi:[0,0,0]
	v_mfma_scale_f32_16x16x128_f8f6f4 v[80:83], v[4:11], v[208:215], v[80:83], v245, v245 op_sel_hi:[0,0,0]
	v_mfma_scale_f32_16x16x128_f8f6f4 v[76:79], v[12:19], v[208:215], v[76:79], v245, v245 op_sel_hi:[0,0,0]
	v_mfma_scale_f32_16x16x128_f8f6f4 v[64:67], v[4:11], v[216:223], v[64:67], v245, v245 op_sel_hi:[0,0,0]
	v_mfma_scale_f32_16x16x128_f8f6f4 v[60:63], v[12:19], v[216:223], v[60:63], v245, v245 op_sel_hi:[0,0,0]
	v_mfma_scale_f32_16x16x128_f8f6f4 v[48:51], v[4:11], v[228:235], v[48:51], v245, v245 op_sel_hi:[0,0,0]
	v_mfma_scale_f32_16x16x128_f8f6f4 v[44:47], v[12:19], v[228:235], v[44:47], v245, v245 op_sel_hi:[0,0,0]
	v_mfma_scale_f32_16x16x128_f8f6f4 v[88:91], v[20:27], v[186:193], v[88:91], v245, v245 op_sel_hi:[0,0,0]
	v_mfma_scale_f32_16x16x128_f8f6f4 v[84:87], v[28:35], v[186:193], v[84:87], v245, v245 op_sel_hi:[0,0,0]
	v_mfma_scale_f32_16x16x128_f8f6f4 v[72:75], v[20:27], v[208:215], v[72:75], v245, v245 op_sel_hi:[0,0,0]
	v_mfma_scale_f32_16x16x128_f8f6f4 v[68:71], v[28:35], v[208:215], v[68:71], v245, v245 op_sel_hi:[0,0,0]
	v_mfma_scale_f32_16x16x128_f8f6f4 v[56:59], v[20:27], v[216:223], v[56:59], v245, v245 op_sel_hi:[0,0,0]
	v_mfma_scale_f32_16x16x128_f8f6f4 v[52:55], v[28:35], v[216:223], v[52:55], v245, v245 op_sel_hi:[0,0,0]
	v_mfma_scale_f32_16x16x128_f8f6f4 v[40:43], v[20:27], v[228:235], v[40:43], v245, v245 op_sel_hi:[0,0,0]
	v_mfma_scale_f32_16x16x128_f8f6f4 v[36:39], v[28:35], v[228:235], v[36:39], v245, v245 op_sel_hi:[0,0,0]
	s_barrier
	s_add_u32 s4, s4, 0x100
	s_addc_u32 s5, s5, 0
	s_add_u32 s54, s54, 0x10000
	s_addc_u32 s55, s55, 0
	s_cmp_gt_u32 s70, 19
	s_cbranch_scc0 .LBB0_1831
	s_waitcnt vmcnt(0)
	s_nop 15
	s_nop 15
	s_and_b64 vcc, exec, s[48:49]
	s_cbranch_vccz .LBB0_1834
	s_barrier
